# v41 + epilogues v3: row factors fetched and prepared up front (packed), saddr stores with running 32-bit offsets, no per-block waits/nops
# baseline (speedup 1.0000x reference)
;     __device__ __forceinline__ void operator()(const f32x4 (&acc)[2][2][4][2], const Unit& u, int wr, int wc, int fr, int fq) const {
;     ...
;                 unsigned char* gb8 = wsb + (pn < 14 ? WS_GA : WS_GB) + ((pn - 10) & 3) * 256 + cl;
; #pragma unroll
;                 for (int ai = 0; ai < 2; ++ai)
; #pragma unroll
;                     for (int m = 0; m < 4; ++m) { unsigned char* rowp = gb8 + (size_t)(row0 + ai * HALF + m * 16) * 1024; const float nrf = -1.4426950408889634f * rsr[ai * HALF + m * 16];
; #pragma unroll
;                         for (int bj = 0; bj < 2; ++bj) { u32x2 w; w.x = 0u; w.y = 0u;
; #pragma unroll
;                             for (int e = 0; e < 4; ++e) { const float x0 = acc[ai][bj][m][0][e], x1 = acc[ai][bj][m][1][e];
;                                 const float r0 = 255.0f * __builtin_amdgcn_rcpf(1.0f + __builtin_amdgcn_exp2f(nrf * x0)), r1 = 255.0f * __builtin_amdgcn_rcpf(1.0f + __builtin_amdgcn_exp2f(nrf * x1));
;                                 w.x |= (unsigned)(r0 + 0.5f) << (8 * e); w.y |= (unsigned)(r1 + 0.5f) << (8 * e); }
;                             *(u32x2*)(rowp + bj * HALF) = w; }
;                         asm volatile("" ::: "memory"); }
.LBB0_398:
	s_and_b32 s0, s70, -4
	v_lshl_add_u32 v132, s18, 8, v202
	s_cmp_lg_u32 s0, 4
	s_mov_b64 s[0:1], -1
	s_cbranch_scc0 .LBB0_538
	s_cmp_gt_i32 s70, 9
	s_cbranch_scc0 .LBB0_401
	ds_read_b32 v182, v205
	ds_read_b32 v183, v205 offset:64
	ds_read_b32 v184, v205 offset:128
	ds_read_b32 v185, v205 offset:192
	ds_read_b32 v186, v205 offset:512
	ds_read_b32 v187, v205 offset:576
	ds_read_b32 v188, v205 offset:640
	ds_read_b32 v189, v205 offset:704
	s_cmp_lt_u32 s70, 14
	s_brev_b32 s0, 8
	s_cselect_b32 s0, s0, 0x11000000
	s_add_u32 s0, s16, s0
	s_addc_u32 s1, s17, 0
	s_lshl_b32 s8, s70, 8
	s_and_b32 s8, s8, 0x300
	s_xor_b32 s8, s8, 0x200
	s_add_u32 s0, s0, s8
	s_addc_u32 s1, s1, 0
	v_lshl_add_u32 v134, v132, 10, v172
	s_mov_b32 s8, 0xbfb8aa3b
	s_waitcnt lgkmcnt(0)
	v_pk_mul_f32 v[182:183], v[182:183], s[8:9] op_sel_hi:[1,0]
	v_pk_mul_f32 v[184:185], v[184:185], s[8:9] op_sel_hi:[1,0]
	v_pk_mul_f32 v[186:187], v[186:187], s[8:9] op_sel_hi:[1,0]
	v_pk_mul_f32 v[188:189], v[188:189], s[8:9] op_sel_hi:[1,0]
	s_mov_b32 s8, 0x3b808081
	v_pk_mul_f32 v[140:141], v[128:129], v[182:183] op_sel:[0,0] op_sel_hi:[1,0]
	v_pk_mul_f32 v[142:143], v[130:131], v[182:183] op_sel:[0,0] op_sel_hi:[1,0]
	v_pk_mul_f32 v[144:145], v[124:125], v[182:183] op_sel:[0,0] op_sel_hi:[1,0]
	v_pk_mul_f32 v[146:147], v[126:127], v[182:183] op_sel:[0,0] op_sel_hi:[1,0]
	v_pk_mul_f32 v[148:149], v[120:121], v[182:183] op_sel:[0,0] op_sel_hi:[1,0]
	v_pk_mul_f32 v[150:151], v[122:123], v[182:183] op_sel:[0,0] op_sel_hi:[1,0]
	v_pk_mul_f32 v[152:153], v[116:117], v[182:183] op_sel:[0,0] op_sel_hi:[1,0]
	v_pk_mul_f32 v[154:155], v[118:119], v[182:183] op_sel:[0,0] op_sel_hi:[1,0]
	v_exp_f32_e32 v140, v140
	v_exp_f32_e32 v141, v141
	v_exp_f32_e32 v142, v142
	v_exp_f32_e32 v143, v143
	v_exp_f32_e32 v144, v144
	v_exp_f32_e32 v145, v145
	v_exp_f32_e32 v146, v146
	v_exp_f32_e32 v147, v147
	v_exp_f32_e32 v148, v148
	v_exp_f32_e32 v149, v149
	v_exp_f32_e32 v150, v150
	v_exp_f32_e32 v151, v151
	v_exp_f32_e32 v152, v152
	v_exp_f32_e32 v153, v153
	v_exp_f32_e32 v154, v154
	v_exp_f32_e32 v155, v155
	v_pk_fma_f32 v[140:141], v[140:141], s[8:9], s[8:9] op_sel_hi:[1,0,0]
	v_pk_fma_f32 v[142:143], v[142:143], s[8:9], s[8:9] op_sel_hi:[1,0,0]
	v_pk_fma_f32 v[144:145], v[144:145], s[8:9], s[8:9] op_sel_hi:[1,0,0]
	v_pk_fma_f32 v[146:147], v[146:147], s[8:9], s[8:9] op_sel_hi:[1,0,0]
	v_pk_fma_f32 v[148:149], v[148:149], s[8:9], s[8:9] op_sel_hi:[1,0,0]
	v_pk_fma_f32 v[150:151], v[150:151], s[8:9], s[8:9] op_sel_hi:[1,0,0]
	v_pk_fma_f32 v[152:153], v[152:153], s[8:9], s[8:9] op_sel_hi:[1,0,0]
	v_pk_fma_f32 v[154:155], v[154:155], s[8:9], s[8:9] op_sel_hi:[1,0,0]
	v_rcp_f32_e32 v140, v140
	v_rcp_f32_e32 v141, v141
	v_rcp_f32_e32 v142, v142
	v_rcp_f32_e32 v143, v143
	v_rcp_f32_e32 v144, v144
	v_rcp_f32_e32 v145, v145
	v_rcp_f32_e32 v146, v146
	v_rcp_f32_e32 v147, v147
	v_rcp_f32_e32 v148, v148
	v_rcp_f32_e32 v149, v149
	v_rcp_f32_e32 v150, v150
	v_rcp_f32_e32 v151, v151
	v_rcp_f32_e32 v152, v152
	v_rcp_f32_e32 v153, v153
	v_rcp_f32_e32 v154, v154
	v_rcp_f32_e32 v155, v155
	v_cvt_rpi_i32_f32_sdwa v156, v140 dst_sel:BYTE_0 dst_unused:UNUSED_PAD src0_sel:DWORD
	v_cvt_rpi_i32_f32_sdwa v157, v144 dst_sel:BYTE_0 dst_unused:UNUSED_PAD src0_sel:DWORD
	v_cvt_rpi_i32_f32_sdwa v158, v148 dst_sel:BYTE_0 dst_unused:UNUSED_PAD src0_sel:DWORD
	v_cvt_rpi_i32_f32_sdwa v159, v152 dst_sel:BYTE_0 dst_unused:UNUSED_PAD src0_sel:DWORD
	v_cvt_rpi_i32_f32_sdwa v156, v141 dst_sel:BYTE_1 dst_unused:UNUSED_PRESERVE src0_sel:DWORD
	v_cvt_rpi_i32_f32_sdwa v157, v145 dst_sel:BYTE_1 dst_unused:UNUSED_PRESERVE src0_sel:DWORD
	v_cvt_rpi_i32_f32_sdwa v158, v149 dst_sel:BYTE_1 dst_unused:UNUSED_PRESERVE src0_sel:DWORD
	v_cvt_rpi_i32_f32_sdwa v159, v153 dst_sel:BYTE_1 dst_unused:UNUSED_PRESERVE src0_sel:DWORD
	v_cvt_rpi_i32_f32_sdwa v156, v142 dst_sel:BYTE_2 dst_unused:UNUSED_PRESERVE src0_sel:DWORD
	v_cvt_rpi_i32_f32_sdwa v157, v146 dst_sel:BYTE_2 dst_unused:UNUSED_PRESERVE src0_sel:DWORD
	v_cvt_rpi_i32_f32_sdwa v158, v150 dst_sel:BYTE_2 dst_unused:UNUSED_PRESERVE src0_sel:DWORD
	v_cvt_rpi_i32_f32_sdwa v159, v154 dst_sel:BYTE_2 dst_unused:UNUSED_PRESERVE src0_sel:DWORD
	v_cvt_rpi_i32_f32_sdwa v156, v143 dst_sel:BYTE_3 dst_unused:UNUSED_PRESERVE src0_sel:DWORD
	v_cvt_rpi_i32_f32_sdwa v157, v147 dst_sel:BYTE_3 dst_unused:UNUSED_PRESERVE src0_sel:DWORD
	v_cvt_rpi_i32_f32_sdwa v158, v151 dst_sel:BYTE_3 dst_unused:UNUSED_PRESERVE src0_sel:DWORD
	v_cvt_rpi_i32_f32_sdwa v159, v155 dst_sel:BYTE_3 dst_unused:UNUSED_PRESERVE src0_sel:DWORD
	s_nop 0
	global_store_dwordx2 v134, v[156:157], s[0:1]
	global_store_dwordx2 v134, v[158:159], s[0:1] offset:128
	v_pk_mul_f32 v[140:141], v[112:113], v[182:183] op_sel:[0,1] op_sel_hi:[1,1]
	v_pk_mul_f32 v[142:143], v[114:115], v[182:183] op_sel:[0,1] op_sel_hi:[1,1]
	v_pk_mul_f32 v[144:145], v[108:109], v[182:183] op_sel:[0,1] op_sel_hi:[1,1]
	v_pk_mul_f32 v[146:147], v[110:111], v[182:183] op_sel:[0,1] op_sel_hi:[1,1]
	v_pk_mul_f32 v[148:149], v[104:105], v[182:183] op_sel:[0,1] op_sel_hi:[1,1]
	v_pk_mul_f32 v[150:151], v[106:107], v[182:183] op_sel:[0,1] op_sel_hi:[1,1]
	v_pk_mul_f32 v[152:153], v[100:101], v[182:183] op_sel:[0,1] op_sel_hi:[1,1]
	v_pk_mul_f32 v[154:155], v[102:103], v[182:183] op_sel:[0,1] op_sel_hi:[1,1]
	v_exp_f32_e32 v140, v140
	v_exp_f32_e32 v141, v141
	v_exp_f32_e32 v142, v142
	v_exp_f32_e32 v143, v143
	v_exp_f32_e32 v144, v144
	v_exp_f32_e32 v145, v145
	v_exp_f32_e32 v146, v146
	v_exp_f32_e32 v147, v147
	v_exp_f32_e32 v148, v148
	v_exp_f32_e32 v149, v149
	v_exp_f32_e32 v150, v150
	v_exp_f32_e32 v151, v151
	v_exp_f32_e32 v152, v152
	v_exp_f32_e32 v153, v153
	v_exp_f32_e32 v154, v154
;     __device__ __forceinline__ void operator()(const f32x4 (&acc)[2][2][4][2], const Unit& u, int wr, int wc, int fr, int fq) const {
;     ...
;                 unsigned char* gb8 = wsb + (pn < 14 ? WS_GA : WS_GB) + ((pn - 10) & 3) * 256 + cl;
; #pragma unroll
;                 for (int ai = 0; ai < 2; ++ai)
; #pragma unroll
;                     for (int m = 0; m < 4; ++m) { unsigned char* rowp = gb8 + (size_t)(row0 + ai * HALF + m * 16) * 1024; const float nrf = -1.4426950408889634f * rsr[ai * HALF + m * 16];
; #pragma unroll
;                         for (int bj = 0; bj < 2; ++bj) { u32x2 w; w.x = 0u; w.y = 0u;
; #pragma unroll
;                             for (int e = 0; e < 4; ++e) { const float x0 = acc[ai][bj][m][0][e], x1 = acc[ai][bj][m][1][e];
;                                 const float r0 = 255.0f * __builtin_amdgcn_rcpf(1.0f + __builtin_amdgcn_exp2f(nrf * x0)), r1 = 255.0f * __builtin_amdgcn_rcpf(1.0f + __builtin_amdgcn_exp2f(nrf * x1));
;                                 w.x |= (unsigned)(r0 + 0.5f) << (8 * e); w.y |= (unsigned)(r1 + 0.5f) << (8 * e); }
;                             *(u32x2*)(rowp + bj * HALF) = w; }
;                         asm volatile("" ::: "memory"); }
	v_exp_f32_e32 v155, v155
	v_pk_fma_f32 v[140:141], v[140:141], s[8:9], s[8:9] op_sel_hi:[1,0,0]
	v_pk_fma_f32 v[142:143], v[142:143], s[8:9], s[8:9] op_sel_hi:[1,0,0]
	v_pk_fma_f32 v[144:145], v[144:145], s[8:9], s[8:9] op_sel_hi:[1,0,0]
	v_pk_fma_f32 v[146:147], v[146:147], s[8:9], s[8:9] op_sel_hi:[1,0,0]
	v_pk_fma_f32 v[148:149], v[148:149], s[8:9], s[8:9] op_sel_hi:[1,0,0]
	v_pk_fma_f32 v[150:151], v[150:151], s[8:9], s[8:9] op_sel_hi:[1,0,0]
	v_pk_fma_f32 v[152:153], v[152:153], s[8:9], s[8:9] op_sel_hi:[1,0,0]
	v_pk_fma_f32 v[154:155], v[154:155], s[8:9], s[8:9] op_sel_hi:[1,0,0]
	v_rcp_f32_e32 v140, v140
	v_rcp_f32_e32 v141, v141
	v_rcp_f32_e32 v142, v142
	v_rcp_f32_e32 v143, v143
	v_rcp_f32_e32 v144, v144
	v_rcp_f32_e32 v145, v145
	v_rcp_f32_e32 v146, v146
	v_rcp_f32_e32 v147, v147
	v_rcp_f32_e32 v148, v148
	v_rcp_f32_e32 v149, v149
	v_rcp_f32_e32 v150, v150
	v_rcp_f32_e32 v151, v151
	v_rcp_f32_e32 v152, v152
	v_rcp_f32_e32 v153, v153
	v_rcp_f32_e32 v154, v154
	v_rcp_f32_e32 v155, v155
	v_cvt_rpi_i32_f32_sdwa v190, v140 dst_sel:BYTE_0 dst_unused:UNUSED_PAD src0_sel:DWORD
	v_cvt_rpi_i32_f32_sdwa v191, v144 dst_sel:BYTE_0 dst_unused:UNUSED_PAD src0_sel:DWORD
	v_cvt_rpi_i32_f32_sdwa v192, v148 dst_sel:BYTE_0 dst_unused:UNUSED_PAD src0_sel:DWORD
	v_cvt_rpi_i32_f32_sdwa v193, v152 dst_sel:BYTE_0 dst_unused:UNUSED_PAD src0_sel:DWORD
	v_cvt_rpi_i32_f32_sdwa v190, v141 dst_sel:BYTE_1 dst_unused:UNUSED_PRESERVE src0_sel:DWORD
	v_cvt_rpi_i32_f32_sdwa v191, v145 dst_sel:BYTE_1 dst_unused:UNUSED_PRESERVE src0_sel:DWORD
	v_cvt_rpi_i32_f32_sdwa v192, v149 dst_sel:BYTE_1 dst_unused:UNUSED_PRESERVE src0_sel:DWORD
	v_cvt_rpi_i32_f32_sdwa v193, v153 dst_sel:BYTE_1 dst_unused:UNUSED_PRESERVE src0_sel:DWORD
	v_cvt_rpi_i32_f32_sdwa v190, v142 dst_sel:BYTE_2 dst_unused:UNUSED_PRESERVE src0_sel:DWORD
	v_cvt_rpi_i32_f32_sdwa v191, v146 dst_sel:BYTE_2 dst_unused:UNUSED_PRESERVE src0_sel:DWORD
	v_cvt_rpi_i32_f32_sdwa v192, v150 dst_sel:BYTE_2 dst_unused:UNUSED_PRESERVE src0_sel:DWORD
	v_cvt_rpi_i32_f32_sdwa v193, v154 dst_sel:BYTE_2 dst_unused:UNUSED_PRESERVE src0_sel:DWORD
	v_cvt_rpi_i32_f32_sdwa v190, v143 dst_sel:BYTE_3 dst_unused:UNUSED_PRESERVE src0_sel:DWORD
	v_cvt_rpi_i32_f32_sdwa v191, v147 dst_sel:BYTE_3 dst_unused:UNUSED_PRESERVE src0_sel:DWORD
	v_cvt_rpi_i32_f32_sdwa v192, v151 dst_sel:BYTE_3 dst_unused:UNUSED_PRESERVE src0_sel:DWORD
	v_cvt_rpi_i32_f32_sdwa v193, v155 dst_sel:BYTE_3 dst_unused:UNUSED_PRESERVE src0_sel:DWORD
	v_add_u32_e32 v134, 0x4000, v134
	global_store_dwordx2 v134, v[190:191], s[0:1]
	global_store_dwordx2 v134, v[192:193], s[0:1] offset:128
	v_pk_mul_f32 v[140:141], v[96:97], v[184:185] op_sel:[0,0] op_sel_hi:[1,0]
	v_pk_mul_f32 v[142:143], v[98:99], v[184:185] op_sel:[0,0] op_sel_hi:[1,0]
	v_pk_mul_f32 v[144:145], v[92:93], v[184:185] op_sel:[0,0] op_sel_hi:[1,0]
	v_pk_mul_f32 v[146:147], v[94:95], v[184:185] op_sel:[0,0] op_sel_hi:[1,0]
	v_pk_mul_f32 v[148:149], v[88:89], v[184:185] op_sel:[0,0] op_sel_hi:[1,0]
	v_pk_mul_f32 v[150:151], v[90:91], v[184:185] op_sel:[0,0] op_sel_hi:[1,0]
	v_pk_mul_f32 v[152:153], v[84:85], v[184:185] op_sel:[0,0] op_sel_hi:[1,0]
	v_pk_mul_f32 v[154:155], v[86:87], v[184:185] op_sel:[0,0] op_sel_hi:[1,0]
	v_exp_f32_e32 v140, v140
	v_exp_f32_e32 v141, v141
	v_exp_f32_e32 v142, v142
	v_exp_f32_e32 v143, v143
	v_exp_f32_e32 v144, v144
	v_exp_f32_e32 v145, v145
	v_exp_f32_e32 v146, v146
	v_exp_f32_e32 v147, v147
	v_exp_f32_e32 v148, v148
	v_exp_f32_e32 v149, v149
	v_exp_f32_e32 v150, v150
	v_exp_f32_e32 v151, v151
	v_exp_f32_e32 v152, v152
	v_exp_f32_e32 v153, v153
	v_exp_f32_e32 v154, v154
	v_exp_f32_e32 v155, v155
	v_pk_fma_f32 v[140:141], v[140:141], s[8:9], s[8:9] op_sel_hi:[1,0,0]
	v_pk_fma_f32 v[142:143], v[142:143], s[8:9], s[8:9] op_sel_hi:[1,0,0]
	v_pk_fma_f32 v[144:145], v[144:145], s[8:9], s[8:9] op_sel_hi:[1,0,0]
	v_pk_fma_f32 v[146:147], v[146:147], s[8:9], s[8:9] op_sel_hi:[1,0,0]
	v_pk_fma_f32 v[148:149], v[148:149], s[8:9], s[8:9] op_sel_hi:[1,0,0]
	v_pk_fma_f32 v[150:151], v[150:151], s[8:9], s[8:9] op_sel_hi:[1,0,0]
	v_pk_fma_f32 v[152:153], v[152:153], s[8:9], s[8:9] op_sel_hi:[1,0,0]
	v_pk_fma_f32 v[154:155], v[154:155], s[8:9], s[8:9] op_sel_hi:[1,0,0]
	v_rcp_f32_e32 v140, v140
	v_rcp_f32_e32 v141, v141
	v_rcp_f32_e32 v142, v142
	v_rcp_f32_e32 v143, v143
	v_rcp_f32_e32 v144, v144
	v_rcp_f32_e32 v145, v145
	v_rcp_f32_e32 v146, v146
	v_rcp_f32_e32 v147, v147
	v_rcp_f32_e32 v148, v148
	v_rcp_f32_e32 v149, v149
	v_rcp_f32_e32 v150, v150
	v_rcp_f32_e32 v151, v151
	v_rcp_f32_e32 v152, v152
	v_rcp_f32_e32 v153, v153
	v_rcp_f32_e32 v154, v154
	v_rcp_f32_e32 v155, v155
	v_cvt_rpi_i32_f32_sdwa v156, v140 dst_sel:BYTE_0 dst_unused:UNUSED_PAD src0_sel:DWORD
	v_cvt_rpi_i32_f32_sdwa v157, v144 dst_sel:BYTE_0 dst_unused:UNUSED_PAD src0_sel:DWORD
	v_cvt_rpi_i32_f32_sdwa v158, v148 dst_sel:BYTE_0 dst_unused:UNUSED_PAD src0_sel:DWORD
	v_cvt_rpi_i32_f32_sdwa v159, v152 dst_sel:BYTE_0 dst_unused:UNUSED_PAD src0_sel:DWORD
	v_cvt_rpi_i32_f32_sdwa v156, v141 dst_sel:BYTE_1 dst_unused:UNUSED_PRESERVE src0_sel:DWORD
	v_cvt_rpi_i32_f32_sdwa v157, v145 dst_sel:BYTE_1 dst_unused:UNUSED_PRESERVE src0_sel:DWORD
	v_cvt_rpi_i32_f32_sdwa v158, v149 dst_sel:BYTE_1 dst_unused:UNUSED_PRESERVE src0_sel:DWORD
	v_cvt_rpi_i32_f32_sdwa v159, v153 dst_sel:BYTE_1 dst_unused:UNUSED_PRESERVE src0_sel:DWORD
	v_cvt_rpi_i32_f32_sdwa v156, v142 dst_sel:BYTE_2 dst_unused:UNUSED_PRESERVE src0_sel:DWORD
	v_cvt_rpi_i32_f32_sdwa v157, v146 dst_sel:BYTE_2 dst_unused:UNUSED_PRESERVE src0_sel:DWORD
	v_cvt_rpi_i32_f32_sdwa v158, v150 dst_sel:BYTE_2 dst_unused:UNUSED_PRESERVE src0_sel:DWORD
;     __device__ __forceinline__ void operator()(const f32x4 (&acc)[2][2][4][2], const Unit& u, int wr, int wc, int fr, int fq) const {
;     ...
;                 unsigned char* gb8 = wsb + (pn < 14 ? WS_GA : WS_GB) + ((pn - 10) & 3) * 256 + cl;
; #pragma unroll
;                 for (int ai = 0; ai < 2; ++ai)
; #pragma unroll
;                     for (int m = 0; m < 4; ++m) { unsigned char* rowp = gb8 + (size_t)(row0 + ai * HALF + m * 16) * 1024; const float nrf = -1.4426950408889634f * rsr[ai * HALF + m * 16];
; #pragma unroll
;                         for (int bj = 0; bj < 2; ++bj) { u32x2 w; w.x = 0u; w.y = 0u;
; #pragma unroll
;                             for (int e = 0; e < 4; ++e) { const float x0 = acc[ai][bj][m][0][e], x1 = acc[ai][bj][m][1][e];
;                                 const float r0 = 255.0f * __builtin_amdgcn_rcpf(1.0f + __builtin_amdgcn_exp2f(nrf * x0)), r1 = 255.0f * __builtin_amdgcn_rcpf(1.0f + __builtin_amdgcn_exp2f(nrf * x1));
;                                 w.x |= (unsigned)(r0 + 0.5f) << (8 * e); w.y |= (unsigned)(r1 + 0.5f) << (8 * e); }
;                             *(u32x2*)(rowp + bj * HALF) = w; }
;                         asm volatile("" ::: "memory"); }
	v_cvt_rpi_i32_f32_sdwa v159, v154 dst_sel:BYTE_2 dst_unused:UNUSED_PRESERVE src0_sel:DWORD
	v_cvt_rpi_i32_f32_sdwa v156, v143 dst_sel:BYTE_3 dst_unused:UNUSED_PRESERVE src0_sel:DWORD
	v_cvt_rpi_i32_f32_sdwa v157, v147 dst_sel:BYTE_3 dst_unused:UNUSED_PRESERVE src0_sel:DWORD
	v_cvt_rpi_i32_f32_sdwa v158, v151 dst_sel:BYTE_3 dst_unused:UNUSED_PRESERVE src0_sel:DWORD
	v_cvt_rpi_i32_f32_sdwa v159, v155 dst_sel:BYTE_3 dst_unused:UNUSED_PRESERVE src0_sel:DWORD
	v_add_u32_e32 v134, 0x4000, v134
	global_store_dwordx2 v134, v[156:157], s[0:1]
	global_store_dwordx2 v134, v[158:159], s[0:1] offset:128
	v_pk_mul_f32 v[140:141], v[80:81], v[184:185] op_sel:[0,1] op_sel_hi:[1,1]
	v_pk_mul_f32 v[142:143], v[82:83], v[184:185] op_sel:[0,1] op_sel_hi:[1,1]
	v_pk_mul_f32 v[144:145], v[76:77], v[184:185] op_sel:[0,1] op_sel_hi:[1,1]
	v_pk_mul_f32 v[146:147], v[78:79], v[184:185] op_sel:[0,1] op_sel_hi:[1,1]
	v_pk_mul_f32 v[148:149], v[72:73], v[184:185] op_sel:[0,1] op_sel_hi:[1,1]
	v_pk_mul_f32 v[150:151], v[74:75], v[184:185] op_sel:[0,1] op_sel_hi:[1,1]
	v_pk_mul_f32 v[152:153], v[68:69], v[184:185] op_sel:[0,1] op_sel_hi:[1,1]
	v_pk_mul_f32 v[154:155], v[70:71], v[184:185] op_sel:[0,1] op_sel_hi:[1,1]
	v_exp_f32_e32 v140, v140
	v_exp_f32_e32 v141, v141
	v_exp_f32_e32 v142, v142
	v_exp_f32_e32 v143, v143
	v_exp_f32_e32 v144, v144
	v_exp_f32_e32 v145, v145
	v_exp_f32_e32 v146, v146
	v_exp_f32_e32 v147, v147
	v_exp_f32_e32 v148, v148
	v_exp_f32_e32 v149, v149
	v_exp_f32_e32 v150, v150
	v_exp_f32_e32 v151, v151
	v_exp_f32_e32 v152, v152
	v_exp_f32_e32 v153, v153
	v_exp_f32_e32 v154, v154
	v_exp_f32_e32 v155, v155
	v_pk_fma_f32 v[140:141], v[140:141], s[8:9], s[8:9] op_sel_hi:[1,0,0]
	v_pk_fma_f32 v[142:143], v[142:143], s[8:9], s[8:9] op_sel_hi:[1,0,0]
	v_pk_fma_f32 v[144:145], v[144:145], s[8:9], s[8:9] op_sel_hi:[1,0,0]
	v_pk_fma_f32 v[146:147], v[146:147], s[8:9], s[8:9] op_sel_hi:[1,0,0]
	v_pk_fma_f32 v[148:149], v[148:149], s[8:9], s[8:9] op_sel_hi:[1,0,0]
	v_pk_fma_f32 v[150:151], v[150:151], s[8:9], s[8:9] op_sel_hi:[1,0,0]
	v_pk_fma_f32 v[152:153], v[152:153], s[8:9], s[8:9] op_sel_hi:[1,0,0]
	v_pk_fma_f32 v[154:155], v[154:155], s[8:9], s[8:9] op_sel_hi:[1,0,0]
	v_rcp_f32_e32 v140, v140
	v_rcp_f32_e32 v141, v141
	v_rcp_f32_e32 v142, v142
	v_rcp_f32_e32 v143, v143
	v_rcp_f32_e32 v144, v144
	v_rcp_f32_e32 v145, v145
	v_rcp_f32_e32 v146, v146
	v_rcp_f32_e32 v147, v147
	v_rcp_f32_e32 v148, v148
	v_rcp_f32_e32 v149, v149
	v_rcp_f32_e32 v150, v150
	v_rcp_f32_e32 v151, v151
	v_rcp_f32_e32 v152, v152
	v_rcp_f32_e32 v153, v153
	v_rcp_f32_e32 v154, v154
	v_rcp_f32_e32 v155, v155
	v_cvt_rpi_i32_f32_sdwa v190, v140 dst_sel:BYTE_0 dst_unused:UNUSED_PAD src0_sel:DWORD
	v_cvt_rpi_i32_f32_sdwa v191, v144 dst_sel:BYTE_0 dst_unused:UNUSED_PAD src0_sel:DWORD
	v_cvt_rpi_i32_f32_sdwa v192, v148 dst_sel:BYTE_0 dst_unused:UNUSED_PAD src0_sel:DWORD
	v_cvt_rpi_i32_f32_sdwa v193, v152 dst_sel:BYTE_0 dst_unused:UNUSED_PAD src0_sel:DWORD
	v_cvt_rpi_i32_f32_sdwa v190, v141 dst_sel:BYTE_1 dst_unused:UNUSED_PRESERVE src0_sel:DWORD
	v_cvt_rpi_i32_f32_sdwa v191, v145 dst_sel:BYTE_1 dst_unused:UNUSED_PRESERVE src0_sel:DWORD
	v_cvt_rpi_i32_f32_sdwa v192, v149 dst_sel:BYTE_1 dst_unused:UNUSED_PRESERVE src0_sel:DWORD
	v_cvt_rpi_i32_f32_sdwa v193, v153 dst_sel:BYTE_1 dst_unused:UNUSED_PRESERVE src0_sel:DWORD
	v_cvt_rpi_i32_f32_sdwa v190, v142 dst_sel:BYTE_2 dst_unused:UNUSED_PRESERVE src0_sel:DWORD
	v_cvt_rpi_i32_f32_sdwa v191, v146 dst_sel:BYTE_2 dst_unused:UNUSED_PRESERVE src0_sel:DWORD
	v_cvt_rpi_i32_f32_sdwa v192, v150 dst_sel:BYTE_2 dst_unused:UNUSED_PRESERVE src0_sel:DWORD
	v_cvt_rpi_i32_f32_sdwa v193, v154 dst_sel:BYTE_2 dst_unused:UNUSED_PRESERVE src0_sel:DWORD
	v_cvt_rpi_i32_f32_sdwa v190, v143 dst_sel:BYTE_3 dst_unused:UNUSED_PRESERVE src0_sel:DWORD
	v_cvt_rpi_i32_f32_sdwa v191, v147 dst_sel:BYTE_3 dst_unused:UNUSED_PRESERVE src0_sel:DWORD
	v_cvt_rpi_i32_f32_sdwa v192, v151 dst_sel:BYTE_3 dst_unused:UNUSED_PRESERVE src0_sel:DWORD
	v_cvt_rpi_i32_f32_sdwa v193, v155 dst_sel:BYTE_3 dst_unused:UNUSED_PRESERVE src0_sel:DWORD
	v_add_u32_e32 v134, 0x4000, v134
	global_store_dwordx2 v134, v[190:191], s[0:1]
	global_store_dwordx2 v134, v[192:193], s[0:1] offset:128
	v_pk_mul_f32 v[140:141], v[64:65], v[186:187] op_sel:[0,0] op_sel_hi:[1,0]
	v_pk_mul_f32 v[142:143], v[66:67], v[186:187] op_sel:[0,0] op_sel_hi:[1,0]
	v_pk_mul_f32 v[144:145], v[60:61], v[186:187] op_sel:[0,0] op_sel_hi:[1,0]
	v_pk_mul_f32 v[146:147], v[62:63], v[186:187] op_sel:[0,0] op_sel_hi:[1,0]
	v_pk_mul_f32 v[148:149], v[56:57], v[186:187] op_sel:[0,0] op_sel_hi:[1,0]
	v_pk_mul_f32 v[150:151], v[58:59], v[186:187] op_sel:[0,0] op_sel_hi:[1,0]
	v_pk_mul_f32 v[152:153], v[52:53], v[186:187] op_sel:[0,0] op_sel_hi:[1,0]
	v_pk_mul_f32 v[154:155], v[54:55], v[186:187] op_sel:[0,0] op_sel_hi:[1,0]
	v_exp_f32_e32 v140, v140
	v_exp_f32_e32 v141, v141
	v_exp_f32_e32 v142, v142
	v_exp_f32_e32 v143, v143
	v_exp_f32_e32 v144, v144
	v_exp_f32_e32 v145, v145
	v_exp_f32_e32 v146, v146
	v_exp_f32_e32 v147, v147
	v_exp_f32_e32 v148, v148
	v_exp_f32_e32 v149, v149
	v_exp_f32_e32 v150, v150
	v_exp_f32_e32 v151, v151
	v_exp_f32_e32 v152, v152
	v_exp_f32_e32 v153, v153
	v_exp_f32_e32 v154, v154
	v_exp_f32_e32 v155, v155
	v_pk_fma_f32 v[140:141], v[140:141], s[8:9], s[8:9] op_sel_hi:[1,0,0]
	v_pk_fma_f32 v[142:143], v[142:143], s[8:9], s[8:9] op_sel_hi:[1,0,0]
	v_pk_fma_f32 v[144:145], v[144:145], s[8:9], s[8:9] op_sel_hi:[1,0,0]
	v_pk_fma_f32 v[146:147], v[146:147], s[8:9], s[8:9] op_sel_hi:[1,0,0]
	v_pk_fma_f32 v[148:149], v[148:149], s[8:9], s[8:9] op_sel_hi:[1,0,0]
	v_pk_fma_f32 v[150:151], v[150:151], s[8:9], s[8:9] op_sel_hi:[1,0,0]
;     __device__ __forceinline__ void operator()(const f32x4 (&acc)[2][2][4][2], const Unit& u, int wr, int wc, int fr, int fq) const {
;     ...
;                     for (int m = 0; m < 4; ++m) { unsigned char* rowp = gb8 + (size_t)(row0 + ai * HALF + m * 16) * 1024; const float nrf = -1.4426950408889634f * rsr[ai * HALF + m * 16];
; #pragma unroll
;                         for (int bj = 0; bj < 2; ++bj) { u32x2 w; w.x = 0u; w.y = 0u;
; #pragma unroll
;                             for (int e = 0; e < 4; ++e) { const float x0 = acc[ai][bj][m][0][e], x1 = acc[ai][bj][m][1][e];
;                                 const float r0 = 255.0f * __builtin_amdgcn_rcpf(1.0f + __builtin_amdgcn_exp2f(nrf * x0)), r1 = 255.0f * __builtin_amdgcn_rcpf(1.0f + __builtin_amdgcn_exp2f(nrf * x1));
;                                 w.x |= (unsigned)(r0 + 0.5f) << (8 * e); w.y |= (unsigned)(r1 + 0.5f) << (8 * e); }
;                             *(u32x2*)(rowp + bj * HALF) = w; }
	v_pk_fma_f32 v[152:153], v[152:153], s[8:9], s[8:9] op_sel_hi:[1,0,0]
	v_pk_fma_f32 v[154:155], v[154:155], s[8:9], s[8:9] op_sel_hi:[1,0,0]
	v_rcp_f32_e32 v140, v140
	v_rcp_f32_e32 v141, v141
	v_rcp_f32_e32 v142, v142
	v_rcp_f32_e32 v143, v143
	v_rcp_f32_e32 v144, v144
	v_rcp_f32_e32 v145, v145
	v_rcp_f32_e32 v146, v146
	v_rcp_f32_e32 v147, v147
	v_rcp_f32_e32 v148, v148
	v_rcp_f32_e32 v149, v149
	v_rcp_f32_e32 v150, v150
	v_rcp_f32_e32 v151, v151
	v_rcp_f32_e32 v152, v152
	v_rcp_f32_e32 v153, v153
	v_rcp_f32_e32 v154, v154
	v_rcp_f32_e32 v155, v155
	v_cvt_rpi_i32_f32_sdwa v156, v140 dst_sel:BYTE_0 dst_unused:UNUSED_PAD src0_sel:DWORD
	v_cvt_rpi_i32_f32_sdwa v157, v144 dst_sel:BYTE_0 dst_unused:UNUSED_PAD src0_sel:DWORD
	v_cvt_rpi_i32_f32_sdwa v158, v148 dst_sel:BYTE_0 dst_unused:UNUSED_PAD src0_sel:DWORD
	v_cvt_rpi_i32_f32_sdwa v159, v152 dst_sel:BYTE_0 dst_unused:UNUSED_PAD src0_sel:DWORD
	v_cvt_rpi_i32_f32_sdwa v156, v141 dst_sel:BYTE_1 dst_unused:UNUSED_PRESERVE src0_sel:DWORD
	v_cvt_rpi_i32_f32_sdwa v157, v145 dst_sel:BYTE_1 dst_unused:UNUSED_PRESERVE src0_sel:DWORD
	v_cvt_rpi_i32_f32_sdwa v158, v149 dst_sel:BYTE_1 dst_unused:UNUSED_PRESERVE src0_sel:DWORD
	v_cvt_rpi_i32_f32_sdwa v159, v153 dst_sel:BYTE_1 dst_unused:UNUSED_PRESERVE src0_sel:DWORD
	v_cvt_rpi_i32_f32_sdwa v156, v142 dst_sel:BYTE_2 dst_unused:UNUSED_PRESERVE src0_sel:DWORD
	v_cvt_rpi_i32_f32_sdwa v157, v146 dst_sel:BYTE_2 dst_unused:UNUSED_PRESERVE src0_sel:DWORD
	v_cvt_rpi_i32_f32_sdwa v158, v150 dst_sel:BYTE_2 dst_unused:UNUSED_PRESERVE src0_sel:DWORD
	v_cvt_rpi_i32_f32_sdwa v159, v154 dst_sel:BYTE_2 dst_unused:UNUSED_PRESERVE src0_sel:DWORD
	v_cvt_rpi_i32_f32_sdwa v156, v143 dst_sel:BYTE_3 dst_unused:UNUSED_PRESERVE src0_sel:DWORD
	v_cvt_rpi_i32_f32_sdwa v157, v147 dst_sel:BYTE_3 dst_unused:UNUSED_PRESERVE src0_sel:DWORD
	v_cvt_rpi_i32_f32_sdwa v158, v151 dst_sel:BYTE_3 dst_unused:UNUSED_PRESERVE src0_sel:DWORD
	v_cvt_rpi_i32_f32_sdwa v159, v155 dst_sel:BYTE_3 dst_unused:UNUSED_PRESERVE src0_sel:DWORD
	v_add_u32_e32 v134, 0x14000, v134
	global_store_dwordx2 v134, v[156:157], s[0:1]
	global_store_dwordx2 v134, v[158:159], s[0:1] offset:128
	v_pk_mul_f32 v[140:141], v[48:49], v[186:187] op_sel:[0,1] op_sel_hi:[1,1]
	v_pk_mul_f32 v[142:143], v[50:51], v[186:187] op_sel:[0,1] op_sel_hi:[1,1]
	v_pk_mul_f32 v[144:145], v[44:45], v[186:187] op_sel:[0,1] op_sel_hi:[1,1]
	v_pk_mul_f32 v[146:147], v[46:47], v[186:187] op_sel:[0,1] op_sel_hi:[1,1]
	v_pk_mul_f32 v[148:149], v[40:41], v[186:187] op_sel:[0,1] op_sel_hi:[1,1]
	v_pk_mul_f32 v[150:151], v[42:43], v[186:187] op_sel:[0,1] op_sel_hi:[1,1]
	v_pk_mul_f32 v[152:153], v[36:37], v[186:187] op_sel:[0,1] op_sel_hi:[1,1]
	v_pk_mul_f32 v[154:155], v[38:39], v[186:187] op_sel:[0,1] op_sel_hi:[1,1]
	v_exp_f32_e32 v140, v140
	v_exp_f32_e32 v141, v141
	v_exp_f32_e32 v142, v142
	v_exp_f32_e32 v143, v143
	v_exp_f32_e32 v144, v144
	v_exp_f32_e32 v145, v145
	v_exp_f32_e32 v146, v146
	v_exp_f32_e32 v147, v147
	v_exp_f32_e32 v148, v148
	v_exp_f32_e32 v149, v149
	v_exp_f32_e32 v150, v150
	v_exp_f32_e32 v151, v151
	v_exp_f32_e32 v152, v152
	v_exp_f32_e32 v153, v153
	v_exp_f32_e32 v154, v154
	v_exp_f32_e32 v155, v155
	v_pk_fma_f32 v[140:141], v[140:141], s[8:9], s[8:9] op_sel_hi:[1,0,0]
	v_pk_fma_f32 v[142:143], v[142:143], s[8:9], s[8:9] op_sel_hi:[1,0,0]
	v_pk_fma_f32 v[144:145], v[144:145], s[8:9], s[8:9] op_sel_hi:[1,0,0]
	v_pk_fma_f32 v[146:147], v[146:147], s[8:9], s[8:9] op_sel_hi:[1,0,0]
	v_pk_fma_f32 v[148:149], v[148:149], s[8:9], s[8:9] op_sel_hi:[1,0,0]
	v_pk_fma_f32 v[150:151], v[150:151], s[8:9], s[8:9] op_sel_hi:[1,0,0]
	v_pk_fma_f32 v[152:153], v[152:153], s[8:9], s[8:9] op_sel_hi:[1,0,0]
	v_pk_fma_f32 v[154:155], v[154:155], s[8:9], s[8:9] op_sel_hi:[1,0,0]
	v_rcp_f32_e32 v140, v140
	v_rcp_f32_e32 v141, v141
	v_rcp_f32_e32 v142, v142
	v_rcp_f32_e32 v143, v143
	v_rcp_f32_e32 v144, v144
	v_rcp_f32_e32 v145, v145
	v_rcp_f32_e32 v146, v146
	v_rcp_f32_e32 v147, v147
	v_rcp_f32_e32 v148, v148
	v_rcp_f32_e32 v149, v149
	v_rcp_f32_e32 v150, v150
	v_rcp_f32_e32 v151, v151
	v_rcp_f32_e32 v152, v152
	v_rcp_f32_e32 v153, v153
	v_rcp_f32_e32 v154, v154
	v_rcp_f32_e32 v155, v155
	v_cvt_rpi_i32_f32_sdwa v190, v140 dst_sel:BYTE_0 dst_unused:UNUSED_PAD src0_sel:DWORD
	v_cvt_rpi_i32_f32_sdwa v191, v144 dst_sel:BYTE_0 dst_unused:UNUSED_PAD src0_sel:DWORD
	v_cvt_rpi_i32_f32_sdwa v192, v148 dst_sel:BYTE_0 dst_unused:UNUSED_PAD src0_sel:DWORD
	v_cvt_rpi_i32_f32_sdwa v193, v152 dst_sel:BYTE_0 dst_unused:UNUSED_PAD src0_sel:DWORD
	v_cvt_rpi_i32_f32_sdwa v190, v141 dst_sel:BYTE_1 dst_unused:UNUSED_PRESERVE src0_sel:DWORD
	v_cvt_rpi_i32_f32_sdwa v191, v145 dst_sel:BYTE_1 dst_unused:UNUSED_PRESERVE src0_sel:DWORD
	v_cvt_rpi_i32_f32_sdwa v192, v149 dst_sel:BYTE_1 dst_unused:UNUSED_PRESERVE src0_sel:DWORD
	v_cvt_rpi_i32_f32_sdwa v193, v153 dst_sel:BYTE_1 dst_unused:UNUSED_PRESERVE src0_sel:DWORD
	v_cvt_rpi_i32_f32_sdwa v190, v142 dst_sel:BYTE_2 dst_unused:UNUSED_PRESERVE src0_sel:DWORD
	v_cvt_rpi_i32_f32_sdwa v191, v146 dst_sel:BYTE_2 dst_unused:UNUSED_PRESERVE src0_sel:DWORD
	v_cvt_rpi_i32_f32_sdwa v192, v150 dst_sel:BYTE_2 dst_unused:UNUSED_PRESERVE src0_sel:DWORD
	v_cvt_rpi_i32_f32_sdwa v193, v154 dst_sel:BYTE_2 dst_unused:UNUSED_PRESERVE src0_sel:DWORD
	v_cvt_rpi_i32_f32_sdwa v190, v143 dst_sel:BYTE_3 dst_unused:UNUSED_PRESERVE src0_sel:DWORD
	v_cvt_rpi_i32_f32_sdwa v191, v147 dst_sel:BYTE_3 dst_unused:UNUSED_PRESERVE src0_sel:DWORD
	v_cvt_rpi_i32_f32_sdwa v192, v151 dst_sel:BYTE_3 dst_unused:UNUSED_PRESERVE src0_sel:DWORD
	v_cvt_rpi_i32_f32_sdwa v193, v155 dst_sel:BYTE_3 dst_unused:UNUSED_PRESERVE src0_sel:DWORD
	v_add_u32_e32 v134, 0x4000, v134
;     __device__ __forceinline__ void operator()(const f32x4 (&acc)[2][2][4][2], const Unit& u, int wr, int wc, int fr, int fq) const {
;     ...
;                     for (int m = 0; m < 4; ++m) { unsigned char* rowp = gb8 + (size_t)(row0 + ai * HALF + m * 16) * 1024; const float nrf = -1.4426950408889634f * rsr[ai * HALF + m * 16];
; #pragma unroll
;                         for (int bj = 0; bj < 2; ++bj) { u32x2 w; w.x = 0u; w.y = 0u;
; #pragma unroll
;                             for (int e = 0; e < 4; ++e) { const float x0 = acc[ai][bj][m][0][e], x1 = acc[ai][bj][m][1][e];
;                                 const float r0 = 255.0f * __builtin_amdgcn_rcpf(1.0f + __builtin_amdgcn_exp2f(nrf * x0)), r1 = 255.0f * __builtin_amdgcn_rcpf(1.0f + __builtin_amdgcn_exp2f(nrf * x1));
;                                 w.x |= (unsigned)(r0 + 0.5f) << (8 * e); w.y |= (unsigned)(r1 + 0.5f) << (8 * e); }
;                             *(u32x2*)(rowp + bj * HALF) = w; }
	global_store_dwordx2 v134, v[190:191], s[0:1]
	global_store_dwordx2 v134, v[192:193], s[0:1] offset:128
	v_pk_mul_f32 v[140:141], v[32:33], v[188:189] op_sel:[0,0] op_sel_hi:[1,0]
	v_pk_mul_f32 v[142:143], v[34:35], v[188:189] op_sel:[0,0] op_sel_hi:[1,0]
	v_pk_mul_f32 v[144:145], v[28:29], v[188:189] op_sel:[0,0] op_sel_hi:[1,0]
	v_pk_mul_f32 v[146:147], v[30:31], v[188:189] op_sel:[0,0] op_sel_hi:[1,0]
	v_pk_mul_f32 v[148:149], v[24:25], v[188:189] op_sel:[0,0] op_sel_hi:[1,0]
	v_pk_mul_f32 v[150:151], v[26:27], v[188:189] op_sel:[0,0] op_sel_hi:[1,0]
	v_pk_mul_f32 v[152:153], v[20:21], v[188:189] op_sel:[0,0] op_sel_hi:[1,0]
	v_pk_mul_f32 v[154:155], v[22:23], v[188:189] op_sel:[0,0] op_sel_hi:[1,0]
	v_exp_f32_e32 v140, v140
	v_exp_f32_e32 v141, v141
	v_exp_f32_e32 v142, v142
	v_exp_f32_e32 v143, v143
	v_exp_f32_e32 v144, v144
	v_exp_f32_e32 v145, v145
	v_exp_f32_e32 v146, v146
	v_exp_f32_e32 v147, v147
	v_exp_f32_e32 v148, v148
	v_exp_f32_e32 v149, v149
	v_exp_f32_e32 v150, v150
	v_exp_f32_e32 v151, v151
	v_exp_f32_e32 v152, v152
	v_exp_f32_e32 v153, v153
	v_exp_f32_e32 v154, v154
	v_exp_f32_e32 v155, v155
	v_pk_fma_f32 v[140:141], v[140:141], s[8:9], s[8:9] op_sel_hi:[1,0,0]
	v_pk_fma_f32 v[142:143], v[142:143], s[8:9], s[8:9] op_sel_hi:[1,0,0]
	v_pk_fma_f32 v[144:145], v[144:145], s[8:9], s[8:9] op_sel_hi:[1,0,0]
	v_pk_fma_f32 v[146:147], v[146:147], s[8:9], s[8:9] op_sel_hi:[1,0,0]
	v_pk_fma_f32 v[148:149], v[148:149], s[8:9], s[8:9] op_sel_hi:[1,0,0]
	v_pk_fma_f32 v[150:151], v[150:151], s[8:9], s[8:9] op_sel_hi:[1,0,0]
	v_pk_fma_f32 v[152:153], v[152:153], s[8:9], s[8:9] op_sel_hi:[1,0,0]
	v_pk_fma_f32 v[154:155], v[154:155], s[8:9], s[8:9] op_sel_hi:[1,0,0]
	v_rcp_f32_e32 v140, v140
	v_rcp_f32_e32 v141, v141
	v_rcp_f32_e32 v142, v142
	v_rcp_f32_e32 v143, v143
	v_rcp_f32_e32 v144, v144
	v_rcp_f32_e32 v145, v145
	v_rcp_f32_e32 v146, v146
	v_rcp_f32_e32 v147, v147
	v_rcp_f32_e32 v148, v148
	v_rcp_f32_e32 v149, v149
	v_rcp_f32_e32 v150, v150
	v_rcp_f32_e32 v151, v151
	v_rcp_f32_e32 v152, v152
	v_rcp_f32_e32 v153, v153
	v_rcp_f32_e32 v154, v154
	v_rcp_f32_e32 v155, v155
	v_cvt_rpi_i32_f32_sdwa v156, v140 dst_sel:BYTE_0 dst_unused:UNUSED_PAD src0_sel:DWORD
	v_cvt_rpi_i32_f32_sdwa v157, v144 dst_sel:BYTE_0 dst_unused:UNUSED_PAD src0_sel:DWORD
	v_cvt_rpi_i32_f32_sdwa v158, v148 dst_sel:BYTE_0 dst_unused:UNUSED_PAD src0_sel:DWORD
	v_cvt_rpi_i32_f32_sdwa v159, v152 dst_sel:BYTE_0 dst_unused:UNUSED_PAD src0_sel:DWORD
	v_cvt_rpi_i32_f32_sdwa v156, v141 dst_sel:BYTE_1 dst_unused:UNUSED_PRESERVE src0_sel:DWORD
	v_cvt_rpi_i32_f32_sdwa v157, v145 dst_sel:BYTE_1 dst_unused:UNUSED_PRESERVE src0_sel:DWORD
	v_cvt_rpi_i32_f32_sdwa v158, v149 dst_sel:BYTE_1 dst_unused:UNUSED_PRESERVE src0_sel:DWORD
	v_cvt_rpi_i32_f32_sdwa v159, v153 dst_sel:BYTE_1 dst_unused:UNUSED_PRESERVE src0_sel:DWORD
	v_cvt_rpi_i32_f32_sdwa v156, v142 dst_sel:BYTE_2 dst_unused:UNUSED_PRESERVE src0_sel:DWORD
	v_cvt_rpi_i32_f32_sdwa v157, v146 dst_sel:BYTE_2 dst_unused:UNUSED_PRESERVE src0_sel:DWORD
	v_cvt_rpi_i32_f32_sdwa v158, v150 dst_sel:BYTE_2 dst_unused:UNUSED_PRESERVE src0_sel:DWORD
	v_cvt_rpi_i32_f32_sdwa v159, v154 dst_sel:BYTE_2 dst_unused:UNUSED_PRESERVE src0_sel:DWORD
	v_cvt_rpi_i32_f32_sdwa v156, v143 dst_sel:BYTE_3 dst_unused:UNUSED_PRESERVE src0_sel:DWORD
	v_cvt_rpi_i32_f32_sdwa v157, v147 dst_sel:BYTE_3 dst_unused:UNUSED_PRESERVE src0_sel:DWORD
	v_cvt_rpi_i32_f32_sdwa v158, v151 dst_sel:BYTE_3 dst_unused:UNUSED_PRESERVE src0_sel:DWORD
	v_cvt_rpi_i32_f32_sdwa v159, v155 dst_sel:BYTE_3 dst_unused:UNUSED_PRESERVE src0_sel:DWORD
	v_add_u32_e32 v134, 0x4000, v134
	global_store_dwordx2 v134, v[156:157], s[0:1]
	global_store_dwordx2 v134, v[158:159], s[0:1] offset:128
	v_pk_mul_f32 v[140:141], v[16:17], v[188:189] op_sel:[0,1] op_sel_hi:[1,1]
	v_pk_mul_f32 v[142:143], v[18:19], v[188:189] op_sel:[0,1] op_sel_hi:[1,1]
	v_pk_mul_f32 v[144:145], v[12:13], v[188:189] op_sel:[0,1] op_sel_hi:[1,1]
	v_pk_mul_f32 v[146:147], v[14:15], v[188:189] op_sel:[0,1] op_sel_hi:[1,1]
	v_pk_mul_f32 v[148:149], v[8:9], v[188:189] op_sel:[0,1] op_sel_hi:[1,1]
	v_pk_mul_f32 v[150:151], v[10:11], v[188:189] op_sel:[0,1] op_sel_hi:[1,1]
	v_pk_mul_f32 v[152:153], v[4:5], v[188:189] op_sel:[0,1] op_sel_hi:[1,1]
	v_pk_mul_f32 v[154:155], v[6:7], v[188:189] op_sel:[0,1] op_sel_hi:[1,1]
	v_exp_f32_e32 v140, v140
	v_exp_f32_e32 v141, v141
	v_exp_f32_e32 v142, v142
	v_exp_f32_e32 v143, v143
	v_exp_f32_e32 v144, v144
	v_exp_f32_e32 v145, v145
	v_exp_f32_e32 v146, v146
	v_exp_f32_e32 v147, v147
	v_exp_f32_e32 v148, v148
	v_exp_f32_e32 v149, v149
	v_exp_f32_e32 v150, v150
	v_exp_f32_e32 v151, v151
	v_exp_f32_e32 v152, v152
	v_exp_f32_e32 v153, v153
	v_exp_f32_e32 v154, v154
	v_exp_f32_e32 v155, v155
	v_pk_fma_f32 v[140:141], v[140:141], s[8:9], s[8:9] op_sel_hi:[1,0,0]
	v_pk_fma_f32 v[142:143], v[142:143], s[8:9], s[8:9] op_sel_hi:[1,0,0]
	v_pk_fma_f32 v[144:145], v[144:145], s[8:9], s[8:9] op_sel_hi:[1,0,0]
	v_pk_fma_f32 v[146:147], v[146:147], s[8:9], s[8:9] op_sel_hi:[1,0,0]
	v_pk_fma_f32 v[148:149], v[148:149], s[8:9], s[8:9] op_sel_hi:[1,0,0]
	v_pk_fma_f32 v[150:151], v[150:151], s[8:9], s[8:9] op_sel_hi:[1,0,0]
	v_pk_fma_f32 v[152:153], v[152:153], s[8:9], s[8:9] op_sel_hi:[1,0,0]
	v_pk_fma_f32 v[154:155], v[154:155], s[8:9], s[8:9] op_sel_hi:[1,0,0]
	v_rcp_f32_e32 v140, v140
	v_rcp_f32_e32 v141, v141
	v_rcp_f32_e32 v142, v142
	v_rcp_f32_e32 v143, v143
	v_rcp_f32_e32 v144, v144
	v_rcp_f32_e32 v145, v145
	v_rcp_f32_e32 v146, v146
	v_rcp_f32_e32 v147, v147
	v_rcp_f32_e32 v148, v148
	v_rcp_f32_e32 v149, v149
	v_rcp_f32_e32 v150, v150
	v_rcp_f32_e32 v151, v151
	v_rcp_f32_e32 v152, v152
;     const float c0 = act == 1 ? -2.302208198f : -1.4426950408889634f, c1 = act == 1 ? -0.10294324f : 0.f;
; #pragma unroll
;     for (int ai = 0; ai < 2; ++ai) { if (ai == 1 && halfunit) break;
; #pragma unroll
;         for (int m = 0; m < 4; ++m) { bf16_t* rowp = base + (size_t)(row0 + ai * HALF + m * 16) * ldc + col0; float ls1 = 0.f, ls2 = 0.f; const float rf = rsr[ai * HALF + m * 16];
; #pragma unroll
;             for (int bj = 0; bj < 2; ++bj) { f32x4 v0 = acc[ai][bj][m][0] * rf, v1 = acc[ai][bj][m][1] * rf;
;                 if (act != 0) {
; #pragma unroll
;                     for (int e = 0; e < 4; ++e) { const float x0 = v0[e], x1 = v1[e];
;                         const float r0 = __builtin_amdgcn_rcpf(1.0f + __builtin_amdgcn_exp2f(x0 * (c0 + c1 * x0 * x0))), r1 = __builtin_amdgcn_rcpf(1.0f + __builtin_amdgcn_exp2f(x1 * (c0 + c1 * x1 * x1)));
;                         v0[e] = act == 1 ? x0 * r0 : r0; v1[e] = act == 1 ? x1 * r1 : r1; } }
;                 if (stat) {
; #pragma unroll
;     __device__ __forceinline__ void operator()(const f32x4 (&acc)[2][2][4][2], const Unit& u, int wr, int wc, int fr, int fq) const {
;     ...
;             bf16_t* base = (bf16_t*)(wsb + (pn < 2 ? WS_U : (pn < 4 ? WS_VG : WS_VA))); const int ldc = 512, pc = pn < 2 ? pn : (pn < 4 ? pn - 2 : pn - 8), act = pn < 4 ? 1 : 0;
;             float* stat = (pn == 2 || pn == 3) ? (float*)(wsb + WS_STAT) + ((pn - 2) * 4 + wc) * 2 : nullptr;
;             if (pn < 10) store_tile8(acc, rsr, base, ldc, row0, pc * 256 + cl, act, u.half != 0, stat, fq);
;     ...
;                     for (int m = 0; m < 4; ++m) { unsigned char* rowp = gb8 + (size_t)(row0 + ai * HALF + m * 16) * 1024; const float nrf = -1.4426950408889634f * rsr[ai * HALF + m * 16];
; #pragma unroll
;                         for (int bj = 0; bj < 2; ++bj) { u32x2 w; w.x = 0u; w.y = 0u;
; #pragma unroll
;                             for (int e = 0; e < 4; ++e) { const float x0 = acc[ai][bj][m][0][e], x1 = acc[ai][bj][m][1][e];
;                                 const float r0 = 255.0f * __builtin_amdgcn_rcpf(1.0f + __builtin_amdgcn_exp2f(nrf * x0)), r1 = 255.0f * __builtin_amdgcn_rcpf(1.0f + __builtin_amdgcn_exp2f(nrf * x1));
;                                 w.x |= (unsigned)(r0 + 0.5f) << (8 * e); w.y |= (unsigned)(r1 + 0.5f) << (8 * e); }
;                             *(u32x2*)(rowp + bj * HALF) = w; }
	v_rcp_f32_e32 v153, v153
	v_rcp_f32_e32 v154, v154
	v_rcp_f32_e32 v155, v155
	v_cvt_rpi_i32_f32_sdwa v190, v140 dst_sel:BYTE_0 dst_unused:UNUSED_PAD src0_sel:DWORD
	v_cvt_rpi_i32_f32_sdwa v191, v144 dst_sel:BYTE_0 dst_unused:UNUSED_PAD src0_sel:DWORD
	v_cvt_rpi_i32_f32_sdwa v192, v148 dst_sel:BYTE_0 dst_unused:UNUSED_PAD src0_sel:DWORD
	v_cvt_rpi_i32_f32_sdwa v193, v152 dst_sel:BYTE_0 dst_unused:UNUSED_PAD src0_sel:DWORD
	v_cvt_rpi_i32_f32_sdwa v190, v141 dst_sel:BYTE_1 dst_unused:UNUSED_PRESERVE src0_sel:DWORD
	v_cvt_rpi_i32_f32_sdwa v191, v145 dst_sel:BYTE_1 dst_unused:UNUSED_PRESERVE src0_sel:DWORD
	v_cvt_rpi_i32_f32_sdwa v192, v149 dst_sel:BYTE_1 dst_unused:UNUSED_PRESERVE src0_sel:DWORD
	v_cvt_rpi_i32_f32_sdwa v193, v153 dst_sel:BYTE_1 dst_unused:UNUSED_PRESERVE src0_sel:DWORD
	v_cvt_rpi_i32_f32_sdwa v190, v142 dst_sel:BYTE_2 dst_unused:UNUSED_PRESERVE src0_sel:DWORD
	v_cvt_rpi_i32_f32_sdwa v191, v146 dst_sel:BYTE_2 dst_unused:UNUSED_PRESERVE src0_sel:DWORD
	v_cvt_rpi_i32_f32_sdwa v192, v150 dst_sel:BYTE_2 dst_unused:UNUSED_PRESERVE src0_sel:DWORD
	v_cvt_rpi_i32_f32_sdwa v193, v154 dst_sel:BYTE_2 dst_unused:UNUSED_PRESERVE src0_sel:DWORD
	v_cvt_rpi_i32_f32_sdwa v190, v143 dst_sel:BYTE_3 dst_unused:UNUSED_PRESERVE src0_sel:DWORD
	v_cvt_rpi_i32_f32_sdwa v191, v147 dst_sel:BYTE_3 dst_unused:UNUSED_PRESERVE src0_sel:DWORD
	v_cvt_rpi_i32_f32_sdwa v192, v151 dst_sel:BYTE_3 dst_unused:UNUSED_PRESERVE src0_sel:DWORD
	v_cvt_rpi_i32_f32_sdwa v193, v155 dst_sel:BYTE_3 dst_unused:UNUSED_PRESERVE src0_sel:DWORD
	v_add_u32_e32 v134, 0x4000, v134
	global_store_dwordx2 v134, v[190:191], s[0:1]
	global_store_dwordx2 v134, v[192:193], s[0:1] offset:128
	s_mov_b64 s[0:1], 0
.LBB0_401:
	s_andn2_b64 vcc, exec, s[0:1]
	s_cbranch_vccnz .LBB0_537
	ds_read_b32 v208, v205
	ds_read_b32 v209, v205 offset:64
	ds_read_b32 v210, v205 offset:128
	ds_read_b32 v211, v205 offset:192
	ds_read_b32 v212, v205 offset:512
	ds_read_b32 v213, v205 offset:576
	ds_read_b32 v214, v205 offset:640
	ds_read_b32 v215, v205 offset:704
	s_mov_b32 s0, 0xe000000
	s_cmp_lt_i32 s70, 4
	s_cselect_b32 s0, 0xc000000, s0
	s_cmp_lt_i32 s70, 2
	s_cselect_b32 s0, 0xa000000, s0
	s_and_b32 s1, s70, 1
	s_lshl_b32 s1, s1, 9
	s_add_i32 s0, s0, s1
	s_add_u32 s0, s16, s0
	s_addc_u32 s1, s17, 0
	v_lshlrev_b32_e32 v134, 1, v172
	v_lshl_add_u32 v134, v132, 10, v134
	s_lshl_b32 s8, s70, 3
	s_add_i32 s8, s74, s8
	s_ashr_i32 s9, s8, 31
	s_lshl_b64 s[8:9], s[8:9], 2
	s_add_u32 s38, s75, s8
	s_addc_u32 s39, s76, s9
	v_lshlrev_b32_e32 v135, 6, v132
	s_cmp_lt_i32 s70, 2
	s_cbranch_scc1 .Lt8_gelu
	s_cmp_lt_i32 s70, 4
	s_cbranch_scc1 .Lt8_gstat
	s_waitcnt lgkmcnt(0)
	v_pk_mul_f32 v[128:129], v[128:129], v[208:209] op_sel:[0,0] op_sel_hi:[1,0]
	v_pk_mul_f32 v[130:131], v[130:131], v[208:209] op_sel:[0,0] op_sel_hi:[1,0]
	v_pk_mul_f32 v[124:125], v[124:125], v[208:209] op_sel:[0,0] op_sel_hi:[1,0]
	v_pk_mul_f32 v[126:127], v[126:127], v[208:209] op_sel:[0,0] op_sel_hi:[1,0]
	v_pk_mul_f32 v[120:121], v[120:121], v[208:209] op_sel:[0,0] op_sel_hi:[1,0]
	v_pk_mul_f32 v[122:123], v[122:123], v[208:209] op_sel:[0,0] op_sel_hi:[1,0]
	v_pk_mul_f32 v[116:117], v[116:117], v[208:209] op_sel:[0,0] op_sel_hi:[1,0]
	v_pk_mul_f32 v[118:119], v[118:119], v[208:209] op_sel:[0,0] op_sel_hi:[1,0]
	v_cvt_pk_bf16_f32 v128, v128, v129
	v_cvt_pk_bf16_f32 v129, v130, v131
	v_cvt_pk_bf16_f32 v130, v124, v125
	v_cvt_pk_bf16_f32 v131, v126, v127
	global_store_dwordx4 v134, v[128:131], s[0:1]
	v_cvt_pk_bf16_f32 v120, v120, v121
	v_cvt_pk_bf16_f32 v121, v122, v123
	v_cvt_pk_bf16_f32 v122, v116, v117
	v_cvt_pk_bf16_f32 v123, v118, v119
	global_store_dwordx4 v134, v[120:123], s[0:1] offset:256
	v_pk_mul_f32 v[112:113], v[112:113], v[208:209] op_sel:[0,1] op_sel_hi:[1,1]
	v_pk_mul_f32 v[114:115], v[114:115], v[208:209] op_sel:[0,1] op_sel_hi:[1,1]
	v_pk_mul_f32 v[108:109], v[108:109], v[208:209] op_sel:[0,1] op_sel_hi:[1,1]
	v_pk_mul_f32 v[110:111], v[110:111], v[208:209] op_sel:[0,1] op_sel_hi:[1,1]
	v_pk_mul_f32 v[104:105], v[104:105], v[208:209] op_sel:[0,1] op_sel_hi:[1,1]
	v_pk_mul_f32 v[106:107], v[106:107], v[208:209] op_sel:[0,1] op_sel_hi:[1,1]
	v_pk_mul_f32 v[100:101], v[100:101], v[208:209] op_sel:[0,1] op_sel_hi:[1,1]
	v_pk_mul_f32 v[102:103], v[102:103], v[208:209] op_sel:[0,1] op_sel_hi:[1,1]
	v_add_u32_e32 v134, 0x4000, v134
	v_cvt_pk_bf16_f32 v112, v112, v113
	v_cvt_pk_bf16_f32 v113, v114, v115
	v_cvt_pk_bf16_f32 v114, v108, v109
	v_cvt_pk_bf16_f32 v115, v110, v111
	global_store_dwordx4 v134, v[112:115], s[0:1]
	v_cvt_pk_bf16_f32 v104, v104, v105
	v_cvt_pk_bf16_f32 v105, v106, v107
	v_cvt_pk_bf16_f32 v106, v100, v101
	v_cvt_pk_bf16_f32 v107, v102, v103
	global_store_dwordx4 v134, v[104:107], s[0:1] offset:256
	v_pk_mul_f32 v[96:97], v[96:97], v[210:211] op_sel:[0,0] op_sel_hi:[1,0]
	v_pk_mul_f32 v[98:99], v[98:99], v[210:211] op_sel:[0,0] op_sel_hi:[1,0]
	v_pk_mul_f32 v[92:93], v[92:93], v[210:211] op_sel:[0,0] op_sel_hi:[1,0]
	v_pk_mul_f32 v[94:95], v[94:95], v[210:211] op_sel:[0,0] op_sel_hi:[1,0]
	v_pk_mul_f32 v[88:89], v[88:89], v[210:211] op_sel:[0,0] op_sel_hi:[1,0]
	v_pk_mul_f32 v[90:91], v[90:91], v[210:211] op_sel:[0,0] op_sel_hi:[1,0]
	v_pk_mul_f32 v[84:85], v[84:85], v[210:211] op_sel:[0,0] op_sel_hi:[1,0]
	v_pk_mul_f32 v[86:87], v[86:87], v[210:211] op_sel:[0,0] op_sel_hi:[1,0]
	v_add_u32_e32 v134, 0x4000, v134
	v_cvt_pk_bf16_f32 v96, v96, v97
	v_cvt_pk_bf16_f32 v97, v98, v99
	v_cvt_pk_bf16_f32 v98, v92, v93
	v_cvt_pk_bf16_f32 v99, v94, v95
	global_store_dwordx4 v134, v[96:99], s[0:1]
	v_cvt_pk_bf16_f32 v88, v88, v89
	v_cvt_pk_bf16_f32 v89, v90, v91
	v_cvt_pk_bf16_f32 v90, v84, v85
	v_cvt_pk_bf16_f32 v91, v86, v87
; __device__ __forceinline__ u32x4 pack8(const f32x4 a, const f32x4 b) { u32x4 w; w.x = cvt_pk_bf16(a[0], a[1]); w.y = cvt_pk_bf16(a[2], a[3]); w.z = cvt_pk_bf16(b[0], b[1]); w.w = cvt_pk_bf16(b[2], b[3]); return w; }
;     const float c0 = act == 1 ? -2.302208198f : -1.4426950408889634f, c1 = act == 1 ? -0.10294324f : 0.f;
; #pragma unroll
;     for (int ai = 0; ai < 2; ++ai) { if (ai == 1 && halfunit) break;
; #pragma unroll
;         for (int m = 0; m < 4; ++m) { bf16_t* rowp = base + (size_t)(row0 + ai * HALF + m * 16) * ldc + col0; float ls1 = 0.f, ls2 = 0.f; const float rf = rsr[ai * HALF + m * 16];
; #pragma unroll
;             for (int bj = 0; bj < 2; ++bj) { f32x4 v0 = acc[ai][bj][m][0] * rf, v1 = acc[ai][bj][m][1] * rf;
;                 if (act != 0) {
; #pragma unroll
;                     for (int e = 0; e < 4; ++e) { const float x0 = v0[e], x1 = v1[e];
;                         const float r0 = __builtin_amdgcn_rcpf(1.0f + __builtin_amdgcn_exp2f(x0 * (c0 + c1 * x0 * x0))), r1 = __builtin_amdgcn_rcpf(1.0f + __builtin_amdgcn_exp2f(x1 * (c0 + c1 * x1 * x1)));
;                         v0[e] = act == 1 ? x0 * r0 : r0; v1[e] = act == 1 ? x1 * r1 : r1; } }
;                 if (stat) {
; #pragma unroll
;                     for (int e = 0; e < 4; ++e) { ls1 += v0[e] + v1[e]; ls2 += v0[e] * v0[e] + v1[e] * v1[e]; } }
;                 *(u32x4*)(rowp + bj * HALF) = pack8(v0, v1); }
;             if (stat) { ls1 = xor_add<16>(ls1); ls1 = xor_add<32>(ls1); ls2 = xor_add<16>(ls2); ls2 = xor_add<32>(ls2);
;                 if (fq == 0) { f32x2 st2; st2.x = ls1; st2.y = ls2; *(f32x2*)(stat + (size_t)(row0 + ai * HALF + m * 16) * 16) = st2; } }
;             asm volatile("" ::: "memory"); } }
	global_store_dwordx4 v134, v[88:91], s[0:1] offset:256
	v_pk_mul_f32 v[80:81], v[80:81], v[210:211] op_sel:[0,1] op_sel_hi:[1,1]
	v_pk_mul_f32 v[82:83], v[82:83], v[210:211] op_sel:[0,1] op_sel_hi:[1,1]
	v_pk_mul_f32 v[76:77], v[76:77], v[210:211] op_sel:[0,1] op_sel_hi:[1,1]
	v_pk_mul_f32 v[78:79], v[78:79], v[210:211] op_sel:[0,1] op_sel_hi:[1,1]
	v_pk_mul_f32 v[72:73], v[72:73], v[210:211] op_sel:[0,1] op_sel_hi:[1,1]
	v_pk_mul_f32 v[74:75], v[74:75], v[210:211] op_sel:[0,1] op_sel_hi:[1,1]
	v_pk_mul_f32 v[68:69], v[68:69], v[210:211] op_sel:[0,1] op_sel_hi:[1,1]
	v_pk_mul_f32 v[70:71], v[70:71], v[210:211] op_sel:[0,1] op_sel_hi:[1,1]
	v_add_u32_e32 v134, 0x4000, v134
	v_cvt_pk_bf16_f32 v80, v80, v81
	v_cvt_pk_bf16_f32 v81, v82, v83
	v_cvt_pk_bf16_f32 v82, v76, v77
	v_cvt_pk_bf16_f32 v83, v78, v79
	global_store_dwordx4 v134, v[80:83], s[0:1]
	v_cvt_pk_bf16_f32 v72, v72, v73
	v_cvt_pk_bf16_f32 v73, v74, v75
	v_cvt_pk_bf16_f32 v74, v68, v69
	v_cvt_pk_bf16_f32 v75, v70, v71
	global_store_dwordx4 v134, v[72:75], s[0:1] offset:256
	v_pk_mul_f32 v[64:65], v[64:65], v[212:213] op_sel:[0,0] op_sel_hi:[1,0]
	v_pk_mul_f32 v[66:67], v[66:67], v[212:213] op_sel:[0,0] op_sel_hi:[1,0]
	v_pk_mul_f32 v[60:61], v[60:61], v[212:213] op_sel:[0,0] op_sel_hi:[1,0]
	v_pk_mul_f32 v[62:63], v[62:63], v[212:213] op_sel:[0,0] op_sel_hi:[1,0]
	v_pk_mul_f32 v[56:57], v[56:57], v[212:213] op_sel:[0,0] op_sel_hi:[1,0]
	v_pk_mul_f32 v[58:59], v[58:59], v[212:213] op_sel:[0,0] op_sel_hi:[1,0]
	v_pk_mul_f32 v[52:53], v[52:53], v[212:213] op_sel:[0,0] op_sel_hi:[1,0]
	v_pk_mul_f32 v[54:55], v[54:55], v[212:213] op_sel:[0,0] op_sel_hi:[1,0]
	v_add_u32_e32 v134, 0x14000, v134
	v_cvt_pk_bf16_f32 v64, v64, v65
	v_cvt_pk_bf16_f32 v65, v66, v67
	v_cvt_pk_bf16_f32 v66, v60, v61
	v_cvt_pk_bf16_f32 v67, v62, v63
	global_store_dwordx4 v134, v[64:67], s[0:1]
	v_cvt_pk_bf16_f32 v56, v56, v57
	v_cvt_pk_bf16_f32 v57, v58, v59
	v_cvt_pk_bf16_f32 v58, v52, v53
	v_cvt_pk_bf16_f32 v59, v54, v55
	global_store_dwordx4 v134, v[56:59], s[0:1] offset:256
	v_pk_mul_f32 v[48:49], v[48:49], v[212:213] op_sel:[0,1] op_sel_hi:[1,1]
	v_pk_mul_f32 v[50:51], v[50:51], v[212:213] op_sel:[0,1] op_sel_hi:[1,1]
	v_pk_mul_f32 v[44:45], v[44:45], v[212:213] op_sel:[0,1] op_sel_hi:[1,1]
	v_pk_mul_f32 v[46:47], v[46:47], v[212:213] op_sel:[0,1] op_sel_hi:[1,1]
	v_pk_mul_f32 v[40:41], v[40:41], v[212:213] op_sel:[0,1] op_sel_hi:[1,1]
	v_pk_mul_f32 v[42:43], v[42:43], v[212:213] op_sel:[0,1] op_sel_hi:[1,1]
	v_pk_mul_f32 v[36:37], v[36:37], v[212:213] op_sel:[0,1] op_sel_hi:[1,1]
	v_pk_mul_f32 v[38:39], v[38:39], v[212:213] op_sel:[0,1] op_sel_hi:[1,1]
	v_add_u32_e32 v134, 0x4000, v134
	v_cvt_pk_bf16_f32 v48, v48, v49
	v_cvt_pk_bf16_f32 v49, v50, v51
	v_cvt_pk_bf16_f32 v50, v44, v45
	v_cvt_pk_bf16_f32 v51, v46, v47
	global_store_dwordx4 v134, v[48:51], s[0:1]
	v_cvt_pk_bf16_f32 v40, v40, v41
	v_cvt_pk_bf16_f32 v41, v42, v43
	v_cvt_pk_bf16_f32 v42, v36, v37
	v_cvt_pk_bf16_f32 v43, v38, v39
	global_store_dwordx4 v134, v[40:43], s[0:1] offset:256
	v_pk_mul_f32 v[32:33], v[32:33], v[214:215] op_sel:[0,0] op_sel_hi:[1,0]
	v_pk_mul_f32 v[34:35], v[34:35], v[214:215] op_sel:[0,0] op_sel_hi:[1,0]
	v_pk_mul_f32 v[28:29], v[28:29], v[214:215] op_sel:[0,0] op_sel_hi:[1,0]
	v_pk_mul_f32 v[30:31], v[30:31], v[214:215] op_sel:[0,0] op_sel_hi:[1,0]
	v_pk_mul_f32 v[24:25], v[24:25], v[214:215] op_sel:[0,0] op_sel_hi:[1,0]
	v_pk_mul_f32 v[26:27], v[26:27], v[214:215] op_sel:[0,0] op_sel_hi:[1,0]
	v_pk_mul_f32 v[20:21], v[20:21], v[214:215] op_sel:[0,0] op_sel_hi:[1,0]
	v_pk_mul_f32 v[22:23], v[22:23], v[214:215] op_sel:[0,0] op_sel_hi:[1,0]
	v_add_u32_e32 v134, 0x4000, v134
	v_cvt_pk_bf16_f32 v32, v32, v33
	v_cvt_pk_bf16_f32 v33, v34, v35
	v_cvt_pk_bf16_f32 v34, v28, v29
	v_cvt_pk_bf16_f32 v35, v30, v31
	global_store_dwordx4 v134, v[32:35], s[0:1]
	v_cvt_pk_bf16_f32 v24, v24, v25
	v_cvt_pk_bf16_f32 v25, v26, v27
	v_cvt_pk_bf16_f32 v26, v20, v21
	v_cvt_pk_bf16_f32 v27, v22, v23
	global_store_dwordx4 v134, v[24:27], s[0:1] offset:256
	v_pk_mul_f32 v[16:17], v[16:17], v[214:215] op_sel:[0,1] op_sel_hi:[1,1]
	v_pk_mul_f32 v[18:19], v[18:19], v[214:215] op_sel:[0,1] op_sel_hi:[1,1]
	v_pk_mul_f32 v[12:13], v[12:13], v[214:215] op_sel:[0,1] op_sel_hi:[1,1]
	v_pk_mul_f32 v[14:15], v[14:15], v[214:215] op_sel:[0,1] op_sel_hi:[1,1]
	v_pk_mul_f32 v[8:9], v[8:9], v[214:215] op_sel:[0,1] op_sel_hi:[1,1]
	v_pk_mul_f32 v[10:11], v[10:11], v[214:215] op_sel:[0,1] op_sel_hi:[1,1]
	v_pk_mul_f32 v[4:5], v[4:5], v[214:215] op_sel:[0,1] op_sel_hi:[1,1]
	v_pk_mul_f32 v[6:7], v[6:7], v[214:215] op_sel:[0,1] op_sel_hi:[1,1]
	v_add_u32_e32 v134, 0x4000, v134
	v_cvt_pk_bf16_f32 v16, v16, v17
	v_cvt_pk_bf16_f32 v17, v18, v19
	v_cvt_pk_bf16_f32 v18, v12, v13
	v_cvt_pk_bf16_f32 v19, v14, v15
	global_store_dwordx4 v134, v[16:19], s[0:1]
	v_cvt_pk_bf16_f32 v8, v8, v9
	v_cvt_pk_bf16_f32 v9, v10, v11
	v_cvt_pk_bf16_f32 v10, v4, v5
	v_cvt_pk_bf16_f32 v11, v6, v7
	global_store_dwordx4 v134, v[8:11], s[0:1] offset:256
	s_branch .Lt8_end
; __device__ __forceinline__ u32x4 pack8(const f32x4 a, const f32x4 b) { u32x4 w; w.x = cvt_pk_bf16(a[0], a[1]); w.y = cvt_pk_bf16(a[2], a[3]); w.z = cvt_pk_bf16(b[0], b[1]); w.w = cvt_pk_bf16(b[2], b[3]); return w; }
;     const float c0 = act == 1 ? -2.302208198f : -1.4426950408889634f, c1 = act == 1 ? -0.10294324f : 0.f;
; #pragma unroll
;     for (int ai = 0; ai < 2; ++ai) { if (ai == 1 && halfunit) break;
; #pragma unroll
;         for (int m = 0; m < 4; ++m) { bf16_t* rowp = base + (size_t)(row0 + ai * HALF + m * 16) * ldc + col0; float ls1 = 0.f, ls2 = 0.f; const float rf = rsr[ai * HALF + m * 16];
; #pragma unroll
;             for (int bj = 0; bj < 2; ++bj) { f32x4 v0 = acc[ai][bj][m][0] * rf, v1 = acc[ai][bj][m][1] * rf;
;                 if (act != 0) {
; #pragma unroll
;                     for (int e = 0; e < 4; ++e) { const float x0 = v0[e], x1 = v1[e];
;                         const float r0 = __builtin_amdgcn_rcpf(1.0f + __builtin_amdgcn_exp2f(x0 * (c0 + c1 * x0 * x0))), r1 = __builtin_amdgcn_rcpf(1.0f + __builtin_amdgcn_exp2f(x1 * (c0 + c1 * x1 * x1)));
;                         v0[e] = act == 1 ? x0 * r0 : r0; v1[e] = act == 1 ? x1 * r1 : r1; } }
;                 if (stat) {
; #pragma unroll
;                     for (int e = 0; e < 4; ++e) { ls1 += v0[e] + v1[e]; ls2 += v0[e] * v0[e] + v1[e] * v1[e]; } }
;                 *(u32x4*)(rowp + bj * HALF) = pack8(v0, v1); }
.Lt8_gelu:
	s_waitcnt lgkmcnt(0)
	s_mov_b32 s8, 0xc0135761
	s_mov_b32 s9, 0xbdd2d3e8
	v_pk_mul_f32 v[182:183], v[208:209], s[8:9] op_sel_hi:[1,0]
	v_pk_mul_f32 v[184:185], v[210:211], s[8:9] op_sel_hi:[1,0]
	v_pk_mul_f32 v[186:187], v[212:213], s[8:9] op_sel_hi:[1,0]
	v_pk_mul_f32 v[188:189], v[214:215], s[8:9] op_sel_hi:[1,0]
	v_pk_mul_f32 v[190:191], v[208:209], v[208:209]
	v_pk_mul_f32 v[192:193], v[210:211], v[210:211]
	v_pk_mul_f32 v[194:195], v[212:213], v[212:213]
	v_pk_mul_f32 v[196:197], v[214:215], v[214:215]
	v_pk_mul_f32 v[190:191], v[190:191], v[208:209]
	v_pk_mul_f32 v[192:193], v[192:193], v[210:211]
	v_pk_mul_f32 v[194:195], v[194:195], v[212:213]
	v_pk_mul_f32 v[196:197], v[196:197], v[214:215]
	v_pk_mul_f32 v[190:191], v[190:191], s[8:9] op_sel:[0,1] op_sel_hi:[1,1]
	v_pk_mul_f32 v[192:193], v[192:193], s[8:9] op_sel:[0,1] op_sel_hi:[1,1]
	v_pk_mul_f32 v[194:195], v[194:195], s[8:9] op_sel:[0,1] op_sel_hi:[1,1]
	v_pk_mul_f32 v[196:197], v[196:197], s[8:9] op_sel:[0,1] op_sel_hi:[1,1]
	v_rcp_f32_e32 v208, v208
	v_rcp_f32_e32 v209, v209
	v_rcp_f32_e32 v210, v210
	v_rcp_f32_e32 v211, v211
	v_rcp_f32_e32 v212, v212
	v_rcp_f32_e32 v213, v213
	v_rcp_f32_e32 v214, v214
	v_rcp_f32_e32 v215, v215
	v_pk_mul_f32 v[140:141], v[128:129], v[128:129]
	v_pk_mul_f32 v[142:143], v[130:131], v[130:131]
	v_pk_mul_f32 v[144:145], v[124:125], v[124:125]
	v_pk_mul_f32 v[146:147], v[126:127], v[126:127]
	v_pk_mul_f32 v[148:149], v[120:121], v[120:121]
	v_pk_mul_f32 v[150:151], v[122:123], v[122:123]
	v_pk_mul_f32 v[152:153], v[116:117], v[116:117]
	v_pk_mul_f32 v[154:155], v[118:119], v[118:119]
	v_pk_fma_f32 v[140:141], v[140:141], v[190:191], v[182:183] op_sel:[0,0,0] op_sel_hi:[1,0,0]
	v_pk_fma_f32 v[142:143], v[142:143], v[190:191], v[182:183] op_sel:[0,0,0] op_sel_hi:[1,0,0]
	v_pk_fma_f32 v[144:145], v[144:145], v[190:191], v[182:183] op_sel:[0,0,0] op_sel_hi:[1,0,0]
	v_pk_fma_f32 v[146:147], v[146:147], v[190:191], v[182:183] op_sel:[0,0,0] op_sel_hi:[1,0,0]
	v_pk_fma_f32 v[148:149], v[148:149], v[190:191], v[182:183] op_sel:[0,0,0] op_sel_hi:[1,0,0]
	v_pk_fma_f32 v[150:151], v[150:151], v[190:191], v[182:183] op_sel:[0,0,0] op_sel_hi:[1,0,0]
	v_pk_fma_f32 v[152:153], v[152:153], v[190:191], v[182:183] op_sel:[0,0,0] op_sel_hi:[1,0,0]
	v_pk_fma_f32 v[154:155], v[154:155], v[190:191], v[182:183] op_sel:[0,0,0] op_sel_hi:[1,0,0]
	v_pk_mul_f32 v[140:141], v[128:129], v[140:141]
	v_pk_mul_f32 v[142:143], v[130:131], v[142:143]
	v_pk_mul_f32 v[144:145], v[124:125], v[144:145]
	v_pk_mul_f32 v[146:147], v[126:127], v[146:147]
	v_pk_mul_f32 v[148:149], v[120:121], v[148:149]
	v_pk_mul_f32 v[150:151], v[122:123], v[150:151]
	v_pk_mul_f32 v[152:153], v[116:117], v[152:153]
	v_pk_mul_f32 v[154:155], v[118:119], v[154:155]
	v_exp_f32_e32 v140, v140
	v_exp_f32_e32 v141, v141
	v_exp_f32_e32 v142, v142
	v_exp_f32_e32 v143, v143
	v_exp_f32_e32 v144, v144
	v_exp_f32_e32 v145, v145
	v_exp_f32_e32 v146, v146
	v_exp_f32_e32 v147, v147
	v_exp_f32_e32 v148, v148
	v_exp_f32_e32 v149, v149
	v_exp_f32_e32 v150, v150
	v_exp_f32_e32 v151, v151
	v_exp_f32_e32 v152, v152
	v_exp_f32_e32 v153, v153
	v_exp_f32_e32 v154, v154
	v_exp_f32_e32 v155, v155
	v_pk_fma_f32 v[140:141], v[140:141], v[208:209], v[208:209] op_sel:[0,0,0] op_sel_hi:[1,0,0]
	v_pk_fma_f32 v[142:143], v[142:143], v[208:209], v[208:209] op_sel:[0,0,0] op_sel_hi:[1,0,0]
	v_pk_fma_f32 v[144:145], v[144:145], v[208:209], v[208:209] op_sel:[0,0,0] op_sel_hi:[1,0,0]
	v_pk_fma_f32 v[146:147], v[146:147], v[208:209], v[208:209] op_sel:[0,0,0] op_sel_hi:[1,0,0]
	v_pk_fma_f32 v[148:149], v[148:149], v[208:209], v[208:209] op_sel:[0,0,0] op_sel_hi:[1,0,0]
	v_pk_fma_f32 v[150:151], v[150:151], v[208:209], v[208:209] op_sel:[0,0,0] op_sel_hi:[1,0,0]
	v_pk_fma_f32 v[152:153], v[152:153], v[208:209], v[208:209] op_sel:[0,0,0] op_sel_hi:[1,0,0]
	v_pk_fma_f32 v[154:155], v[154:155], v[208:209], v[208:209] op_sel:[0,0,0] op_sel_hi:[1,0,0]
	v_rcp_f32_e32 v140, v140
	v_rcp_f32_e32 v141, v141
	v_rcp_f32_e32 v142, v142
	v_rcp_f32_e32 v143, v143
	v_rcp_f32_e32 v144, v144
	v_rcp_f32_e32 v145, v145
	v_rcp_f32_e32 v146, v146
	v_rcp_f32_e32 v147, v147
	v_rcp_f32_e32 v148, v148
	v_rcp_f32_e32 v149, v149
	v_rcp_f32_e32 v150, v150
	v_rcp_f32_e32 v151, v151
	v_rcp_f32_e32 v152, v152
	v_rcp_f32_e32 v153, v153
	v_rcp_f32_e32 v154, v154
	v_rcp_f32_e32 v155, v155
	v_pk_mul_f32 v[128:129], v[128:129], v[140:141]
	v_pk_mul_f32 v[130:131], v[130:131], v[142:143]
	v_pk_mul_f32 v[124:125], v[124:125], v[144:145]
	v_pk_mul_f32 v[126:127], v[126:127], v[146:147]
	v_pk_mul_f32 v[120:121], v[120:121], v[148:149]
	v_pk_mul_f32 v[122:123], v[122:123], v[150:151]
	v_pk_mul_f32 v[116:117], v[116:117], v[152:153]
	v_pk_mul_f32 v[118:119], v[118:119], v[154:155]
	v_cvt_pk_bf16_f32 v128, v128, v129
	v_cvt_pk_bf16_f32 v129, v130, v131
	v_cvt_pk_bf16_f32 v130, v124, v125
	v_cvt_pk_bf16_f32 v131, v126, v127
	global_store_dwordx4 v134, v[128:131], s[0:1]
	v_cvt_pk_bf16_f32 v120, v120, v121
	v_cvt_pk_bf16_f32 v121, v122, v123
	v_cvt_pk_bf16_f32 v122, v116, v117
	v_cvt_pk_bf16_f32 v123, v118, v119
	global_store_dwordx4 v134, v[120:123], s[0:1] offset:256
	v_pk_mul_f32 v[140:141], v[112:113], v[112:113]
	v_pk_mul_f32 v[142:143], v[114:115], v[114:115]
	v_pk_mul_f32 v[144:145], v[108:109], v[108:109]
	v_pk_mul_f32 v[146:147], v[110:111], v[110:111]
	v_pk_mul_f32 v[148:149], v[104:105], v[104:105]
	v_pk_mul_f32 v[150:151], v[106:107], v[106:107]
	v_pk_mul_f32 v[152:153], v[100:101], v[100:101]
	v_pk_mul_f32 v[154:155], v[102:103], v[102:103]
	v_pk_fma_f32 v[140:141], v[140:141], v[190:191], v[182:183] op_sel:[0,1,1] op_sel_hi:[1,1,1]
; __device__ __forceinline__ u32x4 pack8(const f32x4 a, const f32x4 b) { u32x4 w; w.x = cvt_pk_bf16(a[0], a[1]); w.y = cvt_pk_bf16(a[2], a[3]); w.z = cvt_pk_bf16(b[0], b[1]); w.w = cvt_pk_bf16(b[2], b[3]); return w; }
;     ...
;             for (int bj = 0; bj < 2; ++bj) { f32x4 v0 = acc[ai][bj][m][0] * rf, v1 = acc[ai][bj][m][1] * rf;
;                 if (act != 0) {
; #pragma unroll
;                     for (int e = 0; e < 4; ++e) { const float x0 = v0[e], x1 = v1[e];
;                         const float r0 = __builtin_amdgcn_rcpf(1.0f + __builtin_amdgcn_exp2f(x0 * (c0 + c1 * x0 * x0))), r1 = __builtin_amdgcn_rcpf(1.0f + __builtin_amdgcn_exp2f(x1 * (c0 + c1 * x1 * x1)));
;                         v0[e] = act == 1 ? x0 * r0 : r0; v1[e] = act == 1 ? x1 * r1 : r1; } }
;                 if (stat) {
; #pragma unroll
;                     for (int e = 0; e < 4; ++e) { ls1 += v0[e] + v1[e]; ls2 += v0[e] * v0[e] + v1[e] * v1[e]; } }
;                 *(u32x4*)(rowp + bj * HALF) = pack8(v0, v1); }
	v_pk_fma_f32 v[142:143], v[142:143], v[190:191], v[182:183] op_sel:[0,1,1] op_sel_hi:[1,1,1]
	v_pk_fma_f32 v[144:145], v[144:145], v[190:191], v[182:183] op_sel:[0,1,1] op_sel_hi:[1,1,1]
	v_pk_fma_f32 v[146:147], v[146:147], v[190:191], v[182:183] op_sel:[0,1,1] op_sel_hi:[1,1,1]
	v_pk_fma_f32 v[148:149], v[148:149], v[190:191], v[182:183] op_sel:[0,1,1] op_sel_hi:[1,1,1]
	v_pk_fma_f32 v[150:151], v[150:151], v[190:191], v[182:183] op_sel:[0,1,1] op_sel_hi:[1,1,1]
	v_pk_fma_f32 v[152:153], v[152:153], v[190:191], v[182:183] op_sel:[0,1,1] op_sel_hi:[1,1,1]
	v_pk_fma_f32 v[154:155], v[154:155], v[190:191], v[182:183] op_sel:[0,1,1] op_sel_hi:[1,1,1]
	v_pk_mul_f32 v[140:141], v[112:113], v[140:141]
	v_pk_mul_f32 v[142:143], v[114:115], v[142:143]
	v_pk_mul_f32 v[144:145], v[108:109], v[144:145]
	v_pk_mul_f32 v[146:147], v[110:111], v[146:147]
	v_pk_mul_f32 v[148:149], v[104:105], v[148:149]
	v_pk_mul_f32 v[150:151], v[106:107], v[150:151]
	v_pk_mul_f32 v[152:153], v[100:101], v[152:153]
	v_pk_mul_f32 v[154:155], v[102:103], v[154:155]
	v_exp_f32_e32 v140, v140
	v_exp_f32_e32 v141, v141
	v_exp_f32_e32 v142, v142
	v_exp_f32_e32 v143, v143
	v_exp_f32_e32 v144, v144
	v_exp_f32_e32 v145, v145
	v_exp_f32_e32 v146, v146
	v_exp_f32_e32 v147, v147
	v_exp_f32_e32 v148, v148
	v_exp_f32_e32 v149, v149
	v_exp_f32_e32 v150, v150
	v_exp_f32_e32 v151, v151
	v_exp_f32_e32 v152, v152
	v_exp_f32_e32 v153, v153
	v_exp_f32_e32 v154, v154
	v_exp_f32_e32 v155, v155
	v_pk_fma_f32 v[140:141], v[140:141], v[208:209], v[208:209] op_sel:[0,1,1] op_sel_hi:[1,1,1]
	v_pk_fma_f32 v[142:143], v[142:143], v[208:209], v[208:209] op_sel:[0,1,1] op_sel_hi:[1,1,1]
	v_pk_fma_f32 v[144:145], v[144:145], v[208:209], v[208:209] op_sel:[0,1,1] op_sel_hi:[1,1,1]
	v_pk_fma_f32 v[146:147], v[146:147], v[208:209], v[208:209] op_sel:[0,1,1] op_sel_hi:[1,1,1]
	v_pk_fma_f32 v[148:149], v[148:149], v[208:209], v[208:209] op_sel:[0,1,1] op_sel_hi:[1,1,1]
	v_pk_fma_f32 v[150:151], v[150:151], v[208:209], v[208:209] op_sel:[0,1,1] op_sel_hi:[1,1,1]
	v_pk_fma_f32 v[152:153], v[152:153], v[208:209], v[208:209] op_sel:[0,1,1] op_sel_hi:[1,1,1]
	v_pk_fma_f32 v[154:155], v[154:155], v[208:209], v[208:209] op_sel:[0,1,1] op_sel_hi:[1,1,1]
	v_rcp_f32_e32 v140, v140
	v_rcp_f32_e32 v141, v141
	v_rcp_f32_e32 v142, v142
	v_rcp_f32_e32 v143, v143
	v_rcp_f32_e32 v144, v144
	v_rcp_f32_e32 v145, v145
	v_rcp_f32_e32 v146, v146
	v_rcp_f32_e32 v147, v147
	v_rcp_f32_e32 v148, v148
	v_rcp_f32_e32 v149, v149
	v_rcp_f32_e32 v150, v150
	v_rcp_f32_e32 v151, v151
	v_rcp_f32_e32 v152, v152
	v_rcp_f32_e32 v153, v153
	v_rcp_f32_e32 v154, v154
	v_rcp_f32_e32 v155, v155
	v_pk_mul_f32 v[112:113], v[112:113], v[140:141]
	v_pk_mul_f32 v[114:115], v[114:115], v[142:143]
	v_pk_mul_f32 v[108:109], v[108:109], v[144:145]
	v_pk_mul_f32 v[110:111], v[110:111], v[146:147]
	v_pk_mul_f32 v[104:105], v[104:105], v[148:149]
	v_pk_mul_f32 v[106:107], v[106:107], v[150:151]
	v_pk_mul_f32 v[100:101], v[100:101], v[152:153]
	v_pk_mul_f32 v[102:103], v[102:103], v[154:155]
	v_add_u32_e32 v134, 0x4000, v134
	v_cvt_pk_bf16_f32 v112, v112, v113
	v_cvt_pk_bf16_f32 v113, v114, v115
	v_cvt_pk_bf16_f32 v114, v108, v109
	v_cvt_pk_bf16_f32 v115, v110, v111
	global_store_dwordx4 v134, v[112:115], s[0:1]
	v_cvt_pk_bf16_f32 v104, v104, v105
	v_cvt_pk_bf16_f32 v105, v106, v107
	v_cvt_pk_bf16_f32 v106, v100, v101
	v_cvt_pk_bf16_f32 v107, v102, v103
	global_store_dwordx4 v134, v[104:107], s[0:1] offset:256
	v_pk_mul_f32 v[140:141], v[96:97], v[96:97]
	v_pk_mul_f32 v[142:143], v[98:99], v[98:99]
	v_pk_mul_f32 v[144:145], v[92:93], v[92:93]
	v_pk_mul_f32 v[146:147], v[94:95], v[94:95]
	v_pk_mul_f32 v[148:149], v[88:89], v[88:89]
	v_pk_mul_f32 v[150:151], v[90:91], v[90:91]
	v_pk_mul_f32 v[152:153], v[84:85], v[84:85]
	v_pk_mul_f32 v[154:155], v[86:87], v[86:87]
	v_pk_fma_f32 v[140:141], v[140:141], v[192:193], v[184:185] op_sel:[0,0,0] op_sel_hi:[1,0,0]
	v_pk_fma_f32 v[142:143], v[142:143], v[192:193], v[184:185] op_sel:[0,0,0] op_sel_hi:[1,0,0]
	v_pk_fma_f32 v[144:145], v[144:145], v[192:193], v[184:185] op_sel:[0,0,0] op_sel_hi:[1,0,0]
	v_pk_fma_f32 v[146:147], v[146:147], v[192:193], v[184:185] op_sel:[0,0,0] op_sel_hi:[1,0,0]
	v_pk_fma_f32 v[148:149], v[148:149], v[192:193], v[184:185] op_sel:[0,0,0] op_sel_hi:[1,0,0]
	v_pk_fma_f32 v[150:151], v[150:151], v[192:193], v[184:185] op_sel:[0,0,0] op_sel_hi:[1,0,0]
	v_pk_fma_f32 v[152:153], v[152:153], v[192:193], v[184:185] op_sel:[0,0,0] op_sel_hi:[1,0,0]
	v_pk_fma_f32 v[154:155], v[154:155], v[192:193], v[184:185] op_sel:[0,0,0] op_sel_hi:[1,0,0]
	v_pk_mul_f32 v[140:141], v[96:97], v[140:141]
	v_pk_mul_f32 v[142:143], v[98:99], v[142:143]
	v_pk_mul_f32 v[144:145], v[92:93], v[144:145]
	v_pk_mul_f32 v[146:147], v[94:95], v[146:147]
	v_pk_mul_f32 v[148:149], v[88:89], v[148:149]
	v_pk_mul_f32 v[150:151], v[90:91], v[150:151]
	v_pk_mul_f32 v[152:153], v[84:85], v[152:153]
	v_pk_mul_f32 v[154:155], v[86:87], v[154:155]
	v_exp_f32_e32 v140, v140
	v_exp_f32_e32 v141, v141
	v_exp_f32_e32 v142, v142
	v_exp_f32_e32 v143, v143
	v_exp_f32_e32 v144, v144
	v_exp_f32_e32 v145, v145
	v_exp_f32_e32 v146, v146
	v_exp_f32_e32 v147, v147
	v_exp_f32_e32 v148, v148
	v_exp_f32_e32 v149, v149
	v_exp_f32_e32 v150, v150
	v_exp_f32_e32 v151, v151
	v_exp_f32_e32 v152, v152
	v_exp_f32_e32 v153, v153
	v_exp_f32_e32 v154, v154
	v_exp_f32_e32 v155, v155
	v_pk_fma_f32 v[140:141], v[140:141], v[210:211], v[210:211] op_sel:[0,0,0] op_sel_hi:[1,0,0]
	v_pk_fma_f32 v[142:143], v[142:143], v[210:211], v[210:211] op_sel:[0,0,0] op_sel_hi:[1,0,0]
	v_pk_fma_f32 v[144:145], v[144:145], v[210:211], v[210:211] op_sel:[0,0,0] op_sel_hi:[1,0,0]
; __device__ __forceinline__ u32x4 pack8(const f32x4 a, const f32x4 b) { u32x4 w; w.x = cvt_pk_bf16(a[0], a[1]); w.y = cvt_pk_bf16(a[2], a[3]); w.z = cvt_pk_bf16(b[0], b[1]); w.w = cvt_pk_bf16(b[2], b[3]); return w; }
;     ...
;             for (int bj = 0; bj < 2; ++bj) { f32x4 v0 = acc[ai][bj][m][0] * rf, v1 = acc[ai][bj][m][1] * rf;
;                 if (act != 0) {
; #pragma unroll
;                     for (int e = 0; e < 4; ++e) { const float x0 = v0[e], x1 = v1[e];
;                         const float r0 = __builtin_amdgcn_rcpf(1.0f + __builtin_amdgcn_exp2f(x0 * (c0 + c1 * x0 * x0))), r1 = __builtin_amdgcn_rcpf(1.0f + __builtin_amdgcn_exp2f(x1 * (c0 + c1 * x1 * x1)));
;                         v0[e] = act == 1 ? x0 * r0 : r0; v1[e] = act == 1 ? x1 * r1 : r1; } }
;                 if (stat) {
; #pragma unroll
;                     for (int e = 0; e < 4; ++e) { ls1 += v0[e] + v1[e]; ls2 += v0[e] * v0[e] + v1[e] * v1[e]; } }
;                 *(u32x4*)(rowp + bj * HALF) = pack8(v0, v1); }
	v_pk_fma_f32 v[146:147], v[146:147], v[210:211], v[210:211] op_sel:[0,0,0] op_sel_hi:[1,0,0]
	v_pk_fma_f32 v[148:149], v[148:149], v[210:211], v[210:211] op_sel:[0,0,0] op_sel_hi:[1,0,0]
	v_pk_fma_f32 v[150:151], v[150:151], v[210:211], v[210:211] op_sel:[0,0,0] op_sel_hi:[1,0,0]
	v_pk_fma_f32 v[152:153], v[152:153], v[210:211], v[210:211] op_sel:[0,0,0] op_sel_hi:[1,0,0]
	v_pk_fma_f32 v[154:155], v[154:155], v[210:211], v[210:211] op_sel:[0,0,0] op_sel_hi:[1,0,0]
	v_rcp_f32_e32 v140, v140
	v_rcp_f32_e32 v141, v141
	v_rcp_f32_e32 v142, v142
	v_rcp_f32_e32 v143, v143
	v_rcp_f32_e32 v144, v144
	v_rcp_f32_e32 v145, v145
	v_rcp_f32_e32 v146, v146
	v_rcp_f32_e32 v147, v147
	v_rcp_f32_e32 v148, v148
	v_rcp_f32_e32 v149, v149
	v_rcp_f32_e32 v150, v150
	v_rcp_f32_e32 v151, v151
	v_rcp_f32_e32 v152, v152
	v_rcp_f32_e32 v153, v153
	v_rcp_f32_e32 v154, v154
	v_rcp_f32_e32 v155, v155
	v_pk_mul_f32 v[96:97], v[96:97], v[140:141]
	v_pk_mul_f32 v[98:99], v[98:99], v[142:143]
	v_pk_mul_f32 v[92:93], v[92:93], v[144:145]
	v_pk_mul_f32 v[94:95], v[94:95], v[146:147]
	v_pk_mul_f32 v[88:89], v[88:89], v[148:149]
	v_pk_mul_f32 v[90:91], v[90:91], v[150:151]
	v_pk_mul_f32 v[84:85], v[84:85], v[152:153]
	v_pk_mul_f32 v[86:87], v[86:87], v[154:155]
	v_add_u32_e32 v134, 0x4000, v134
	v_cvt_pk_bf16_f32 v96, v96, v97
	v_cvt_pk_bf16_f32 v97, v98, v99
	v_cvt_pk_bf16_f32 v98, v92, v93
	v_cvt_pk_bf16_f32 v99, v94, v95
	global_store_dwordx4 v134, v[96:99], s[0:1]
	v_cvt_pk_bf16_f32 v88, v88, v89
	v_cvt_pk_bf16_f32 v89, v90, v91
	v_cvt_pk_bf16_f32 v90, v84, v85
	v_cvt_pk_bf16_f32 v91, v86, v87
	global_store_dwordx4 v134, v[88:91], s[0:1] offset:256
	v_pk_mul_f32 v[140:141], v[80:81], v[80:81]
	v_pk_mul_f32 v[142:143], v[82:83], v[82:83]
	v_pk_mul_f32 v[144:145], v[76:77], v[76:77]
	v_pk_mul_f32 v[146:147], v[78:79], v[78:79]
	v_pk_mul_f32 v[148:149], v[72:73], v[72:73]
	v_pk_mul_f32 v[150:151], v[74:75], v[74:75]
	v_pk_mul_f32 v[152:153], v[68:69], v[68:69]
	v_pk_mul_f32 v[154:155], v[70:71], v[70:71]
	v_pk_fma_f32 v[140:141], v[140:141], v[192:193], v[184:185] op_sel:[0,1,1] op_sel_hi:[1,1,1]
	v_pk_fma_f32 v[142:143], v[142:143], v[192:193], v[184:185] op_sel:[0,1,1] op_sel_hi:[1,1,1]
	v_pk_fma_f32 v[144:145], v[144:145], v[192:193], v[184:185] op_sel:[0,1,1] op_sel_hi:[1,1,1]
	v_pk_fma_f32 v[146:147], v[146:147], v[192:193], v[184:185] op_sel:[0,1,1] op_sel_hi:[1,1,1]
	v_pk_fma_f32 v[148:149], v[148:149], v[192:193], v[184:185] op_sel:[0,1,1] op_sel_hi:[1,1,1]
	v_pk_fma_f32 v[150:151], v[150:151], v[192:193], v[184:185] op_sel:[0,1,1] op_sel_hi:[1,1,1]
	v_pk_fma_f32 v[152:153], v[152:153], v[192:193], v[184:185] op_sel:[0,1,1] op_sel_hi:[1,1,1]
	v_pk_fma_f32 v[154:155], v[154:155], v[192:193], v[184:185] op_sel:[0,1,1] op_sel_hi:[1,1,1]
	v_pk_mul_f32 v[140:141], v[80:81], v[140:141]
	v_pk_mul_f32 v[142:143], v[82:83], v[142:143]
	v_pk_mul_f32 v[144:145], v[76:77], v[144:145]
	v_pk_mul_f32 v[146:147], v[78:79], v[146:147]
	v_pk_mul_f32 v[148:149], v[72:73], v[148:149]
	v_pk_mul_f32 v[150:151], v[74:75], v[150:151]
	v_pk_mul_f32 v[152:153], v[68:69], v[152:153]
	v_pk_mul_f32 v[154:155], v[70:71], v[154:155]
	v_exp_f32_e32 v140, v140
	v_exp_f32_e32 v141, v141
	v_exp_f32_e32 v142, v142
	v_exp_f32_e32 v143, v143
	v_exp_f32_e32 v144, v144
	v_exp_f32_e32 v145, v145
	v_exp_f32_e32 v146, v146
	v_exp_f32_e32 v147, v147
	v_exp_f32_e32 v148, v148
	v_exp_f32_e32 v149, v149
	v_exp_f32_e32 v150, v150
	v_exp_f32_e32 v151, v151
	v_exp_f32_e32 v152, v152
	v_exp_f32_e32 v153, v153
	v_exp_f32_e32 v154, v154
	v_exp_f32_e32 v155, v155
	v_pk_fma_f32 v[140:141], v[140:141], v[210:211], v[210:211] op_sel:[0,1,1] op_sel_hi:[1,1,1]
	v_pk_fma_f32 v[142:143], v[142:143], v[210:211], v[210:211] op_sel:[0,1,1] op_sel_hi:[1,1,1]
	v_pk_fma_f32 v[144:145], v[144:145], v[210:211], v[210:211] op_sel:[0,1,1] op_sel_hi:[1,1,1]
	v_pk_fma_f32 v[146:147], v[146:147], v[210:211], v[210:211] op_sel:[0,1,1] op_sel_hi:[1,1,1]
	v_pk_fma_f32 v[148:149], v[148:149], v[210:211], v[210:211] op_sel:[0,1,1] op_sel_hi:[1,1,1]
	v_pk_fma_f32 v[150:151], v[150:151], v[210:211], v[210:211] op_sel:[0,1,1] op_sel_hi:[1,1,1]
	v_pk_fma_f32 v[152:153], v[152:153], v[210:211], v[210:211] op_sel:[0,1,1] op_sel_hi:[1,1,1]
	v_pk_fma_f32 v[154:155], v[154:155], v[210:211], v[210:211] op_sel:[0,1,1] op_sel_hi:[1,1,1]
	v_rcp_f32_e32 v140, v140
	v_rcp_f32_e32 v141, v141
	v_rcp_f32_e32 v142, v142
	v_rcp_f32_e32 v143, v143
	v_rcp_f32_e32 v144, v144
	v_rcp_f32_e32 v145, v145
	v_rcp_f32_e32 v146, v146
	v_rcp_f32_e32 v147, v147
	v_rcp_f32_e32 v148, v148
	v_rcp_f32_e32 v149, v149
	v_rcp_f32_e32 v150, v150
	v_rcp_f32_e32 v151, v151
	v_rcp_f32_e32 v152, v152
	v_rcp_f32_e32 v153, v153
	v_rcp_f32_e32 v154, v154
	v_rcp_f32_e32 v155, v155
	v_pk_mul_f32 v[80:81], v[80:81], v[140:141]
	v_pk_mul_f32 v[82:83], v[82:83], v[142:143]
	v_pk_mul_f32 v[76:77], v[76:77], v[144:145]
	v_pk_mul_f32 v[78:79], v[78:79], v[146:147]
	v_pk_mul_f32 v[72:73], v[72:73], v[148:149]
	v_pk_mul_f32 v[74:75], v[74:75], v[150:151]
	v_pk_mul_f32 v[68:69], v[68:69], v[152:153]
	v_pk_mul_f32 v[70:71], v[70:71], v[154:155]
	v_add_u32_e32 v134, 0x4000, v134
	v_cvt_pk_bf16_f32 v80, v80, v81
	v_cvt_pk_bf16_f32 v81, v82, v83
	v_cvt_pk_bf16_f32 v82, v76, v77
	v_cvt_pk_bf16_f32 v83, v78, v79
	global_store_dwordx4 v134, v[80:83], s[0:1]
	v_cvt_pk_bf16_f32 v72, v72, v73
	v_cvt_pk_bf16_f32 v73, v74, v75
	v_cvt_pk_bf16_f32 v74, v68, v69
	v_cvt_pk_bf16_f32 v75, v70, v71
	global_store_dwordx4 v134, v[72:75], s[0:1] offset:256
	v_pk_mul_f32 v[140:141], v[64:65], v[64:65]
	v_pk_mul_f32 v[142:143], v[66:67], v[66:67]
	v_pk_mul_f32 v[144:145], v[60:61], v[60:61]
	v_pk_mul_f32 v[146:147], v[62:63], v[62:63]
; __device__ __forceinline__ u32x4 pack8(const f32x4 a, const f32x4 b) { u32x4 w; w.x = cvt_pk_bf16(a[0], a[1]); w.y = cvt_pk_bf16(a[2], a[3]); w.z = cvt_pk_bf16(b[0], b[1]); w.w = cvt_pk_bf16(b[2], b[3]); return w; }
;     ...
;             for (int bj = 0; bj < 2; ++bj) { f32x4 v0 = acc[ai][bj][m][0] * rf, v1 = acc[ai][bj][m][1] * rf;
;                 if (act != 0) {
; #pragma unroll
;                     for (int e = 0; e < 4; ++e) { const float x0 = v0[e], x1 = v1[e];
;                         const float r0 = __builtin_amdgcn_rcpf(1.0f + __builtin_amdgcn_exp2f(x0 * (c0 + c1 * x0 * x0))), r1 = __builtin_amdgcn_rcpf(1.0f + __builtin_amdgcn_exp2f(x1 * (c0 + c1 * x1 * x1)));
;                         v0[e] = act == 1 ? x0 * r0 : r0; v1[e] = act == 1 ? x1 * r1 : r1; } }
;                 if (stat) {
; #pragma unroll
;                     for (int e = 0; e < 4; ++e) { ls1 += v0[e] + v1[e]; ls2 += v0[e] * v0[e] + v1[e] * v1[e]; } }
;                 *(u32x4*)(rowp + bj * HALF) = pack8(v0, v1); }
	v_pk_mul_f32 v[148:149], v[56:57], v[56:57]
	v_pk_mul_f32 v[150:151], v[58:59], v[58:59]
	v_pk_mul_f32 v[152:153], v[52:53], v[52:53]
	v_pk_mul_f32 v[154:155], v[54:55], v[54:55]
	v_pk_fma_f32 v[140:141], v[140:141], v[194:195], v[186:187] op_sel:[0,0,0] op_sel_hi:[1,0,0]
	v_pk_fma_f32 v[142:143], v[142:143], v[194:195], v[186:187] op_sel:[0,0,0] op_sel_hi:[1,0,0]
	v_pk_fma_f32 v[144:145], v[144:145], v[194:195], v[186:187] op_sel:[0,0,0] op_sel_hi:[1,0,0]
	v_pk_fma_f32 v[146:147], v[146:147], v[194:195], v[186:187] op_sel:[0,0,0] op_sel_hi:[1,0,0]
	v_pk_fma_f32 v[148:149], v[148:149], v[194:195], v[186:187] op_sel:[0,0,0] op_sel_hi:[1,0,0]
	v_pk_fma_f32 v[150:151], v[150:151], v[194:195], v[186:187] op_sel:[0,0,0] op_sel_hi:[1,0,0]
	v_pk_fma_f32 v[152:153], v[152:153], v[194:195], v[186:187] op_sel:[0,0,0] op_sel_hi:[1,0,0]
	v_pk_fma_f32 v[154:155], v[154:155], v[194:195], v[186:187] op_sel:[0,0,0] op_sel_hi:[1,0,0]
	v_pk_mul_f32 v[140:141], v[64:65], v[140:141]
	v_pk_mul_f32 v[142:143], v[66:67], v[142:143]
	v_pk_mul_f32 v[144:145], v[60:61], v[144:145]
	v_pk_mul_f32 v[146:147], v[62:63], v[146:147]
	v_pk_mul_f32 v[148:149], v[56:57], v[148:149]
	v_pk_mul_f32 v[150:151], v[58:59], v[150:151]
	v_pk_mul_f32 v[152:153], v[52:53], v[152:153]
	v_pk_mul_f32 v[154:155], v[54:55], v[154:155]
	v_exp_f32_e32 v140, v140
	v_exp_f32_e32 v141, v141
	v_exp_f32_e32 v142, v142
	v_exp_f32_e32 v143, v143
	v_exp_f32_e32 v144, v144
	v_exp_f32_e32 v145, v145
	v_exp_f32_e32 v146, v146
	v_exp_f32_e32 v147, v147
	v_exp_f32_e32 v148, v148
	v_exp_f32_e32 v149, v149
	v_exp_f32_e32 v150, v150
	v_exp_f32_e32 v151, v151
	v_exp_f32_e32 v152, v152
	v_exp_f32_e32 v153, v153
	v_exp_f32_e32 v154, v154
	v_exp_f32_e32 v155, v155
	v_pk_fma_f32 v[140:141], v[140:141], v[212:213], v[212:213] op_sel:[0,0,0] op_sel_hi:[1,0,0]
	v_pk_fma_f32 v[142:143], v[142:143], v[212:213], v[212:213] op_sel:[0,0,0] op_sel_hi:[1,0,0]
	v_pk_fma_f32 v[144:145], v[144:145], v[212:213], v[212:213] op_sel:[0,0,0] op_sel_hi:[1,0,0]
	v_pk_fma_f32 v[146:147], v[146:147], v[212:213], v[212:213] op_sel:[0,0,0] op_sel_hi:[1,0,0]
	v_pk_fma_f32 v[148:149], v[148:149], v[212:213], v[212:213] op_sel:[0,0,0] op_sel_hi:[1,0,0]
	v_pk_fma_f32 v[150:151], v[150:151], v[212:213], v[212:213] op_sel:[0,0,0] op_sel_hi:[1,0,0]
	v_pk_fma_f32 v[152:153], v[152:153], v[212:213], v[212:213] op_sel:[0,0,0] op_sel_hi:[1,0,0]
	v_pk_fma_f32 v[154:155], v[154:155], v[212:213], v[212:213] op_sel:[0,0,0] op_sel_hi:[1,0,0]
	v_rcp_f32_e32 v140, v140
	v_rcp_f32_e32 v141, v141
	v_rcp_f32_e32 v142, v142
	v_rcp_f32_e32 v143, v143
	v_rcp_f32_e32 v144, v144
	v_rcp_f32_e32 v145, v145
	v_rcp_f32_e32 v146, v146
	v_rcp_f32_e32 v147, v147
	v_rcp_f32_e32 v148, v148
	v_rcp_f32_e32 v149, v149
	v_rcp_f32_e32 v150, v150
	v_rcp_f32_e32 v151, v151
	v_rcp_f32_e32 v152, v152
	v_rcp_f32_e32 v153, v153
	v_rcp_f32_e32 v154, v154
	v_rcp_f32_e32 v155, v155
	v_pk_mul_f32 v[64:65], v[64:65], v[140:141]
	v_pk_mul_f32 v[66:67], v[66:67], v[142:143]
	v_pk_mul_f32 v[60:61], v[60:61], v[144:145]
	v_pk_mul_f32 v[62:63], v[62:63], v[146:147]
	v_pk_mul_f32 v[56:57], v[56:57], v[148:149]
	v_pk_mul_f32 v[58:59], v[58:59], v[150:151]
	v_pk_mul_f32 v[52:53], v[52:53], v[152:153]
	v_pk_mul_f32 v[54:55], v[54:55], v[154:155]
	v_add_u32_e32 v134, 0x14000, v134
	v_cvt_pk_bf16_f32 v64, v64, v65
	v_cvt_pk_bf16_f32 v65, v66, v67
	v_cvt_pk_bf16_f32 v66, v60, v61
	v_cvt_pk_bf16_f32 v67, v62, v63
	global_store_dwordx4 v134, v[64:67], s[0:1]
	v_cvt_pk_bf16_f32 v56, v56, v57
	v_cvt_pk_bf16_f32 v57, v58, v59
	v_cvt_pk_bf16_f32 v58, v52, v53
	v_cvt_pk_bf16_f32 v59, v54, v55
	global_store_dwordx4 v134, v[56:59], s[0:1] offset:256
	v_pk_mul_f32 v[140:141], v[48:49], v[48:49]
	v_pk_mul_f32 v[142:143], v[50:51], v[50:51]
	v_pk_mul_f32 v[144:145], v[44:45], v[44:45]
	v_pk_mul_f32 v[146:147], v[46:47], v[46:47]
	v_pk_mul_f32 v[148:149], v[40:41], v[40:41]
	v_pk_mul_f32 v[150:151], v[42:43], v[42:43]
	v_pk_mul_f32 v[152:153], v[36:37], v[36:37]
	v_pk_mul_f32 v[154:155], v[38:39], v[38:39]
	v_pk_fma_f32 v[140:141], v[140:141], v[194:195], v[186:187] op_sel:[0,1,1] op_sel_hi:[1,1,1]
	v_pk_fma_f32 v[142:143], v[142:143], v[194:195], v[186:187] op_sel:[0,1,1] op_sel_hi:[1,1,1]
	v_pk_fma_f32 v[144:145], v[144:145], v[194:195], v[186:187] op_sel:[0,1,1] op_sel_hi:[1,1,1]
	v_pk_fma_f32 v[146:147], v[146:147], v[194:195], v[186:187] op_sel:[0,1,1] op_sel_hi:[1,1,1]
	v_pk_fma_f32 v[148:149], v[148:149], v[194:195], v[186:187] op_sel:[0,1,1] op_sel_hi:[1,1,1]
	v_pk_fma_f32 v[150:151], v[150:151], v[194:195], v[186:187] op_sel:[0,1,1] op_sel_hi:[1,1,1]
	v_pk_fma_f32 v[152:153], v[152:153], v[194:195], v[186:187] op_sel:[0,1,1] op_sel_hi:[1,1,1]
	v_pk_fma_f32 v[154:155], v[154:155], v[194:195], v[186:187] op_sel:[0,1,1] op_sel_hi:[1,1,1]
	v_pk_mul_f32 v[140:141], v[48:49], v[140:141]
	v_pk_mul_f32 v[142:143], v[50:51], v[142:143]
	v_pk_mul_f32 v[144:145], v[44:45], v[144:145]
	v_pk_mul_f32 v[146:147], v[46:47], v[146:147]
	v_pk_mul_f32 v[148:149], v[40:41], v[148:149]
	v_pk_mul_f32 v[150:151], v[42:43], v[150:151]
	v_pk_mul_f32 v[152:153], v[36:37], v[152:153]
	v_pk_mul_f32 v[154:155], v[38:39], v[154:155]
	v_exp_f32_e32 v140, v140
	v_exp_f32_e32 v141, v141
	v_exp_f32_e32 v142, v142
	v_exp_f32_e32 v143, v143
	v_exp_f32_e32 v144, v144
	v_exp_f32_e32 v145, v145
	v_exp_f32_e32 v146, v146
	v_exp_f32_e32 v147, v147
	v_exp_f32_e32 v148, v148
	v_exp_f32_e32 v149, v149
	v_exp_f32_e32 v150, v150
	v_exp_f32_e32 v151, v151
	v_exp_f32_e32 v152, v152
	v_exp_f32_e32 v153, v153
	v_exp_f32_e32 v154, v154
	v_exp_f32_e32 v155, v155
	v_pk_fma_f32 v[140:141], v[140:141], v[212:213], v[212:213] op_sel:[0,1,1] op_sel_hi:[1,1,1]
; __device__ __forceinline__ u32x4 pack8(const f32x4 a, const f32x4 b) { u32x4 w; w.x = cvt_pk_bf16(a[0], a[1]); w.y = cvt_pk_bf16(a[2], a[3]); w.z = cvt_pk_bf16(b[0], b[1]); w.w = cvt_pk_bf16(b[2], b[3]); return w; }
;     ...
;             for (int bj = 0; bj < 2; ++bj) { f32x4 v0 = acc[ai][bj][m][0] * rf, v1 = acc[ai][bj][m][1] * rf;
;                 if (act != 0) {
; #pragma unroll
;                     for (int e = 0; e < 4; ++e) { const float x0 = v0[e], x1 = v1[e];
;                         const float r0 = __builtin_amdgcn_rcpf(1.0f + __builtin_amdgcn_exp2f(x0 * (c0 + c1 * x0 * x0))), r1 = __builtin_amdgcn_rcpf(1.0f + __builtin_amdgcn_exp2f(x1 * (c0 + c1 * x1 * x1)));
;                         v0[e] = act == 1 ? x0 * r0 : r0; v1[e] = act == 1 ? x1 * r1 : r1; } }
;                 if (stat) {
; #pragma unroll
;                     for (int e = 0; e < 4; ++e) { ls1 += v0[e] + v1[e]; ls2 += v0[e] * v0[e] + v1[e] * v1[e]; } }
;                 *(u32x4*)(rowp + bj * HALF) = pack8(v0, v1); }
	v_pk_fma_f32 v[142:143], v[142:143], v[212:213], v[212:213] op_sel:[0,1,1] op_sel_hi:[1,1,1]
	v_pk_fma_f32 v[144:145], v[144:145], v[212:213], v[212:213] op_sel:[0,1,1] op_sel_hi:[1,1,1]
	v_pk_fma_f32 v[146:147], v[146:147], v[212:213], v[212:213] op_sel:[0,1,1] op_sel_hi:[1,1,1]
	v_pk_fma_f32 v[148:149], v[148:149], v[212:213], v[212:213] op_sel:[0,1,1] op_sel_hi:[1,1,1]
	v_pk_fma_f32 v[150:151], v[150:151], v[212:213], v[212:213] op_sel:[0,1,1] op_sel_hi:[1,1,1]
	v_pk_fma_f32 v[152:153], v[152:153], v[212:213], v[212:213] op_sel:[0,1,1] op_sel_hi:[1,1,1]
	v_pk_fma_f32 v[154:155], v[154:155], v[212:213], v[212:213] op_sel:[0,1,1] op_sel_hi:[1,1,1]
	v_rcp_f32_e32 v140, v140
	v_rcp_f32_e32 v141, v141
	v_rcp_f32_e32 v142, v142
	v_rcp_f32_e32 v143, v143
	v_rcp_f32_e32 v144, v144
	v_rcp_f32_e32 v145, v145
	v_rcp_f32_e32 v146, v146
	v_rcp_f32_e32 v147, v147
	v_rcp_f32_e32 v148, v148
	v_rcp_f32_e32 v149, v149
	v_rcp_f32_e32 v150, v150
	v_rcp_f32_e32 v151, v151
	v_rcp_f32_e32 v152, v152
	v_rcp_f32_e32 v153, v153
	v_rcp_f32_e32 v154, v154
	v_rcp_f32_e32 v155, v155
	v_pk_mul_f32 v[48:49], v[48:49], v[140:141]
	v_pk_mul_f32 v[50:51], v[50:51], v[142:143]
	v_pk_mul_f32 v[44:45], v[44:45], v[144:145]
	v_pk_mul_f32 v[46:47], v[46:47], v[146:147]
	v_pk_mul_f32 v[40:41], v[40:41], v[148:149]
	v_pk_mul_f32 v[42:43], v[42:43], v[150:151]
	v_pk_mul_f32 v[36:37], v[36:37], v[152:153]
	v_pk_mul_f32 v[38:39], v[38:39], v[154:155]
	v_add_u32_e32 v134, 0x4000, v134
	v_cvt_pk_bf16_f32 v48, v48, v49
	v_cvt_pk_bf16_f32 v49, v50, v51
	v_cvt_pk_bf16_f32 v50, v44, v45
	v_cvt_pk_bf16_f32 v51, v46, v47
	global_store_dwordx4 v134, v[48:51], s[0:1]
	v_cvt_pk_bf16_f32 v40, v40, v41
	v_cvt_pk_bf16_f32 v41, v42, v43
	v_cvt_pk_bf16_f32 v42, v36, v37
	v_cvt_pk_bf16_f32 v43, v38, v39
	global_store_dwordx4 v134, v[40:43], s[0:1] offset:256
	v_pk_mul_f32 v[140:141], v[32:33], v[32:33]
	v_pk_mul_f32 v[142:143], v[34:35], v[34:35]
	v_pk_mul_f32 v[144:145], v[28:29], v[28:29]
	v_pk_mul_f32 v[146:147], v[30:31], v[30:31]
	v_pk_mul_f32 v[148:149], v[24:25], v[24:25]
	v_pk_mul_f32 v[150:151], v[26:27], v[26:27]
	v_pk_mul_f32 v[152:153], v[20:21], v[20:21]
	v_pk_mul_f32 v[154:155], v[22:23], v[22:23]
	v_pk_fma_f32 v[140:141], v[140:141], v[196:197], v[188:189] op_sel:[0,0,0] op_sel_hi:[1,0,0]
	v_pk_fma_f32 v[142:143], v[142:143], v[196:197], v[188:189] op_sel:[0,0,0] op_sel_hi:[1,0,0]
	v_pk_fma_f32 v[144:145], v[144:145], v[196:197], v[188:189] op_sel:[0,0,0] op_sel_hi:[1,0,0]
	v_pk_fma_f32 v[146:147], v[146:147], v[196:197], v[188:189] op_sel:[0,0,0] op_sel_hi:[1,0,0]
	v_pk_fma_f32 v[148:149], v[148:149], v[196:197], v[188:189] op_sel:[0,0,0] op_sel_hi:[1,0,0]
	v_pk_fma_f32 v[150:151], v[150:151], v[196:197], v[188:189] op_sel:[0,0,0] op_sel_hi:[1,0,0]
	v_pk_fma_f32 v[152:153], v[152:153], v[196:197], v[188:189] op_sel:[0,0,0] op_sel_hi:[1,0,0]
	v_pk_fma_f32 v[154:155], v[154:155], v[196:197], v[188:189] op_sel:[0,0,0] op_sel_hi:[1,0,0]
	v_pk_mul_f32 v[140:141], v[32:33], v[140:141]
	v_pk_mul_f32 v[142:143], v[34:35], v[142:143]
	v_pk_mul_f32 v[144:145], v[28:29], v[144:145]
	v_pk_mul_f32 v[146:147], v[30:31], v[146:147]
	v_pk_mul_f32 v[148:149], v[24:25], v[148:149]
	v_pk_mul_f32 v[150:151], v[26:27], v[150:151]
	v_pk_mul_f32 v[152:153], v[20:21], v[152:153]
	v_pk_mul_f32 v[154:155], v[22:23], v[154:155]
	v_exp_f32_e32 v140, v140
	v_exp_f32_e32 v141, v141
	v_exp_f32_e32 v142, v142
	v_exp_f32_e32 v143, v143
	v_exp_f32_e32 v144, v144
	v_exp_f32_e32 v145, v145
	v_exp_f32_e32 v146, v146
	v_exp_f32_e32 v147, v147
	v_exp_f32_e32 v148, v148
	v_exp_f32_e32 v149, v149
	v_exp_f32_e32 v150, v150
	v_exp_f32_e32 v151, v151
	v_exp_f32_e32 v152, v152
	v_exp_f32_e32 v153, v153
	v_exp_f32_e32 v154, v154
	v_exp_f32_e32 v155, v155
	v_pk_fma_f32 v[140:141], v[140:141], v[214:215], v[214:215] op_sel:[0,0,0] op_sel_hi:[1,0,0]
	v_pk_fma_f32 v[142:143], v[142:143], v[214:215], v[214:215] op_sel:[0,0,0] op_sel_hi:[1,0,0]
	v_pk_fma_f32 v[144:145], v[144:145], v[214:215], v[214:215] op_sel:[0,0,0] op_sel_hi:[1,0,0]
	v_pk_fma_f32 v[146:147], v[146:147], v[214:215], v[214:215] op_sel:[0,0,0] op_sel_hi:[1,0,0]
	v_pk_fma_f32 v[148:149], v[148:149], v[214:215], v[214:215] op_sel:[0,0,0] op_sel_hi:[1,0,0]
	v_pk_fma_f32 v[150:151], v[150:151], v[214:215], v[214:215] op_sel:[0,0,0] op_sel_hi:[1,0,0]
	v_pk_fma_f32 v[152:153], v[152:153], v[214:215], v[214:215] op_sel:[0,0,0] op_sel_hi:[1,0,0]
	v_pk_fma_f32 v[154:155], v[154:155], v[214:215], v[214:215] op_sel:[0,0,0] op_sel_hi:[1,0,0]
	v_rcp_f32_e32 v140, v140
	v_rcp_f32_e32 v141, v141
	v_rcp_f32_e32 v142, v142
	v_rcp_f32_e32 v143, v143
	v_rcp_f32_e32 v144, v144
	v_rcp_f32_e32 v145, v145
	v_rcp_f32_e32 v146, v146
	v_rcp_f32_e32 v147, v147
	v_rcp_f32_e32 v148, v148
	v_rcp_f32_e32 v149, v149
	v_rcp_f32_e32 v150, v150
	v_rcp_f32_e32 v151, v151
	v_rcp_f32_e32 v152, v152
	v_rcp_f32_e32 v153, v153
	v_rcp_f32_e32 v154, v154
	v_rcp_f32_e32 v155, v155
	v_pk_mul_f32 v[32:33], v[32:33], v[140:141]
	v_pk_mul_f32 v[34:35], v[34:35], v[142:143]
	v_pk_mul_f32 v[28:29], v[28:29], v[144:145]
	v_pk_mul_f32 v[30:31], v[30:31], v[146:147]
	v_pk_mul_f32 v[24:25], v[24:25], v[148:149]
	v_pk_mul_f32 v[26:27], v[26:27], v[150:151]
	v_pk_mul_f32 v[20:21], v[20:21], v[152:153]
	v_pk_mul_f32 v[22:23], v[22:23], v[154:155]
	v_add_u32_e32 v134, 0x4000, v134
	v_cvt_pk_bf16_f32 v32, v32, v33
	v_cvt_pk_bf16_f32 v33, v34, v35
	v_cvt_pk_bf16_f32 v34, v28, v29
	v_cvt_pk_bf16_f32 v35, v30, v31
	global_store_dwordx4 v134, v[32:35], s[0:1]
	v_cvt_pk_bf16_f32 v24, v24, v25
	v_cvt_pk_bf16_f32 v25, v26, v27
	v_cvt_pk_bf16_f32 v26, v20, v21
	v_cvt_pk_bf16_f32 v27, v22, v23
	global_store_dwordx4 v134, v[24:27], s[0:1] offset:256
; __device__ __forceinline__ u32x4 pack8(const f32x4 a, const f32x4 b) { u32x4 w; w.x = cvt_pk_bf16(a[0], a[1]); w.y = cvt_pk_bf16(a[2], a[3]); w.z = cvt_pk_bf16(b[0], b[1]); w.w = cvt_pk_bf16(b[2], b[3]); return w; }
;     ...
;             for (int bj = 0; bj < 2; ++bj) { f32x4 v0 = acc[ai][bj][m][0] * rf, v1 = acc[ai][bj][m][1] * rf;
;                 if (act != 0) {
; #pragma unroll
;                     for (int e = 0; e < 4; ++e) { const float x0 = v0[e], x1 = v1[e];
;                         const float r0 = __builtin_amdgcn_rcpf(1.0f + __builtin_amdgcn_exp2f(x0 * (c0 + c1 * x0 * x0))), r1 = __builtin_amdgcn_rcpf(1.0f + __builtin_amdgcn_exp2f(x1 * (c0 + c1 * x1 * x1)));
;                         v0[e] = act == 1 ? x0 * r0 : r0; v1[e] = act == 1 ? x1 * r1 : r1; } }
;                 if (stat) {
; #pragma unroll
;                     for (int e = 0; e < 4; ++e) { ls1 += v0[e] + v1[e]; ls2 += v0[e] * v0[e] + v1[e] * v1[e]; } }
;                 *(u32x4*)(rowp + bj * HALF) = pack8(v0, v1); }
	v_pk_mul_f32 v[140:141], v[16:17], v[16:17]
	v_pk_mul_f32 v[142:143], v[18:19], v[18:19]
	v_pk_mul_f32 v[144:145], v[12:13], v[12:13]
	v_pk_mul_f32 v[146:147], v[14:15], v[14:15]
	v_pk_mul_f32 v[148:149], v[8:9], v[8:9]
	v_pk_mul_f32 v[150:151], v[10:11], v[10:11]
	v_pk_mul_f32 v[152:153], v[4:5], v[4:5]
	v_pk_mul_f32 v[154:155], v[6:7], v[6:7]
	v_pk_fma_f32 v[140:141], v[140:141], v[196:197], v[188:189] op_sel:[0,1,1] op_sel_hi:[1,1,1]
	v_pk_fma_f32 v[142:143], v[142:143], v[196:197], v[188:189] op_sel:[0,1,1] op_sel_hi:[1,1,1]
	v_pk_fma_f32 v[144:145], v[144:145], v[196:197], v[188:189] op_sel:[0,1,1] op_sel_hi:[1,1,1]
	v_pk_fma_f32 v[146:147], v[146:147], v[196:197], v[188:189] op_sel:[0,1,1] op_sel_hi:[1,1,1]
	v_pk_fma_f32 v[148:149], v[148:149], v[196:197], v[188:189] op_sel:[0,1,1] op_sel_hi:[1,1,1]
	v_pk_fma_f32 v[150:151], v[150:151], v[196:197], v[188:189] op_sel:[0,1,1] op_sel_hi:[1,1,1]
	v_pk_fma_f32 v[152:153], v[152:153], v[196:197], v[188:189] op_sel:[0,1,1] op_sel_hi:[1,1,1]
	v_pk_fma_f32 v[154:155], v[154:155], v[196:197], v[188:189] op_sel:[0,1,1] op_sel_hi:[1,1,1]
	v_pk_mul_f32 v[140:141], v[16:17], v[140:141]
	v_pk_mul_f32 v[142:143], v[18:19], v[142:143]
	v_pk_mul_f32 v[144:145], v[12:13], v[144:145]
	v_pk_mul_f32 v[146:147], v[14:15], v[146:147]
	v_pk_mul_f32 v[148:149], v[8:9], v[148:149]
	v_pk_mul_f32 v[150:151], v[10:11], v[150:151]
	v_pk_mul_f32 v[152:153], v[4:5], v[152:153]
	v_pk_mul_f32 v[154:155], v[6:7], v[154:155]
	v_exp_f32_e32 v140, v140
	v_exp_f32_e32 v141, v141
	v_exp_f32_e32 v142, v142
	v_exp_f32_e32 v143, v143
	v_exp_f32_e32 v144, v144
	v_exp_f32_e32 v145, v145
	v_exp_f32_e32 v146, v146
	v_exp_f32_e32 v147, v147
	v_exp_f32_e32 v148, v148
	v_exp_f32_e32 v149, v149
	v_exp_f32_e32 v150, v150
	v_exp_f32_e32 v151, v151
	v_exp_f32_e32 v152, v152
	v_exp_f32_e32 v153, v153
	v_exp_f32_e32 v154, v154
	v_exp_f32_e32 v155, v155
	v_pk_fma_f32 v[140:141], v[140:141], v[214:215], v[214:215] op_sel:[0,1,1] op_sel_hi:[1,1,1]
	v_pk_fma_f32 v[142:143], v[142:143], v[214:215], v[214:215] op_sel:[0,1,1] op_sel_hi:[1,1,1]
	v_pk_fma_f32 v[144:145], v[144:145], v[214:215], v[214:215] op_sel:[0,1,1] op_sel_hi:[1,1,1]
	v_pk_fma_f32 v[146:147], v[146:147], v[214:215], v[214:215] op_sel:[0,1,1] op_sel_hi:[1,1,1]
	v_pk_fma_f32 v[148:149], v[148:149], v[214:215], v[214:215] op_sel:[0,1,1] op_sel_hi:[1,1,1]
	v_pk_fma_f32 v[150:151], v[150:151], v[214:215], v[214:215] op_sel:[0,1,1] op_sel_hi:[1,1,1]
	v_pk_fma_f32 v[152:153], v[152:153], v[214:215], v[214:215] op_sel:[0,1,1] op_sel_hi:[1,1,1]
	v_pk_fma_f32 v[154:155], v[154:155], v[214:215], v[214:215] op_sel:[0,1,1] op_sel_hi:[1,1,1]
	v_rcp_f32_e32 v140, v140
	v_rcp_f32_e32 v141, v141
	v_rcp_f32_e32 v142, v142
	v_rcp_f32_e32 v143, v143
	v_rcp_f32_e32 v144, v144
	v_rcp_f32_e32 v145, v145
	v_rcp_f32_e32 v146, v146
	v_rcp_f32_e32 v147, v147
	v_rcp_f32_e32 v148, v148
	v_rcp_f32_e32 v149, v149
	v_rcp_f32_e32 v150, v150
	v_rcp_f32_e32 v151, v151
	v_rcp_f32_e32 v152, v152
	v_rcp_f32_e32 v153, v153
	v_rcp_f32_e32 v154, v154
	v_rcp_f32_e32 v155, v155
	v_pk_mul_f32 v[16:17], v[16:17], v[140:141]
	v_pk_mul_f32 v[18:19], v[18:19], v[142:143]
	v_pk_mul_f32 v[12:13], v[12:13], v[144:145]
	v_pk_mul_f32 v[14:15], v[14:15], v[146:147]
	v_pk_mul_f32 v[8:9], v[8:9], v[148:149]
	v_pk_mul_f32 v[10:11], v[10:11], v[150:151]
	v_pk_mul_f32 v[4:5], v[4:5], v[152:153]
	v_pk_mul_f32 v[6:7], v[6:7], v[154:155]
	v_add_u32_e32 v134, 0x4000, v134
	v_cvt_pk_bf16_f32 v16, v16, v17
	v_cvt_pk_bf16_f32 v17, v18, v19
	v_cvt_pk_bf16_f32 v18, v12, v13
	v_cvt_pk_bf16_f32 v19, v14, v15
	global_store_dwordx4 v134, v[16:19], s[0:1]
	v_cvt_pk_bf16_f32 v8, v8, v9
	v_cvt_pk_bf16_f32 v9, v10, v11
	v_cvt_pk_bf16_f32 v10, v4, v5
	v_cvt_pk_bf16_f32 v11, v6, v7
	global_store_dwordx4 v134, v[8:11], s[0:1] offset:256
	s_branch .Lt8_end
.Lt8_gstat:
	s_waitcnt lgkmcnt(0)
	s_mov_b32 s8, 0xc0135761
	s_mov_b32 s9, 0xbdd2d3e8
	v_pk_mul_f32 v[182:183], v[208:209], s[8:9] op_sel_hi:[1,0]
	v_pk_mul_f32 v[184:185], v[210:211], s[8:9] op_sel_hi:[1,0]
	v_pk_mul_f32 v[186:187], v[212:213], s[8:9] op_sel_hi:[1,0]
	v_pk_mul_f32 v[188:189], v[214:215], s[8:9] op_sel_hi:[1,0]
	v_pk_mul_f32 v[190:191], v[208:209], v[208:209]
	v_pk_mul_f32 v[192:193], v[210:211], v[210:211]
	v_pk_mul_f32 v[194:195], v[212:213], v[212:213]
	v_pk_mul_f32 v[196:197], v[214:215], v[214:215]
	v_pk_mul_f32 v[190:191], v[190:191], v[208:209]
	v_pk_mul_f32 v[192:193], v[192:193], v[210:211]
	v_pk_mul_f32 v[194:195], v[194:195], v[212:213]
	v_pk_mul_f32 v[196:197], v[196:197], v[214:215]
	v_pk_mul_f32 v[190:191], v[190:191], s[8:9] op_sel:[0,1] op_sel_hi:[1,1]
	v_pk_mul_f32 v[192:193], v[192:193], s[8:9] op_sel:[0,1] op_sel_hi:[1,1]
	v_pk_mul_f32 v[194:195], v[194:195], s[8:9] op_sel:[0,1] op_sel_hi:[1,1]
	v_pk_mul_f32 v[196:197], v[196:197], s[8:9] op_sel:[0,1] op_sel_hi:[1,1]
	v_rcp_f32_e32 v208, v208
	v_rcp_f32_e32 v209, v209
	v_rcp_f32_e32 v210, v210
	v_rcp_f32_e32 v211, v211
	v_rcp_f32_e32 v212, v212
	v_rcp_f32_e32 v213, v213
	v_rcp_f32_e32 v214, v214
	v_rcp_f32_e32 v215, v215
	v_pk_mul_f32 v[140:141], v[128:129], v[128:129]
	v_pk_mul_f32 v[142:143], v[130:131], v[130:131]
	v_pk_mul_f32 v[144:145], v[124:125], v[124:125]
	v_pk_mul_f32 v[146:147], v[126:127], v[126:127]
	v_pk_mul_f32 v[148:149], v[120:121], v[120:121]
	v_pk_mul_f32 v[150:151], v[122:123], v[122:123]
	v_pk_mul_f32 v[152:153], v[116:117], v[116:117]
	v_pk_mul_f32 v[154:155], v[118:119], v[118:119]
	v_pk_fma_f32 v[140:141], v[140:141], v[190:191], v[182:183] op_sel:[0,0,0] op_sel_hi:[1,0,0]
	v_pk_fma_f32 v[142:143], v[142:143], v[190:191], v[182:183] op_sel:[0,0,0] op_sel_hi:[1,0,0]
; __device__ __forceinline__ u32x4 pack8(const f32x4 a, const f32x4 b) { u32x4 w; w.x = cvt_pk_bf16(a[0], a[1]); w.y = cvt_pk_bf16(a[2], a[3]); w.z = cvt_pk_bf16(b[0], b[1]); w.w = cvt_pk_bf16(b[2], b[3]); return w; }
;     ...
;             for (int bj = 0; bj < 2; ++bj) { f32x4 v0 = acc[ai][bj][m][0] * rf, v1 = acc[ai][bj][m][1] * rf;
;                 if (act != 0) {
; #pragma unroll
;                     for (int e = 0; e < 4; ++e) { const float x0 = v0[e], x1 = v1[e];
;                         const float r0 = __builtin_amdgcn_rcpf(1.0f + __builtin_amdgcn_exp2f(x0 * (c0 + c1 * x0 * x0))), r1 = __builtin_amdgcn_rcpf(1.0f + __builtin_amdgcn_exp2f(x1 * (c0 + c1 * x1 * x1)));
;                         v0[e] = act == 1 ? x0 * r0 : r0; v1[e] = act == 1 ? x1 * r1 : r1; } }
;                 if (stat) {
; #pragma unroll
;                     for (int e = 0; e < 4; ++e) { ls1 += v0[e] + v1[e]; ls2 += v0[e] * v0[e] + v1[e] * v1[e]; } }
;                 *(u32x4*)(rowp + bj * HALF) = pack8(v0, v1); }
;             if (stat) { ls1 = xor_add<16>(ls1); ls1 = xor_add<32>(ls1); ls2 = xor_add<16>(ls2); ls2 = xor_add<32>(ls2);
;                 if (fq == 0) { f32x2 st2; st2.x = ls1; st2.y = ls2; *(f32x2*)(stat + (size_t)(row0 + ai * HALF + m * 16) * 16) = st2; } }
	v_pk_fma_f32 v[144:145], v[144:145], v[190:191], v[182:183] op_sel:[0,0,0] op_sel_hi:[1,0,0]
	v_pk_fma_f32 v[146:147], v[146:147], v[190:191], v[182:183] op_sel:[0,0,0] op_sel_hi:[1,0,0]
	v_pk_fma_f32 v[148:149], v[148:149], v[190:191], v[182:183] op_sel:[0,0,0] op_sel_hi:[1,0,0]
	v_pk_fma_f32 v[150:151], v[150:151], v[190:191], v[182:183] op_sel:[0,0,0] op_sel_hi:[1,0,0]
	v_pk_fma_f32 v[152:153], v[152:153], v[190:191], v[182:183] op_sel:[0,0,0] op_sel_hi:[1,0,0]
	v_pk_fma_f32 v[154:155], v[154:155], v[190:191], v[182:183] op_sel:[0,0,0] op_sel_hi:[1,0,0]
	v_pk_mul_f32 v[140:141], v[128:129], v[140:141]
	v_pk_mul_f32 v[142:143], v[130:131], v[142:143]
	v_pk_mul_f32 v[144:145], v[124:125], v[144:145]
	v_pk_mul_f32 v[146:147], v[126:127], v[146:147]
	v_pk_mul_f32 v[148:149], v[120:121], v[148:149]
	v_pk_mul_f32 v[150:151], v[122:123], v[150:151]
	v_pk_mul_f32 v[152:153], v[116:117], v[152:153]
	v_pk_mul_f32 v[154:155], v[118:119], v[154:155]
	v_exp_f32_e32 v140, v140
	v_exp_f32_e32 v141, v141
	v_exp_f32_e32 v142, v142
	v_exp_f32_e32 v143, v143
	v_exp_f32_e32 v144, v144
	v_exp_f32_e32 v145, v145
	v_exp_f32_e32 v146, v146
	v_exp_f32_e32 v147, v147
	v_exp_f32_e32 v148, v148
	v_exp_f32_e32 v149, v149
	v_exp_f32_e32 v150, v150
	v_exp_f32_e32 v151, v151
	v_exp_f32_e32 v152, v152
	v_exp_f32_e32 v153, v153
	v_exp_f32_e32 v154, v154
	v_exp_f32_e32 v155, v155
	v_pk_fma_f32 v[140:141], v[140:141], v[208:209], v[208:209] op_sel:[0,0,0] op_sel_hi:[1,0,0]
	v_pk_fma_f32 v[142:143], v[142:143], v[208:209], v[208:209] op_sel:[0,0,0] op_sel_hi:[1,0,0]
	v_pk_fma_f32 v[144:145], v[144:145], v[208:209], v[208:209] op_sel:[0,0,0] op_sel_hi:[1,0,0]
	v_pk_fma_f32 v[146:147], v[146:147], v[208:209], v[208:209] op_sel:[0,0,0] op_sel_hi:[1,0,0]
	v_pk_fma_f32 v[148:149], v[148:149], v[208:209], v[208:209] op_sel:[0,0,0] op_sel_hi:[1,0,0]
	v_pk_fma_f32 v[150:151], v[150:151], v[208:209], v[208:209] op_sel:[0,0,0] op_sel_hi:[1,0,0]
	v_pk_fma_f32 v[152:153], v[152:153], v[208:209], v[208:209] op_sel:[0,0,0] op_sel_hi:[1,0,0]
	v_pk_fma_f32 v[154:155], v[154:155], v[208:209], v[208:209] op_sel:[0,0,0] op_sel_hi:[1,0,0]
	v_rcp_f32_e32 v140, v140
	v_rcp_f32_e32 v141, v141
	v_rcp_f32_e32 v142, v142
	v_rcp_f32_e32 v143, v143
	v_rcp_f32_e32 v144, v144
	v_rcp_f32_e32 v145, v145
	v_rcp_f32_e32 v146, v146
	v_rcp_f32_e32 v147, v147
	v_rcp_f32_e32 v148, v148
	v_rcp_f32_e32 v149, v149
	v_rcp_f32_e32 v150, v150
	v_rcp_f32_e32 v151, v151
	v_rcp_f32_e32 v152, v152
	v_rcp_f32_e32 v153, v153
	v_rcp_f32_e32 v154, v154
	v_rcp_f32_e32 v155, v155
	v_pk_mul_f32 v[128:129], v[128:129], v[140:141]
	v_pk_mul_f32 v[130:131], v[130:131], v[142:143]
	v_pk_mul_f32 v[124:125], v[124:125], v[144:145]
	v_pk_mul_f32 v[126:127], v[126:127], v[146:147]
	v_pk_mul_f32 v[120:121], v[120:121], v[148:149]
	v_pk_mul_f32 v[122:123], v[122:123], v[150:151]
	v_pk_mul_f32 v[116:117], v[116:117], v[152:153]
	v_pk_mul_f32 v[118:119], v[118:119], v[154:155]
	v_pk_add_f32 v[216:217], v[128:129], v[130:131]
	v_pk_mul_f32 v[218:219], v[128:129], v[128:129]
	v_pk_fma_f32 v[218:219], v[130:131], v[130:131], v[218:219]
	v_pk_add_f32 v[216:217], v[216:217], v[124:125]
	v_pk_fma_f32 v[218:219], v[124:125], v[124:125], v[218:219]
	v_pk_add_f32 v[216:217], v[216:217], v[126:127]
	v_pk_fma_f32 v[218:219], v[126:127], v[126:127], v[218:219]
	v_pk_add_f32 v[216:217], v[216:217], v[120:121]
	v_pk_fma_f32 v[218:219], v[120:121], v[120:121], v[218:219]
	v_pk_add_f32 v[216:217], v[216:217], v[122:123]
	v_pk_fma_f32 v[218:219], v[122:123], v[122:123], v[218:219]
	v_pk_add_f32 v[216:217], v[216:217], v[116:117]
	v_pk_fma_f32 v[218:219], v[116:117], v[116:117], v[218:219]
	v_pk_add_f32 v[216:217], v[216:217], v[118:119]
	v_pk_fma_f32 v[218:219], v[118:119], v[118:119], v[218:219]
	v_add_f32_e32 v162, v216, v217
	v_add_f32_e32 v163, v218, v219
	ds_swizzle_b32 v161, v162 offset:swizzle(SWAP,16)
	ds_swizzle_b32 v198, v163 offset:swizzle(SWAP,16)
	v_cvt_pk_bf16_f32 v128, v128, v129
	v_cvt_pk_bf16_f32 v129, v130, v131
	v_cvt_pk_bf16_f32 v130, v124, v125
	v_cvt_pk_bf16_f32 v131, v126, v127
	global_store_dwordx4 v134, v[128:131], s[0:1]
	v_cvt_pk_bf16_f32 v120, v120, v121
	v_cvt_pk_bf16_f32 v121, v122, v123
	v_cvt_pk_bf16_f32 v122, v116, v117
	v_cvt_pk_bf16_f32 v123, v118, v119
	global_store_dwordx4 v134, v[120:123], s[0:1] offset:256
	s_waitcnt lgkmcnt(0)
; __device__ __forceinline__ u32x4 pack8(const f32x4 a, const f32x4 b) { u32x4 w; w.x = cvt_pk_bf16(a[0], a[1]); w.y = cvt_pk_bf16(a[2], a[3]); w.z = cvt_pk_bf16(b[0], b[1]); w.w = cvt_pk_bf16(b[2], b[3]); return w; }
;     ...
;             for (int bj = 0; bj < 2; ++bj) { f32x4 v0 = acc[ai][bj][m][0] * rf, v1 = acc[ai][bj][m][1] * rf;
;                 if (act != 0) {
; #pragma unroll
;                     for (int e = 0; e < 4; ++e) { const float x0 = v0[e], x1 = v1[e];
;                         const float r0 = __builtin_amdgcn_rcpf(1.0f + __builtin_amdgcn_exp2f(x0 * (c0 + c1 * x0 * x0))), r1 = __builtin_amdgcn_rcpf(1.0f + __builtin_amdgcn_exp2f(x1 * (c0 + c1 * x1 * x1)));
;                         v0[e] = act == 1 ? x0 * r0 : r0; v1[e] = act == 1 ? x1 * r1 : r1; } }
;                 if (stat) {
; #pragma unroll
;                     for (int e = 0; e < 4; ++e) { ls1 += v0[e] + v1[e]; ls2 += v0[e] * v0[e] + v1[e] * v1[e]; } }
;                 *(u32x4*)(rowp + bj * HALF) = pack8(v0, v1); }
;             if (stat) { ls1 = xor_add<16>(ls1); ls1 = xor_add<32>(ls1); ls2 = xor_add<16>(ls2); ls2 = xor_add<32>(ls2);
;                 if (fq == 0) { f32x2 st2; st2.x = ls1; st2.y = ls2; *(f32x2*)(stat + (size_t)(row0 + ai * HALF + m * 16) * 16) = st2; } }
	v_add_f32_e32 v162, v162, v161
	v_add_f32_e32 v163, v163, v198
	v_mov_b32_e32 v199, v162
	v_mov_b32_e32 v200, v163
	s_nop 1
	v_permlane32_swap_b32_e32 v162, v199
	v_permlane32_swap_b32_e32 v163, v200
	s_and_b64 exec, exec, s[4:5]
	v_add_f32_e32 v162, v162, v199
	v_add_f32_e32 v163, v163, v200
	global_store_dwordx2 v135, v[162:163], s[38:39]
	s_mov_b64 exec, -1
	v_pk_mul_f32 v[140:141], v[112:113], v[112:113]
	v_pk_mul_f32 v[142:143], v[114:115], v[114:115]
	v_pk_mul_f32 v[144:145], v[108:109], v[108:109]
	v_pk_mul_f32 v[146:147], v[110:111], v[110:111]
	v_pk_mul_f32 v[148:149], v[104:105], v[104:105]
	v_pk_mul_f32 v[150:151], v[106:107], v[106:107]
	v_pk_mul_f32 v[152:153], v[100:101], v[100:101]
	v_pk_mul_f32 v[154:155], v[102:103], v[102:103]
	v_pk_fma_f32 v[140:141], v[140:141], v[190:191], v[182:183] op_sel:[0,1,1] op_sel_hi:[1,1,1]
	v_pk_fma_f32 v[142:143], v[142:143], v[190:191], v[182:183] op_sel:[0,1,1] op_sel_hi:[1,1,1]
	v_pk_fma_f32 v[144:145], v[144:145], v[190:191], v[182:183] op_sel:[0,1,1] op_sel_hi:[1,1,1]
	v_pk_fma_f32 v[146:147], v[146:147], v[190:191], v[182:183] op_sel:[0,1,1] op_sel_hi:[1,1,1]
	v_pk_fma_f32 v[148:149], v[148:149], v[190:191], v[182:183] op_sel:[0,1,1] op_sel_hi:[1,1,1]
	v_pk_fma_f32 v[150:151], v[150:151], v[190:191], v[182:183] op_sel:[0,1,1] op_sel_hi:[1,1,1]
	v_pk_fma_f32 v[152:153], v[152:153], v[190:191], v[182:183] op_sel:[0,1,1] op_sel_hi:[1,1,1]
	v_pk_fma_f32 v[154:155], v[154:155], v[190:191], v[182:183] op_sel:[0,1,1] op_sel_hi:[1,1,1]
	v_pk_mul_f32 v[140:141], v[112:113], v[140:141]
	v_pk_mul_f32 v[142:143], v[114:115], v[142:143]
	v_pk_mul_f32 v[144:145], v[108:109], v[144:145]
	v_pk_mul_f32 v[146:147], v[110:111], v[146:147]
	v_pk_mul_f32 v[148:149], v[104:105], v[148:149]
	v_pk_mul_f32 v[150:151], v[106:107], v[150:151]
	v_pk_mul_f32 v[152:153], v[100:101], v[152:153]
	v_pk_mul_f32 v[154:155], v[102:103], v[154:155]
	v_exp_f32_e32 v140, v140
	v_exp_f32_e32 v141, v141
	v_exp_f32_e32 v142, v142
	v_exp_f32_e32 v143, v143
	v_exp_f32_e32 v144, v144
	v_exp_f32_e32 v145, v145
	v_exp_f32_e32 v146, v146
	v_exp_f32_e32 v147, v147
	v_exp_f32_e32 v148, v148
	v_exp_f32_e32 v149, v149
	v_exp_f32_e32 v150, v150
	v_exp_f32_e32 v151, v151
	v_exp_f32_e32 v152, v152
	v_exp_f32_e32 v153, v153
	v_exp_f32_e32 v154, v154
	v_exp_f32_e32 v155, v155
	v_pk_fma_f32 v[140:141], v[140:141], v[208:209], v[208:209] op_sel:[0,1,1] op_sel_hi:[1,1,1]
	v_pk_fma_f32 v[142:143], v[142:143], v[208:209], v[208:209] op_sel:[0,1,1] op_sel_hi:[1,1,1]
	v_pk_fma_f32 v[144:145], v[144:145], v[208:209], v[208:209] op_sel:[0,1,1] op_sel_hi:[1,1,1]
	v_pk_fma_f32 v[146:147], v[146:147], v[208:209], v[208:209] op_sel:[0,1,1] op_sel_hi:[1,1,1]
	v_pk_fma_f32 v[148:149], v[148:149], v[208:209], v[208:209] op_sel:[0,1,1] op_sel_hi:[1,1,1]
	v_pk_fma_f32 v[150:151], v[150:151], v[208:209], v[208:209] op_sel:[0,1,1] op_sel_hi:[1,1,1]
	v_pk_fma_f32 v[152:153], v[152:153], v[208:209], v[208:209] op_sel:[0,1,1] op_sel_hi:[1,1,1]
	v_pk_fma_f32 v[154:155], v[154:155], v[208:209], v[208:209] op_sel:[0,1,1] op_sel_hi:[1,1,1]
	v_rcp_f32_e32 v140, v140
	v_rcp_f32_e32 v141, v141
	v_rcp_f32_e32 v142, v142
	v_rcp_f32_e32 v143, v143
	v_rcp_f32_e32 v144, v144
	v_rcp_f32_e32 v145, v145
	v_rcp_f32_e32 v146, v146
	v_rcp_f32_e32 v147, v147
	v_rcp_f32_e32 v148, v148
	v_rcp_f32_e32 v149, v149
	v_rcp_f32_e32 v150, v150
	v_rcp_f32_e32 v151, v151
	v_rcp_f32_e32 v152, v152
	v_rcp_f32_e32 v153, v153
	v_rcp_f32_e32 v154, v154
	v_rcp_f32_e32 v155, v155
	v_pk_mul_f32 v[112:113], v[112:113], v[140:141]
	v_pk_mul_f32 v[114:115], v[114:115], v[142:143]
	v_pk_mul_f32 v[108:109], v[108:109], v[144:145]
	v_pk_mul_f32 v[110:111], v[110:111], v[146:147]
	v_pk_mul_f32 v[104:105], v[104:105], v[148:149]
	v_pk_mul_f32 v[106:107], v[106:107], v[150:151]
	v_pk_mul_f32 v[100:101], v[100:101], v[152:153]
	v_pk_mul_f32 v[102:103], v[102:103], v[154:155]
	v_add_u32_e32 v134, 0x4000, v134
	v_add_u32_e32 v135, 0x400, v135
	v_pk_add_f32 v[216:217], v[112:113], v[114:115]
	v_pk_mul_f32 v[218:219], v[112:113], v[112:113]
	v_pk_fma_f32 v[218:219], v[114:115], v[114:115], v[218:219]
	v_pk_add_f32 v[216:217], v[216:217], v[108:109]
	v_pk_fma_f32 v[218:219], v[108:109], v[108:109], v[218:219]
	v_pk_add_f32 v[216:217], v[216:217], v[110:111]
	v_pk_fma_f32 v[218:219], v[110:111], v[110:111], v[218:219]
	v_pk_add_f32 v[216:217], v[216:217], v[104:105]
	v_pk_fma_f32 v[218:219], v[104:105], v[104:105], v[218:219]
	v_pk_add_f32 v[216:217], v[216:217], v[106:107]
	v_pk_fma_f32 v[218:219], v[106:107], v[106:107], v[218:219]
	v_pk_add_f32 v[216:217], v[216:217], v[100:101]
	v_pk_fma_f32 v[218:219], v[100:101], v[100:101], v[218:219]
	v_pk_add_f32 v[216:217], v[216:217], v[102:103]
	v_pk_fma_f32 v[218:219], v[102:103], v[102:103], v[218:219]
	v_add_f32_e32 v162, v216, v217
	v_add_f32_e32 v163, v218, v219
	ds_swizzle_b32 v161, v162 offset:swizzle(SWAP,16)
	ds_swizzle_b32 v198, v163 offset:swizzle(SWAP,16)
	v_cvt_pk_bf16_f32 v112, v112, v113
	v_cvt_pk_bf16_f32 v113, v114, v115
	v_cvt_pk_bf16_f32 v114, v108, v109
	v_cvt_pk_bf16_f32 v115, v110, v111
	global_store_dwordx4 v134, v[112:115], s[0:1]
	v_cvt_pk_bf16_f32 v104, v104, v105
	v_cvt_pk_bf16_f32 v105, v106, v107
	v_cvt_pk_bf16_f32 v106, v100, v101
	v_cvt_pk_bf16_f32 v107, v102, v103
	global_store_dwordx4 v134, v[104:107], s[0:1] offset:256
	s_waitcnt lgkmcnt(0)
; __device__ __forceinline__ u32x4 pack8(const f32x4 a, const f32x4 b) { u32x4 w; w.x = cvt_pk_bf16(a[0], a[1]); w.y = cvt_pk_bf16(a[2], a[3]); w.z = cvt_pk_bf16(b[0], b[1]); w.w = cvt_pk_bf16(b[2], b[3]); return w; }
;     ...
;             for (int bj = 0; bj < 2; ++bj) { f32x4 v0 = acc[ai][bj][m][0] * rf, v1 = acc[ai][bj][m][1] * rf;
;                 if (act != 0) {
; #pragma unroll
;                     for (int e = 0; e < 4; ++e) { const float x0 = v0[e], x1 = v1[e];
;                         const float r0 = __builtin_amdgcn_rcpf(1.0f + __builtin_amdgcn_exp2f(x0 * (c0 + c1 * x0 * x0))), r1 = __builtin_amdgcn_rcpf(1.0f + __builtin_amdgcn_exp2f(x1 * (c0 + c1 * x1 * x1)));
;                         v0[e] = act == 1 ? x0 * r0 : r0; v1[e] = act == 1 ? x1 * r1 : r1; } }
;                 if (stat) {
; #pragma unroll
;                     for (int e = 0; e < 4; ++e) { ls1 += v0[e] + v1[e]; ls2 += v0[e] * v0[e] + v1[e] * v1[e]; } }
;                 *(u32x4*)(rowp + bj * HALF) = pack8(v0, v1); }
;             if (stat) { ls1 = xor_add<16>(ls1); ls1 = xor_add<32>(ls1); ls2 = xor_add<16>(ls2); ls2 = xor_add<32>(ls2);
;                 if (fq == 0) { f32x2 st2; st2.x = ls1; st2.y = ls2; *(f32x2*)(stat + (size_t)(row0 + ai * HALF + m * 16) * 16) = st2; } }
	v_add_f32_e32 v162, v162, v161
	v_add_f32_e32 v163, v163, v198
	v_mov_b32_e32 v199, v162
	v_mov_b32_e32 v200, v163
	s_nop 1
	v_permlane32_swap_b32_e32 v162, v199
	v_permlane32_swap_b32_e32 v163, v200
	s_and_b64 exec, exec, s[4:5]
	v_add_f32_e32 v162, v162, v199
	v_add_f32_e32 v163, v163, v200
	global_store_dwordx2 v135, v[162:163], s[38:39]
	s_mov_b64 exec, -1
	v_pk_mul_f32 v[140:141], v[96:97], v[96:97]
	v_pk_mul_f32 v[142:143], v[98:99], v[98:99]
	v_pk_mul_f32 v[144:145], v[92:93], v[92:93]
	v_pk_mul_f32 v[146:147], v[94:95], v[94:95]
	v_pk_mul_f32 v[148:149], v[88:89], v[88:89]
	v_pk_mul_f32 v[150:151], v[90:91], v[90:91]
	v_pk_mul_f32 v[152:153], v[84:85], v[84:85]
	v_pk_mul_f32 v[154:155], v[86:87], v[86:87]
	v_pk_fma_f32 v[140:141], v[140:141], v[192:193], v[184:185] op_sel:[0,0,0] op_sel_hi:[1,0,0]
	v_pk_fma_f32 v[142:143], v[142:143], v[192:193], v[184:185] op_sel:[0,0,0] op_sel_hi:[1,0,0]
	v_pk_fma_f32 v[144:145], v[144:145], v[192:193], v[184:185] op_sel:[0,0,0] op_sel_hi:[1,0,0]
	v_pk_fma_f32 v[146:147], v[146:147], v[192:193], v[184:185] op_sel:[0,0,0] op_sel_hi:[1,0,0]
	v_pk_fma_f32 v[148:149], v[148:149], v[192:193], v[184:185] op_sel:[0,0,0] op_sel_hi:[1,0,0]
	v_pk_fma_f32 v[150:151], v[150:151], v[192:193], v[184:185] op_sel:[0,0,0] op_sel_hi:[1,0,0]
	v_pk_fma_f32 v[152:153], v[152:153], v[192:193], v[184:185] op_sel:[0,0,0] op_sel_hi:[1,0,0]
	v_pk_fma_f32 v[154:155], v[154:155], v[192:193], v[184:185] op_sel:[0,0,0] op_sel_hi:[1,0,0]
	v_pk_mul_f32 v[140:141], v[96:97], v[140:141]
	v_pk_mul_f32 v[142:143], v[98:99], v[142:143]
	v_pk_mul_f32 v[144:145], v[92:93], v[144:145]
	v_pk_mul_f32 v[146:147], v[94:95], v[146:147]
	v_pk_mul_f32 v[148:149], v[88:89], v[148:149]
	v_pk_mul_f32 v[150:151], v[90:91], v[150:151]
	v_pk_mul_f32 v[152:153], v[84:85], v[152:153]
	v_pk_mul_f32 v[154:155], v[86:87], v[154:155]
	v_exp_f32_e32 v140, v140
	v_exp_f32_e32 v141, v141
	v_exp_f32_e32 v142, v142
	v_exp_f32_e32 v143, v143
	v_exp_f32_e32 v144, v144
	v_exp_f32_e32 v145, v145
	v_exp_f32_e32 v146, v146
	v_exp_f32_e32 v147, v147
	v_exp_f32_e32 v148, v148
	v_exp_f32_e32 v149, v149
	v_exp_f32_e32 v150, v150
	v_exp_f32_e32 v151, v151
	v_exp_f32_e32 v152, v152
	v_exp_f32_e32 v153, v153
	v_exp_f32_e32 v154, v154
	v_exp_f32_e32 v155, v155
	v_pk_fma_f32 v[140:141], v[140:141], v[210:211], v[210:211] op_sel:[0,0,0] op_sel_hi:[1,0,0]
	v_pk_fma_f32 v[142:143], v[142:143], v[210:211], v[210:211] op_sel:[0,0,0] op_sel_hi:[1,0,0]
	v_pk_fma_f32 v[144:145], v[144:145], v[210:211], v[210:211] op_sel:[0,0,0] op_sel_hi:[1,0,0]
	v_pk_fma_f32 v[146:147], v[146:147], v[210:211], v[210:211] op_sel:[0,0,0] op_sel_hi:[1,0,0]
	v_pk_fma_f32 v[148:149], v[148:149], v[210:211], v[210:211] op_sel:[0,0,0] op_sel_hi:[1,0,0]
	v_pk_fma_f32 v[150:151], v[150:151], v[210:211], v[210:211] op_sel:[0,0,0] op_sel_hi:[1,0,0]
	v_pk_fma_f32 v[152:153], v[152:153], v[210:211], v[210:211] op_sel:[0,0,0] op_sel_hi:[1,0,0]
	v_pk_fma_f32 v[154:155], v[154:155], v[210:211], v[210:211] op_sel:[0,0,0] op_sel_hi:[1,0,0]
	v_rcp_f32_e32 v140, v140
	v_rcp_f32_e32 v141, v141
	v_rcp_f32_e32 v142, v142
	v_rcp_f32_e32 v143, v143
	v_rcp_f32_e32 v144, v144
	v_rcp_f32_e32 v145, v145
	v_rcp_f32_e32 v146, v146
	v_rcp_f32_e32 v147, v147
	v_rcp_f32_e32 v148, v148
	v_rcp_f32_e32 v149, v149
	v_rcp_f32_e32 v150, v150
	v_rcp_f32_e32 v151, v151
	v_rcp_f32_e32 v152, v152
	v_rcp_f32_e32 v153, v153
	v_rcp_f32_e32 v154, v154
	v_rcp_f32_e32 v155, v155
	v_pk_mul_f32 v[96:97], v[96:97], v[140:141]
	v_pk_mul_f32 v[98:99], v[98:99], v[142:143]
	v_pk_mul_f32 v[92:93], v[92:93], v[144:145]
	v_pk_mul_f32 v[94:95], v[94:95], v[146:147]
	v_pk_mul_f32 v[88:89], v[88:89], v[148:149]
	v_pk_mul_f32 v[90:91], v[90:91], v[150:151]
	v_pk_mul_f32 v[84:85], v[84:85], v[152:153]
	v_pk_mul_f32 v[86:87], v[86:87], v[154:155]
	v_add_u32_e32 v134, 0x4000, v134
	v_add_u32_e32 v135, 0x400, v135
	v_pk_add_f32 v[216:217], v[96:97], v[98:99]
	v_pk_mul_f32 v[218:219], v[96:97], v[96:97]
	v_pk_fma_f32 v[218:219], v[98:99], v[98:99], v[218:219]
	v_pk_add_f32 v[216:217], v[216:217], v[92:93]
	v_pk_fma_f32 v[218:219], v[92:93], v[92:93], v[218:219]
	v_pk_add_f32 v[216:217], v[216:217], v[94:95]
	v_pk_fma_f32 v[218:219], v[94:95], v[94:95], v[218:219]
	v_pk_add_f32 v[216:217], v[216:217], v[88:89]
	v_pk_fma_f32 v[218:219], v[88:89], v[88:89], v[218:219]
	v_pk_add_f32 v[216:217], v[216:217], v[90:91]
	v_pk_fma_f32 v[218:219], v[90:91], v[90:91], v[218:219]
	v_pk_add_f32 v[216:217], v[216:217], v[84:85]
	v_pk_fma_f32 v[218:219], v[84:85], v[84:85], v[218:219]
	v_pk_add_f32 v[216:217], v[216:217], v[86:87]
	v_pk_fma_f32 v[218:219], v[86:87], v[86:87], v[218:219]
	v_add_f32_e32 v162, v216, v217
	v_add_f32_e32 v163, v218, v219
	ds_swizzle_b32 v161, v162 offset:swizzle(SWAP,16)
	ds_swizzle_b32 v198, v163 offset:swizzle(SWAP,16)
	v_cvt_pk_bf16_f32 v96, v96, v97
	v_cvt_pk_bf16_f32 v97, v98, v99
	v_cvt_pk_bf16_f32 v98, v92, v93
	v_cvt_pk_bf16_f32 v99, v94, v95
	global_store_dwordx4 v134, v[96:99], s[0:1]
	v_cvt_pk_bf16_f32 v88, v88, v89
	v_cvt_pk_bf16_f32 v89, v90, v91
	v_cvt_pk_bf16_f32 v90, v84, v85
	v_cvt_pk_bf16_f32 v91, v86, v87
	global_store_dwordx4 v134, v[88:91], s[0:1] offset:256
	s_waitcnt lgkmcnt(0)
; __device__ __forceinline__ u32x4 pack8(const f32x4 a, const f32x4 b) { u32x4 w; w.x = cvt_pk_bf16(a[0], a[1]); w.y = cvt_pk_bf16(a[2], a[3]); w.z = cvt_pk_bf16(b[0], b[1]); w.w = cvt_pk_bf16(b[2], b[3]); return w; }
;     ...
;             for (int bj = 0; bj < 2; ++bj) { f32x4 v0 = acc[ai][bj][m][0] * rf, v1 = acc[ai][bj][m][1] * rf;
;                 if (act != 0) {
; #pragma unroll
;                     for (int e = 0; e < 4; ++e) { const float x0 = v0[e], x1 = v1[e];
;                         const float r0 = __builtin_amdgcn_rcpf(1.0f + __builtin_amdgcn_exp2f(x0 * (c0 + c1 * x0 * x0))), r1 = __builtin_amdgcn_rcpf(1.0f + __builtin_amdgcn_exp2f(x1 * (c0 + c1 * x1 * x1)));
;                         v0[e] = act == 1 ? x0 * r0 : r0; v1[e] = act == 1 ? x1 * r1 : r1; } }
;                 if (stat) {
; #pragma unroll
;                     for (int e = 0; e < 4; ++e) { ls1 += v0[e] + v1[e]; ls2 += v0[e] * v0[e] + v1[e] * v1[e]; } }
;                 *(u32x4*)(rowp + bj * HALF) = pack8(v0, v1); }
;             if (stat) { ls1 = xor_add<16>(ls1); ls1 = xor_add<32>(ls1); ls2 = xor_add<16>(ls2); ls2 = xor_add<32>(ls2);
;                 if (fq == 0) { f32x2 st2; st2.x = ls1; st2.y = ls2; *(f32x2*)(stat + (size_t)(row0 + ai * HALF + m * 16) * 16) = st2; } }
	v_add_f32_e32 v162, v162, v161
	v_add_f32_e32 v163, v163, v198
	v_mov_b32_e32 v199, v162
	v_mov_b32_e32 v200, v163
	s_nop 1
	v_permlane32_swap_b32_e32 v162, v199
	v_permlane32_swap_b32_e32 v163, v200
	s_and_b64 exec, exec, s[4:5]
	v_add_f32_e32 v162, v162, v199
	v_add_f32_e32 v163, v163, v200
	global_store_dwordx2 v135, v[162:163], s[38:39]
	s_mov_b64 exec, -1
	v_pk_mul_f32 v[140:141], v[80:81], v[80:81]
	v_pk_mul_f32 v[142:143], v[82:83], v[82:83]
	v_pk_mul_f32 v[144:145], v[76:77], v[76:77]
	v_pk_mul_f32 v[146:147], v[78:79], v[78:79]
	v_pk_mul_f32 v[148:149], v[72:73], v[72:73]
	v_pk_mul_f32 v[150:151], v[74:75], v[74:75]
	v_pk_mul_f32 v[152:153], v[68:69], v[68:69]
	v_pk_mul_f32 v[154:155], v[70:71], v[70:71]
	v_pk_fma_f32 v[140:141], v[140:141], v[192:193], v[184:185] op_sel:[0,1,1] op_sel_hi:[1,1,1]
	v_pk_fma_f32 v[142:143], v[142:143], v[192:193], v[184:185] op_sel:[0,1,1] op_sel_hi:[1,1,1]
	v_pk_fma_f32 v[144:145], v[144:145], v[192:193], v[184:185] op_sel:[0,1,1] op_sel_hi:[1,1,1]
	v_pk_fma_f32 v[146:147], v[146:147], v[192:193], v[184:185] op_sel:[0,1,1] op_sel_hi:[1,1,1]
	v_pk_fma_f32 v[148:149], v[148:149], v[192:193], v[184:185] op_sel:[0,1,1] op_sel_hi:[1,1,1]
	v_pk_fma_f32 v[150:151], v[150:151], v[192:193], v[184:185] op_sel:[0,1,1] op_sel_hi:[1,1,1]
	v_pk_fma_f32 v[152:153], v[152:153], v[192:193], v[184:185] op_sel:[0,1,1] op_sel_hi:[1,1,1]
	v_pk_fma_f32 v[154:155], v[154:155], v[192:193], v[184:185] op_sel:[0,1,1] op_sel_hi:[1,1,1]
	v_pk_mul_f32 v[140:141], v[80:81], v[140:141]
	v_pk_mul_f32 v[142:143], v[82:83], v[142:143]
	v_pk_mul_f32 v[144:145], v[76:77], v[144:145]
	v_pk_mul_f32 v[146:147], v[78:79], v[146:147]
	v_pk_mul_f32 v[148:149], v[72:73], v[148:149]
	v_pk_mul_f32 v[150:151], v[74:75], v[150:151]
	v_pk_mul_f32 v[152:153], v[68:69], v[152:153]
	v_pk_mul_f32 v[154:155], v[70:71], v[154:155]
	v_exp_f32_e32 v140, v140
	v_exp_f32_e32 v141, v141
	v_exp_f32_e32 v142, v142
	v_exp_f32_e32 v143, v143
	v_exp_f32_e32 v144, v144
	v_exp_f32_e32 v145, v145
	v_exp_f32_e32 v146, v146
	v_exp_f32_e32 v147, v147
	v_exp_f32_e32 v148, v148
	v_exp_f32_e32 v149, v149
	v_exp_f32_e32 v150, v150
	v_exp_f32_e32 v151, v151
	v_exp_f32_e32 v152, v152
	v_exp_f32_e32 v153, v153
	v_exp_f32_e32 v154, v154
	v_exp_f32_e32 v155, v155
	v_pk_fma_f32 v[140:141], v[140:141], v[210:211], v[210:211] op_sel:[0,1,1] op_sel_hi:[1,1,1]
	v_pk_fma_f32 v[142:143], v[142:143], v[210:211], v[210:211] op_sel:[0,1,1] op_sel_hi:[1,1,1]
	v_pk_fma_f32 v[144:145], v[144:145], v[210:211], v[210:211] op_sel:[0,1,1] op_sel_hi:[1,1,1]
	v_pk_fma_f32 v[146:147], v[146:147], v[210:211], v[210:211] op_sel:[0,1,1] op_sel_hi:[1,1,1]
	v_pk_fma_f32 v[148:149], v[148:149], v[210:211], v[210:211] op_sel:[0,1,1] op_sel_hi:[1,1,1]
	v_pk_fma_f32 v[150:151], v[150:151], v[210:211], v[210:211] op_sel:[0,1,1] op_sel_hi:[1,1,1]
	v_pk_fma_f32 v[152:153], v[152:153], v[210:211], v[210:211] op_sel:[0,1,1] op_sel_hi:[1,1,1]
	v_pk_fma_f32 v[154:155], v[154:155], v[210:211], v[210:211] op_sel:[0,1,1] op_sel_hi:[1,1,1]
	v_rcp_f32_e32 v140, v140
	v_rcp_f32_e32 v141, v141
	v_rcp_f32_e32 v142, v142
	v_rcp_f32_e32 v143, v143
	v_rcp_f32_e32 v144, v144
	v_rcp_f32_e32 v145, v145
	v_rcp_f32_e32 v146, v146
	v_rcp_f32_e32 v147, v147
	v_rcp_f32_e32 v148, v148
	v_rcp_f32_e32 v149, v149
	v_rcp_f32_e32 v150, v150
	v_rcp_f32_e32 v151, v151
	v_rcp_f32_e32 v152, v152
	v_rcp_f32_e32 v153, v153
	v_rcp_f32_e32 v154, v154
	v_rcp_f32_e32 v155, v155
	v_pk_mul_f32 v[80:81], v[80:81], v[140:141]
	v_pk_mul_f32 v[82:83], v[82:83], v[142:143]
	v_pk_mul_f32 v[76:77], v[76:77], v[144:145]
	v_pk_mul_f32 v[78:79], v[78:79], v[146:147]
	v_pk_mul_f32 v[72:73], v[72:73], v[148:149]
	v_pk_mul_f32 v[74:75], v[74:75], v[150:151]
	v_pk_mul_f32 v[68:69], v[68:69], v[152:153]
	v_pk_mul_f32 v[70:71], v[70:71], v[154:155]
	v_add_u32_e32 v134, 0x4000, v134
	v_add_u32_e32 v135, 0x400, v135
	v_pk_add_f32 v[216:217], v[80:81], v[82:83]
	v_pk_mul_f32 v[218:219], v[80:81], v[80:81]
	v_pk_fma_f32 v[218:219], v[82:83], v[82:83], v[218:219]
	v_pk_add_f32 v[216:217], v[216:217], v[76:77]
	v_pk_fma_f32 v[218:219], v[76:77], v[76:77], v[218:219]
	v_pk_add_f32 v[216:217], v[216:217], v[78:79]
	v_pk_fma_f32 v[218:219], v[78:79], v[78:79], v[218:219]
	v_pk_add_f32 v[216:217], v[216:217], v[72:73]
	v_pk_fma_f32 v[218:219], v[72:73], v[72:73], v[218:219]
	v_pk_add_f32 v[216:217], v[216:217], v[74:75]
	v_pk_fma_f32 v[218:219], v[74:75], v[74:75], v[218:219]
	v_pk_add_f32 v[216:217], v[216:217], v[68:69]
	v_pk_fma_f32 v[218:219], v[68:69], v[68:69], v[218:219]
	v_pk_add_f32 v[216:217], v[216:217], v[70:71]
	v_pk_fma_f32 v[218:219], v[70:71], v[70:71], v[218:219]
	v_add_f32_e32 v162, v216, v217
	v_add_f32_e32 v163, v218, v219
	ds_swizzle_b32 v161, v162 offset:swizzle(SWAP,16)
	ds_swizzle_b32 v198, v163 offset:swizzle(SWAP,16)
	v_cvt_pk_bf16_f32 v80, v80, v81
	v_cvt_pk_bf16_f32 v81, v82, v83
	v_cvt_pk_bf16_f32 v82, v76, v77
	v_cvt_pk_bf16_f32 v83, v78, v79
	global_store_dwordx4 v134, v[80:83], s[0:1]
	v_cvt_pk_bf16_f32 v72, v72, v73
	v_cvt_pk_bf16_f32 v73, v74, v75
	v_cvt_pk_bf16_f32 v74, v68, v69
	v_cvt_pk_bf16_f32 v75, v70, v71
	global_store_dwordx4 v134, v[72:75], s[0:1] offset:256
	s_waitcnt lgkmcnt(0)
; __device__ __forceinline__ u32x4 pack8(const f32x4 a, const f32x4 b) { u32x4 w; w.x = cvt_pk_bf16(a[0], a[1]); w.y = cvt_pk_bf16(a[2], a[3]); w.z = cvt_pk_bf16(b[0], b[1]); w.w = cvt_pk_bf16(b[2], b[3]); return w; }
;     ...
;             for (int bj = 0; bj < 2; ++bj) { f32x4 v0 = acc[ai][bj][m][0] * rf, v1 = acc[ai][bj][m][1] * rf;
;                 if (act != 0) {
; #pragma unroll
;                     for (int e = 0; e < 4; ++e) { const float x0 = v0[e], x1 = v1[e];
;                         const float r0 = __builtin_amdgcn_rcpf(1.0f + __builtin_amdgcn_exp2f(x0 * (c0 + c1 * x0 * x0))), r1 = __builtin_amdgcn_rcpf(1.0f + __builtin_amdgcn_exp2f(x1 * (c0 + c1 * x1 * x1)));
;                         v0[e] = act == 1 ? x0 * r0 : r0; v1[e] = act == 1 ? x1 * r1 : r1; } }
;                 if (stat) {
; #pragma unroll
;                     for (int e = 0; e < 4; ++e) { ls1 += v0[e] + v1[e]; ls2 += v0[e] * v0[e] + v1[e] * v1[e]; } }
;                 *(u32x4*)(rowp + bj * HALF) = pack8(v0, v1); }
;             if (stat) { ls1 = xor_add<16>(ls1); ls1 = xor_add<32>(ls1); ls2 = xor_add<16>(ls2); ls2 = xor_add<32>(ls2);
;                 if (fq == 0) { f32x2 st2; st2.x = ls1; st2.y = ls2; *(f32x2*)(stat + (size_t)(row0 + ai * HALF + m * 16) * 16) = st2; } }
	v_add_f32_e32 v162, v162, v161
	v_add_f32_e32 v163, v163, v198
	v_mov_b32_e32 v199, v162
	v_mov_b32_e32 v200, v163
	s_nop 1
	v_permlane32_swap_b32_e32 v162, v199
	v_permlane32_swap_b32_e32 v163, v200
	s_and_b64 exec, exec, s[4:5]
	v_add_f32_e32 v162, v162, v199
	v_add_f32_e32 v163, v163, v200
	global_store_dwordx2 v135, v[162:163], s[38:39]
	s_mov_b64 exec, -1
	v_pk_mul_f32 v[140:141], v[64:65], v[64:65]
	v_pk_mul_f32 v[142:143], v[66:67], v[66:67]
	v_pk_mul_f32 v[144:145], v[60:61], v[60:61]
	v_pk_mul_f32 v[146:147], v[62:63], v[62:63]
	v_pk_mul_f32 v[148:149], v[56:57], v[56:57]
	v_pk_mul_f32 v[150:151], v[58:59], v[58:59]
	v_pk_mul_f32 v[152:153], v[52:53], v[52:53]
	v_pk_mul_f32 v[154:155], v[54:55], v[54:55]
	v_pk_fma_f32 v[140:141], v[140:141], v[194:195], v[186:187] op_sel:[0,0,0] op_sel_hi:[1,0,0]
	v_pk_fma_f32 v[142:143], v[142:143], v[194:195], v[186:187] op_sel:[0,0,0] op_sel_hi:[1,0,0]
	v_pk_fma_f32 v[144:145], v[144:145], v[194:195], v[186:187] op_sel:[0,0,0] op_sel_hi:[1,0,0]
	v_pk_fma_f32 v[146:147], v[146:147], v[194:195], v[186:187] op_sel:[0,0,0] op_sel_hi:[1,0,0]
	v_pk_fma_f32 v[148:149], v[148:149], v[194:195], v[186:187] op_sel:[0,0,0] op_sel_hi:[1,0,0]
	v_pk_fma_f32 v[150:151], v[150:151], v[194:195], v[186:187] op_sel:[0,0,0] op_sel_hi:[1,0,0]
	v_pk_fma_f32 v[152:153], v[152:153], v[194:195], v[186:187] op_sel:[0,0,0] op_sel_hi:[1,0,0]
	v_pk_fma_f32 v[154:155], v[154:155], v[194:195], v[186:187] op_sel:[0,0,0] op_sel_hi:[1,0,0]
	v_pk_mul_f32 v[140:141], v[64:65], v[140:141]
	v_pk_mul_f32 v[142:143], v[66:67], v[142:143]
	v_pk_mul_f32 v[144:145], v[60:61], v[144:145]
	v_pk_mul_f32 v[146:147], v[62:63], v[146:147]
	v_pk_mul_f32 v[148:149], v[56:57], v[148:149]
	v_pk_mul_f32 v[150:151], v[58:59], v[150:151]
	v_pk_mul_f32 v[152:153], v[52:53], v[152:153]
	v_pk_mul_f32 v[154:155], v[54:55], v[154:155]
	v_exp_f32_e32 v140, v140
	v_exp_f32_e32 v141, v141
	v_exp_f32_e32 v142, v142
	v_exp_f32_e32 v143, v143
	v_exp_f32_e32 v144, v144
	v_exp_f32_e32 v145, v145
	v_exp_f32_e32 v146, v146
	v_exp_f32_e32 v147, v147
	v_exp_f32_e32 v148, v148
	v_exp_f32_e32 v149, v149
	v_exp_f32_e32 v150, v150
	v_exp_f32_e32 v151, v151
	v_exp_f32_e32 v152, v152
	v_exp_f32_e32 v153, v153
	v_exp_f32_e32 v154, v154
	v_exp_f32_e32 v155, v155
	v_pk_fma_f32 v[140:141], v[140:141], v[212:213], v[212:213] op_sel:[0,0,0] op_sel_hi:[1,0,0]
	v_pk_fma_f32 v[142:143], v[142:143], v[212:213], v[212:213] op_sel:[0,0,0] op_sel_hi:[1,0,0]
	v_pk_fma_f32 v[144:145], v[144:145], v[212:213], v[212:213] op_sel:[0,0,0] op_sel_hi:[1,0,0]
	v_pk_fma_f32 v[146:147], v[146:147], v[212:213], v[212:213] op_sel:[0,0,0] op_sel_hi:[1,0,0]
	v_pk_fma_f32 v[148:149], v[148:149], v[212:213], v[212:213] op_sel:[0,0,0] op_sel_hi:[1,0,0]
	v_pk_fma_f32 v[150:151], v[150:151], v[212:213], v[212:213] op_sel:[0,0,0] op_sel_hi:[1,0,0]
	v_pk_fma_f32 v[152:153], v[152:153], v[212:213], v[212:213] op_sel:[0,0,0] op_sel_hi:[1,0,0]
	v_pk_fma_f32 v[154:155], v[154:155], v[212:213], v[212:213] op_sel:[0,0,0] op_sel_hi:[1,0,0]
	v_rcp_f32_e32 v140, v140
	v_rcp_f32_e32 v141, v141
	v_rcp_f32_e32 v142, v142
	v_rcp_f32_e32 v143, v143
	v_rcp_f32_e32 v144, v144
	v_rcp_f32_e32 v145, v145
	v_rcp_f32_e32 v146, v146
	v_rcp_f32_e32 v147, v147
	v_rcp_f32_e32 v148, v148
	v_rcp_f32_e32 v149, v149
	v_rcp_f32_e32 v150, v150
	v_rcp_f32_e32 v151, v151
	v_rcp_f32_e32 v152, v152
	v_rcp_f32_e32 v153, v153
	v_rcp_f32_e32 v154, v154
	v_rcp_f32_e32 v155, v155
	v_pk_mul_f32 v[64:65], v[64:65], v[140:141]
	v_pk_mul_f32 v[66:67], v[66:67], v[142:143]
	v_pk_mul_f32 v[60:61], v[60:61], v[144:145]
	v_pk_mul_f32 v[62:63], v[62:63], v[146:147]
	v_pk_mul_f32 v[56:57], v[56:57], v[148:149]
	v_pk_mul_f32 v[58:59], v[58:59], v[150:151]
	v_pk_mul_f32 v[52:53], v[52:53], v[152:153]
	v_pk_mul_f32 v[54:55], v[54:55], v[154:155]
	v_add_u32_e32 v134, 0x14000, v134
	v_add_u32_e32 v135, 0x1400, v135
	v_pk_add_f32 v[216:217], v[64:65], v[66:67]
	v_pk_mul_f32 v[218:219], v[64:65], v[64:65]
	v_pk_fma_f32 v[218:219], v[66:67], v[66:67], v[218:219]
	v_pk_add_f32 v[216:217], v[216:217], v[60:61]
	v_pk_fma_f32 v[218:219], v[60:61], v[60:61], v[218:219]
	v_pk_add_f32 v[216:217], v[216:217], v[62:63]
	v_pk_fma_f32 v[218:219], v[62:63], v[62:63], v[218:219]
	v_pk_add_f32 v[216:217], v[216:217], v[56:57]
	v_pk_fma_f32 v[218:219], v[56:57], v[56:57], v[218:219]
	v_pk_add_f32 v[216:217], v[216:217], v[58:59]
	v_pk_fma_f32 v[218:219], v[58:59], v[58:59], v[218:219]
	v_pk_add_f32 v[216:217], v[216:217], v[52:53]
	v_pk_fma_f32 v[218:219], v[52:53], v[52:53], v[218:219]
	v_pk_add_f32 v[216:217], v[216:217], v[54:55]
	v_pk_fma_f32 v[218:219], v[54:55], v[54:55], v[218:219]
	v_add_f32_e32 v162, v216, v217
	v_add_f32_e32 v163, v218, v219
	ds_swizzle_b32 v161, v162 offset:swizzle(SWAP,16)
	ds_swizzle_b32 v198, v163 offset:swizzle(SWAP,16)
	v_cvt_pk_bf16_f32 v64, v64, v65
	v_cvt_pk_bf16_f32 v65, v66, v67
	v_cvt_pk_bf16_f32 v66, v60, v61
	v_cvt_pk_bf16_f32 v67, v62, v63
	global_store_dwordx4 v134, v[64:67], s[0:1]
	v_cvt_pk_bf16_f32 v56, v56, v57
	v_cvt_pk_bf16_f32 v57, v58, v59
	v_cvt_pk_bf16_f32 v58, v52, v53
	v_cvt_pk_bf16_f32 v59, v54, v55
	global_store_dwordx4 v134, v[56:59], s[0:1] offset:256
	s_waitcnt lgkmcnt(0)
; __device__ __forceinline__ u32x4 pack8(const f32x4 a, const f32x4 b) { u32x4 w; w.x = cvt_pk_bf16(a[0], a[1]); w.y = cvt_pk_bf16(a[2], a[3]); w.z = cvt_pk_bf16(b[0], b[1]); w.w = cvt_pk_bf16(b[2], b[3]); return w; }
; template <int O> __device__ __forceinline__ float xor_add(float v) {
;     if constexpr (O < 32) return v + __builtin_bit_cast(float, __builtin_amdgcn_ds_swizzle(__builtin_bit_cast(int, v), (O << 10) | 0x1f));
;     else { const auto rr = __builtin_amdgcn_permlane32_swap(__float_as_uint(v), __float_as_uint(v), false, false); return __uint_as_float(rr[0]) + __uint_as_float(rr[1]); }
;     ...
;         for (int m = 0; m < 4; ++m) { bf16_t* rowp = base + (size_t)(row0 + ai * HALF + m * 16) * ldc + col0; float ls1 = 0.f, ls2 = 0.f; const float rf = rsr[ai * HALF + m * 16];
; #pragma unroll
;             for (int bj = 0; bj < 2; ++bj) { f32x4 v0 = acc[ai][bj][m][0] * rf, v1 = acc[ai][bj][m][1] * rf;
;                 if (act != 0) {
; #pragma unroll
;                     for (int e = 0; e < 4; ++e) { const float x0 = v0[e], x1 = v1[e];
;                         const float r0 = __builtin_amdgcn_rcpf(1.0f + __builtin_amdgcn_exp2f(x0 * (c0 + c1 * x0 * x0))), r1 = __builtin_amdgcn_rcpf(1.0f + __builtin_amdgcn_exp2f(x1 * (c0 + c1 * x1 * x1)));
;                         v0[e] = act == 1 ? x0 * r0 : r0; v1[e] = act == 1 ? x1 * r1 : r1; } }
;                 if (stat) {
; #pragma unroll
;                     for (int e = 0; e < 4; ++e) { ls1 += v0[e] + v1[e]; ls2 += v0[e] * v0[e] + v1[e] * v1[e]; } }
;                 *(u32x4*)(rowp + bj * HALF) = pack8(v0, v1); }
;             if (stat) { ls1 = xor_add<16>(ls1); ls1 = xor_add<32>(ls1); ls2 = xor_add<16>(ls2); ls2 = xor_add<32>(ls2);
;                 if (fq == 0) { f32x2 st2; st2.x = ls1; st2.y = ls2; *(f32x2*)(stat + (size_t)(row0 + ai * HALF + m * 16) * 16) = st2; } }
	v_add_f32_e32 v162, v162, v161
	v_add_f32_e32 v163, v163, v198
	v_mov_b32_e32 v199, v162
	v_mov_b32_e32 v200, v163
	s_nop 1
	v_permlane32_swap_b32_e32 v162, v199
	v_permlane32_swap_b32_e32 v163, v200
	s_and_b64 exec, exec, s[4:5]
	v_add_f32_e32 v162, v162, v199
	v_add_f32_e32 v163, v163, v200
	global_store_dwordx2 v135, v[162:163], s[38:39]
	s_mov_b64 exec, -1
	v_pk_mul_f32 v[140:141], v[48:49], v[48:49]
	v_pk_mul_f32 v[142:143], v[50:51], v[50:51]
	v_pk_mul_f32 v[144:145], v[44:45], v[44:45]
	v_pk_mul_f32 v[146:147], v[46:47], v[46:47]
	v_pk_mul_f32 v[148:149], v[40:41], v[40:41]
	v_pk_mul_f32 v[150:151], v[42:43], v[42:43]
	v_pk_mul_f32 v[152:153], v[36:37], v[36:37]
	v_pk_mul_f32 v[154:155], v[38:39], v[38:39]
	v_pk_fma_f32 v[140:141], v[140:141], v[194:195], v[186:187] op_sel:[0,1,1] op_sel_hi:[1,1,1]
	v_pk_fma_f32 v[142:143], v[142:143], v[194:195], v[186:187] op_sel:[0,1,1] op_sel_hi:[1,1,1]
	v_pk_fma_f32 v[144:145], v[144:145], v[194:195], v[186:187] op_sel:[0,1,1] op_sel_hi:[1,1,1]
	v_pk_fma_f32 v[146:147], v[146:147], v[194:195], v[186:187] op_sel:[0,1,1] op_sel_hi:[1,1,1]
	v_pk_fma_f32 v[148:149], v[148:149], v[194:195], v[186:187] op_sel:[0,1,1] op_sel_hi:[1,1,1]
	v_pk_fma_f32 v[150:151], v[150:151], v[194:195], v[186:187] op_sel:[0,1,1] op_sel_hi:[1,1,1]
	v_pk_fma_f32 v[152:153], v[152:153], v[194:195], v[186:187] op_sel:[0,1,1] op_sel_hi:[1,1,1]
	v_pk_fma_f32 v[154:155], v[154:155], v[194:195], v[186:187] op_sel:[0,1,1] op_sel_hi:[1,1,1]
	v_pk_mul_f32 v[140:141], v[48:49], v[140:141]
	v_pk_mul_f32 v[142:143], v[50:51], v[142:143]
	v_pk_mul_f32 v[144:145], v[44:45], v[144:145]
	v_pk_mul_f32 v[146:147], v[46:47], v[146:147]
	v_pk_mul_f32 v[148:149], v[40:41], v[148:149]
	v_pk_mul_f32 v[150:151], v[42:43], v[150:151]
	v_pk_mul_f32 v[152:153], v[36:37], v[152:153]
	v_pk_mul_f32 v[154:155], v[38:39], v[154:155]
	v_exp_f32_e32 v140, v140
	v_exp_f32_e32 v141, v141
	v_exp_f32_e32 v142, v142
	v_exp_f32_e32 v143, v143
	v_exp_f32_e32 v144, v144
	v_exp_f32_e32 v145, v145
	v_exp_f32_e32 v146, v146
	v_exp_f32_e32 v147, v147
	v_exp_f32_e32 v148, v148
	v_exp_f32_e32 v149, v149
	v_exp_f32_e32 v150, v150
	v_exp_f32_e32 v151, v151
	v_exp_f32_e32 v152, v152
	v_exp_f32_e32 v153, v153
	v_exp_f32_e32 v154, v154
	v_exp_f32_e32 v155, v155
	v_pk_fma_f32 v[140:141], v[140:141], v[212:213], v[212:213] op_sel:[0,1,1] op_sel_hi:[1,1,1]
	v_pk_fma_f32 v[142:143], v[142:143], v[212:213], v[212:213] op_sel:[0,1,1] op_sel_hi:[1,1,1]
	v_pk_fma_f32 v[144:145], v[144:145], v[212:213], v[212:213] op_sel:[0,1,1] op_sel_hi:[1,1,1]
	v_pk_fma_f32 v[146:147], v[146:147], v[212:213], v[212:213] op_sel:[0,1,1] op_sel_hi:[1,1,1]
	v_pk_fma_f32 v[148:149], v[148:149], v[212:213], v[212:213] op_sel:[0,1,1] op_sel_hi:[1,1,1]
	v_pk_fma_f32 v[150:151], v[150:151], v[212:213], v[212:213] op_sel:[0,1,1] op_sel_hi:[1,1,1]
	v_pk_fma_f32 v[152:153], v[152:153], v[212:213], v[212:213] op_sel:[0,1,1] op_sel_hi:[1,1,1]
	v_pk_fma_f32 v[154:155], v[154:155], v[212:213], v[212:213] op_sel:[0,1,1] op_sel_hi:[1,1,1]
	v_rcp_f32_e32 v140, v140
	v_rcp_f32_e32 v141, v141
	v_rcp_f32_e32 v142, v142
	v_rcp_f32_e32 v143, v143
	v_rcp_f32_e32 v144, v144
	v_rcp_f32_e32 v145, v145
	v_rcp_f32_e32 v146, v146
	v_rcp_f32_e32 v147, v147
	v_rcp_f32_e32 v148, v148
	v_rcp_f32_e32 v149, v149
	v_rcp_f32_e32 v150, v150
	v_rcp_f32_e32 v151, v151
	v_rcp_f32_e32 v152, v152
	v_rcp_f32_e32 v153, v153
	v_rcp_f32_e32 v154, v154
	v_rcp_f32_e32 v155, v155
	v_pk_mul_f32 v[48:49], v[48:49], v[140:141]
	v_pk_mul_f32 v[50:51], v[50:51], v[142:143]
	v_pk_mul_f32 v[44:45], v[44:45], v[144:145]
	v_pk_mul_f32 v[46:47], v[46:47], v[146:147]
	v_pk_mul_f32 v[40:41], v[40:41], v[148:149]
	v_pk_mul_f32 v[42:43], v[42:43], v[150:151]
	v_pk_mul_f32 v[36:37], v[36:37], v[152:153]
	v_pk_mul_f32 v[38:39], v[38:39], v[154:155]
	v_add_u32_e32 v134, 0x4000, v134
	v_add_u32_e32 v135, 0x400, v135
	v_pk_add_f32 v[216:217], v[48:49], v[50:51]
	v_pk_mul_f32 v[218:219], v[48:49], v[48:49]
	v_pk_fma_f32 v[218:219], v[50:51], v[50:51], v[218:219]
	v_pk_add_f32 v[216:217], v[216:217], v[44:45]
	v_pk_fma_f32 v[218:219], v[44:45], v[44:45], v[218:219]
	v_pk_add_f32 v[216:217], v[216:217], v[46:47]
	v_pk_fma_f32 v[218:219], v[46:47], v[46:47], v[218:219]
	v_pk_add_f32 v[216:217], v[216:217], v[40:41]
	v_pk_fma_f32 v[218:219], v[40:41], v[40:41], v[218:219]
	v_pk_add_f32 v[216:217], v[216:217], v[42:43]
	v_pk_fma_f32 v[218:219], v[42:43], v[42:43], v[218:219]
	v_pk_add_f32 v[216:217], v[216:217], v[36:37]
	v_pk_fma_f32 v[218:219], v[36:37], v[36:37], v[218:219]
	v_pk_add_f32 v[216:217], v[216:217], v[38:39]
	v_pk_fma_f32 v[218:219], v[38:39], v[38:39], v[218:219]
	v_add_f32_e32 v162, v216, v217
	v_add_f32_e32 v163, v218, v219
	ds_swizzle_b32 v161, v162 offset:swizzle(SWAP,16)
	ds_swizzle_b32 v198, v163 offset:swizzle(SWAP,16)
	v_cvt_pk_bf16_f32 v48, v48, v49
	v_cvt_pk_bf16_f32 v49, v50, v51
	v_cvt_pk_bf16_f32 v50, v44, v45
	v_cvt_pk_bf16_f32 v51, v46, v47
	global_store_dwordx4 v134, v[48:51], s[0:1]
	v_cvt_pk_bf16_f32 v40, v40, v41
	v_cvt_pk_bf16_f32 v41, v42, v43
	v_cvt_pk_bf16_f32 v42, v36, v37
	v_cvt_pk_bf16_f32 v43, v38, v39
	global_store_dwordx4 v134, v[40:43], s[0:1] offset:256
	s_waitcnt lgkmcnt(0)
; __device__ __forceinline__ u32x4 pack8(const f32x4 a, const f32x4 b) { u32x4 w; w.x = cvt_pk_bf16(a[0], a[1]); w.y = cvt_pk_bf16(a[2], a[3]); w.z = cvt_pk_bf16(b[0], b[1]); w.w = cvt_pk_bf16(b[2], b[3]); return w; }
; template <int O> __device__ __forceinline__ float xor_add(float v) {
;     if constexpr (O < 32) return v + __builtin_bit_cast(float, __builtin_amdgcn_ds_swizzle(__builtin_bit_cast(int, v), (O << 10) | 0x1f));
;     else { const auto rr = __builtin_amdgcn_permlane32_swap(__float_as_uint(v), __float_as_uint(v), false, false); return __uint_as_float(rr[0]) + __uint_as_float(rr[1]); }
;     ...
;         for (int m = 0; m < 4; ++m) { bf16_t* rowp = base + (size_t)(row0 + ai * HALF + m * 16) * ldc + col0; float ls1 = 0.f, ls2 = 0.f; const float rf = rsr[ai * HALF + m * 16];
; #pragma unroll
;             for (int bj = 0; bj < 2; ++bj) { f32x4 v0 = acc[ai][bj][m][0] * rf, v1 = acc[ai][bj][m][1] * rf;
;                 if (act != 0) {
; #pragma unroll
;                     for (int e = 0; e < 4; ++e) { const float x0 = v0[e], x1 = v1[e];
;                         const float r0 = __builtin_amdgcn_rcpf(1.0f + __builtin_amdgcn_exp2f(x0 * (c0 + c1 * x0 * x0))), r1 = __builtin_amdgcn_rcpf(1.0f + __builtin_amdgcn_exp2f(x1 * (c0 + c1 * x1 * x1)));
;                         v0[e] = act == 1 ? x0 * r0 : r0; v1[e] = act == 1 ? x1 * r1 : r1; } }
;                 if (stat) {
; #pragma unroll
;                     for (int e = 0; e < 4; ++e) { ls1 += v0[e] + v1[e]; ls2 += v0[e] * v0[e] + v1[e] * v1[e]; } }
;                 *(u32x4*)(rowp + bj * HALF) = pack8(v0, v1); }
;             if (stat) { ls1 = xor_add<16>(ls1); ls1 = xor_add<32>(ls1); ls2 = xor_add<16>(ls2); ls2 = xor_add<32>(ls2);
;                 if (fq == 0) { f32x2 st2; st2.x = ls1; st2.y = ls2; *(f32x2*)(stat + (size_t)(row0 + ai * HALF + m * 16) * 16) = st2; } }
	v_add_f32_e32 v162, v162, v161
	v_add_f32_e32 v163, v163, v198
	v_mov_b32_e32 v199, v162
	v_mov_b32_e32 v200, v163
	s_nop 1
	v_permlane32_swap_b32_e32 v162, v199
	v_permlane32_swap_b32_e32 v163, v200
	s_and_b64 exec, exec, s[4:5]
	v_add_f32_e32 v162, v162, v199
	v_add_f32_e32 v163, v163, v200
	global_store_dwordx2 v135, v[162:163], s[38:39]
	s_mov_b64 exec, -1
	v_pk_mul_f32 v[140:141], v[32:33], v[32:33]
	v_pk_mul_f32 v[142:143], v[34:35], v[34:35]
	v_pk_mul_f32 v[144:145], v[28:29], v[28:29]
	v_pk_mul_f32 v[146:147], v[30:31], v[30:31]
	v_pk_mul_f32 v[148:149], v[24:25], v[24:25]
	v_pk_mul_f32 v[150:151], v[26:27], v[26:27]
	v_pk_mul_f32 v[152:153], v[20:21], v[20:21]
	v_pk_mul_f32 v[154:155], v[22:23], v[22:23]
	v_pk_fma_f32 v[140:141], v[140:141], v[196:197], v[188:189] op_sel:[0,0,0] op_sel_hi:[1,0,0]
	v_pk_fma_f32 v[142:143], v[142:143], v[196:197], v[188:189] op_sel:[0,0,0] op_sel_hi:[1,0,0]
	v_pk_fma_f32 v[144:145], v[144:145], v[196:197], v[188:189] op_sel:[0,0,0] op_sel_hi:[1,0,0]
	v_pk_fma_f32 v[146:147], v[146:147], v[196:197], v[188:189] op_sel:[0,0,0] op_sel_hi:[1,0,0]
	v_pk_fma_f32 v[148:149], v[148:149], v[196:197], v[188:189] op_sel:[0,0,0] op_sel_hi:[1,0,0]
	v_pk_fma_f32 v[150:151], v[150:151], v[196:197], v[188:189] op_sel:[0,0,0] op_sel_hi:[1,0,0]
	v_pk_fma_f32 v[152:153], v[152:153], v[196:197], v[188:189] op_sel:[0,0,0] op_sel_hi:[1,0,0]
	v_pk_fma_f32 v[154:155], v[154:155], v[196:197], v[188:189] op_sel:[0,0,0] op_sel_hi:[1,0,0]
	v_pk_mul_f32 v[140:141], v[32:33], v[140:141]
	v_pk_mul_f32 v[142:143], v[34:35], v[142:143]
	v_pk_mul_f32 v[144:145], v[28:29], v[144:145]
	v_pk_mul_f32 v[146:147], v[30:31], v[146:147]
	v_pk_mul_f32 v[148:149], v[24:25], v[148:149]
	v_pk_mul_f32 v[150:151], v[26:27], v[150:151]
	v_pk_mul_f32 v[152:153], v[20:21], v[152:153]
	v_pk_mul_f32 v[154:155], v[22:23], v[154:155]
	v_exp_f32_e32 v140, v140
	v_exp_f32_e32 v141, v141
	v_exp_f32_e32 v142, v142
	v_exp_f32_e32 v143, v143
	v_exp_f32_e32 v144, v144
	v_exp_f32_e32 v145, v145
	v_exp_f32_e32 v146, v146
	v_exp_f32_e32 v147, v147
	v_exp_f32_e32 v148, v148
	v_exp_f32_e32 v149, v149
	v_exp_f32_e32 v150, v150
	v_exp_f32_e32 v151, v151
	v_exp_f32_e32 v152, v152
	v_exp_f32_e32 v153, v153
	v_exp_f32_e32 v154, v154
	v_exp_f32_e32 v155, v155
	v_pk_fma_f32 v[140:141], v[140:141], v[214:215], v[214:215] op_sel:[0,0,0] op_sel_hi:[1,0,0]
	v_pk_fma_f32 v[142:143], v[142:143], v[214:215], v[214:215] op_sel:[0,0,0] op_sel_hi:[1,0,0]
	v_pk_fma_f32 v[144:145], v[144:145], v[214:215], v[214:215] op_sel:[0,0,0] op_sel_hi:[1,0,0]
	v_pk_fma_f32 v[146:147], v[146:147], v[214:215], v[214:215] op_sel:[0,0,0] op_sel_hi:[1,0,0]
	v_pk_fma_f32 v[148:149], v[148:149], v[214:215], v[214:215] op_sel:[0,0,0] op_sel_hi:[1,0,0]
	v_pk_fma_f32 v[150:151], v[150:151], v[214:215], v[214:215] op_sel:[0,0,0] op_sel_hi:[1,0,0]
	v_pk_fma_f32 v[152:153], v[152:153], v[214:215], v[214:215] op_sel:[0,0,0] op_sel_hi:[1,0,0]
	v_pk_fma_f32 v[154:155], v[154:155], v[214:215], v[214:215] op_sel:[0,0,0] op_sel_hi:[1,0,0]
	v_rcp_f32_e32 v140, v140
	v_rcp_f32_e32 v141, v141
	v_rcp_f32_e32 v142, v142
	v_rcp_f32_e32 v143, v143
	v_rcp_f32_e32 v144, v144
	v_rcp_f32_e32 v145, v145
	v_rcp_f32_e32 v146, v146
	v_rcp_f32_e32 v147, v147
	v_rcp_f32_e32 v148, v148
	v_rcp_f32_e32 v149, v149
	v_rcp_f32_e32 v150, v150
	v_rcp_f32_e32 v151, v151
	v_rcp_f32_e32 v152, v152
	v_rcp_f32_e32 v153, v153
	v_rcp_f32_e32 v154, v154
	v_rcp_f32_e32 v155, v155
	v_pk_mul_f32 v[32:33], v[32:33], v[140:141]
	v_pk_mul_f32 v[34:35], v[34:35], v[142:143]
	v_pk_mul_f32 v[28:29], v[28:29], v[144:145]
	v_pk_mul_f32 v[30:31], v[30:31], v[146:147]
	v_pk_mul_f32 v[24:25], v[24:25], v[148:149]
	v_pk_mul_f32 v[26:27], v[26:27], v[150:151]
	v_pk_mul_f32 v[20:21], v[20:21], v[152:153]
	v_pk_mul_f32 v[22:23], v[22:23], v[154:155]
	v_add_u32_e32 v134, 0x4000, v134
	v_add_u32_e32 v135, 0x400, v135
	v_pk_add_f32 v[216:217], v[32:33], v[34:35]
	v_pk_mul_f32 v[218:219], v[32:33], v[32:33]
	v_pk_fma_f32 v[218:219], v[34:35], v[34:35], v[218:219]
	v_pk_add_f32 v[216:217], v[216:217], v[28:29]
	v_pk_fma_f32 v[218:219], v[28:29], v[28:29], v[218:219]
	v_pk_add_f32 v[216:217], v[216:217], v[30:31]
	v_pk_fma_f32 v[218:219], v[30:31], v[30:31], v[218:219]
	v_pk_add_f32 v[216:217], v[216:217], v[24:25]
	v_pk_fma_f32 v[218:219], v[24:25], v[24:25], v[218:219]
	v_pk_add_f32 v[216:217], v[216:217], v[26:27]
	v_pk_fma_f32 v[218:219], v[26:27], v[26:27], v[218:219]
	v_pk_add_f32 v[216:217], v[216:217], v[20:21]
	v_pk_fma_f32 v[218:219], v[20:21], v[20:21], v[218:219]
	v_pk_add_f32 v[216:217], v[216:217], v[22:23]
	v_pk_fma_f32 v[218:219], v[22:23], v[22:23], v[218:219]
	v_add_f32_e32 v162, v216, v217
	v_add_f32_e32 v163, v218, v219
	ds_swizzle_b32 v161, v162 offset:swizzle(SWAP,16)
	ds_swizzle_b32 v198, v163 offset:swizzle(SWAP,16)
	v_cvt_pk_bf16_f32 v32, v32, v33
	v_cvt_pk_bf16_f32 v33, v34, v35
	v_cvt_pk_bf16_f32 v34, v28, v29
	v_cvt_pk_bf16_f32 v35, v30, v31
	global_store_dwordx4 v134, v[32:35], s[0:1]
	v_cvt_pk_bf16_f32 v24, v24, v25
	v_cvt_pk_bf16_f32 v25, v26, v27
	v_cvt_pk_bf16_f32 v26, v20, v21
	v_cvt_pk_bf16_f32 v27, v22, v23
	global_store_dwordx4 v134, v[24:27], s[0:1] offset:256
	s_waitcnt lgkmcnt(0)
; __device__ __forceinline__ u32x4 pack8(const f32x4 a, const f32x4 b) { u32x4 w; w.x = cvt_pk_bf16(a[0], a[1]); w.y = cvt_pk_bf16(a[2], a[3]); w.z = cvt_pk_bf16(b[0], b[1]); w.w = cvt_pk_bf16(b[2], b[3]); return w; }
; template <int O> __device__ __forceinline__ float xor_add(float v) {
;     if constexpr (O < 32) return v + __builtin_bit_cast(float, __builtin_amdgcn_ds_swizzle(__builtin_bit_cast(int, v), (O << 10) | 0x1f));
;     else { const auto rr = __builtin_amdgcn_permlane32_swap(__float_as_uint(v), __float_as_uint(v), false, false); return __uint_as_float(rr[0]) + __uint_as_float(rr[1]); }
;     ...
;         for (int m = 0; m < 4; ++m) { bf16_t* rowp = base + (size_t)(row0 + ai * HALF + m * 16) * ldc + col0; float ls1 = 0.f, ls2 = 0.f; const float rf = rsr[ai * HALF + m * 16];
; #pragma unroll
;             for (int bj = 0; bj < 2; ++bj) { f32x4 v0 = acc[ai][bj][m][0] * rf, v1 = acc[ai][bj][m][1] * rf;
;                 if (act != 0) {
; #pragma unroll
;                     for (int e = 0; e < 4; ++e) { const float x0 = v0[e], x1 = v1[e];
;                         const float r0 = __builtin_amdgcn_rcpf(1.0f + __builtin_amdgcn_exp2f(x0 * (c0 + c1 * x0 * x0))), r1 = __builtin_amdgcn_rcpf(1.0f + __builtin_amdgcn_exp2f(x1 * (c0 + c1 * x1 * x1)));
;                         v0[e] = act == 1 ? x0 * r0 : r0; v1[e] = act == 1 ? x1 * r1 : r1; } }
;                 if (stat) {
; #pragma unroll
;                     for (int e = 0; e < 4; ++e) { ls1 += v0[e] + v1[e]; ls2 += v0[e] * v0[e] + v1[e] * v1[e]; } }
;                 *(u32x4*)(rowp + bj * HALF) = pack8(v0, v1); }
;             if (stat) { ls1 = xor_add<16>(ls1); ls1 = xor_add<32>(ls1); ls2 = xor_add<16>(ls2); ls2 = xor_add<32>(ls2);
;                 if (fq == 0) { f32x2 st2; st2.x = ls1; st2.y = ls2; *(f32x2*)(stat + (size_t)(row0 + ai * HALF + m * 16) * 16) = st2; } }
	v_add_f32_e32 v162, v162, v161
	v_add_f32_e32 v163, v163, v198
	v_mov_b32_e32 v199, v162
	v_mov_b32_e32 v200, v163
	s_nop 1
	v_permlane32_swap_b32_e32 v162, v199
	v_permlane32_swap_b32_e32 v163, v200
	s_and_b64 exec, exec, s[4:5]
	v_add_f32_e32 v162, v162, v199
	v_add_f32_e32 v163, v163, v200
	global_store_dwordx2 v135, v[162:163], s[38:39]
	s_mov_b64 exec, -1
	v_pk_mul_f32 v[140:141], v[16:17], v[16:17]
	v_pk_mul_f32 v[142:143], v[18:19], v[18:19]
	v_pk_mul_f32 v[144:145], v[12:13], v[12:13]
	v_pk_mul_f32 v[146:147], v[14:15], v[14:15]
	v_pk_mul_f32 v[148:149], v[8:9], v[8:9]
	v_pk_mul_f32 v[150:151], v[10:11], v[10:11]
	v_pk_mul_f32 v[152:153], v[4:5], v[4:5]
	v_pk_mul_f32 v[154:155], v[6:7], v[6:7]
	v_pk_fma_f32 v[140:141], v[140:141], v[196:197], v[188:189] op_sel:[0,1,1] op_sel_hi:[1,1,1]
	v_pk_fma_f32 v[142:143], v[142:143], v[196:197], v[188:189] op_sel:[0,1,1] op_sel_hi:[1,1,1]
	v_pk_fma_f32 v[144:145], v[144:145], v[196:197], v[188:189] op_sel:[0,1,1] op_sel_hi:[1,1,1]
	v_pk_fma_f32 v[146:147], v[146:147], v[196:197], v[188:189] op_sel:[0,1,1] op_sel_hi:[1,1,1]
	v_pk_fma_f32 v[148:149], v[148:149], v[196:197], v[188:189] op_sel:[0,1,1] op_sel_hi:[1,1,1]
	v_pk_fma_f32 v[150:151], v[150:151], v[196:197], v[188:189] op_sel:[0,1,1] op_sel_hi:[1,1,1]
	v_pk_fma_f32 v[152:153], v[152:153], v[196:197], v[188:189] op_sel:[0,1,1] op_sel_hi:[1,1,1]
	v_pk_fma_f32 v[154:155], v[154:155], v[196:197], v[188:189] op_sel:[0,1,1] op_sel_hi:[1,1,1]
	v_pk_mul_f32 v[140:141], v[16:17], v[140:141]
	v_pk_mul_f32 v[142:143], v[18:19], v[142:143]
	v_pk_mul_f32 v[144:145], v[12:13], v[144:145]
	v_pk_mul_f32 v[146:147], v[14:15], v[146:147]
	v_pk_mul_f32 v[148:149], v[8:9], v[148:149]
	v_pk_mul_f32 v[150:151], v[10:11], v[150:151]
	v_pk_mul_f32 v[152:153], v[4:5], v[152:153]
	v_pk_mul_f32 v[154:155], v[6:7], v[154:155]
	v_exp_f32_e32 v140, v140
	v_exp_f32_e32 v141, v141
	v_exp_f32_e32 v142, v142
	v_exp_f32_e32 v143, v143
	v_exp_f32_e32 v144, v144
	v_exp_f32_e32 v145, v145
	v_exp_f32_e32 v146, v146
	v_exp_f32_e32 v147, v147
	v_exp_f32_e32 v148, v148
	v_exp_f32_e32 v149, v149
	v_exp_f32_e32 v150, v150
	v_exp_f32_e32 v151, v151
	v_exp_f32_e32 v152, v152
	v_exp_f32_e32 v153, v153
	v_exp_f32_e32 v154, v154
	v_exp_f32_e32 v155, v155
	v_pk_fma_f32 v[140:141], v[140:141], v[214:215], v[214:215] op_sel:[0,1,1] op_sel_hi:[1,1,1]
	v_pk_fma_f32 v[142:143], v[142:143], v[214:215], v[214:215] op_sel:[0,1,1] op_sel_hi:[1,1,1]
	v_pk_fma_f32 v[144:145], v[144:145], v[214:215], v[214:215] op_sel:[0,1,1] op_sel_hi:[1,1,1]
	v_pk_fma_f32 v[146:147], v[146:147], v[214:215], v[214:215] op_sel:[0,1,1] op_sel_hi:[1,1,1]
	v_pk_fma_f32 v[148:149], v[148:149], v[214:215], v[214:215] op_sel:[0,1,1] op_sel_hi:[1,1,1]
	v_pk_fma_f32 v[150:151], v[150:151], v[214:215], v[214:215] op_sel:[0,1,1] op_sel_hi:[1,1,1]
	v_pk_fma_f32 v[152:153], v[152:153], v[214:215], v[214:215] op_sel:[0,1,1] op_sel_hi:[1,1,1]
	v_pk_fma_f32 v[154:155], v[154:155], v[214:215], v[214:215] op_sel:[0,1,1] op_sel_hi:[1,1,1]
	v_rcp_f32_e32 v140, v140
	v_rcp_f32_e32 v141, v141
	v_rcp_f32_e32 v142, v142
	v_rcp_f32_e32 v143, v143
	v_rcp_f32_e32 v144, v144
	v_rcp_f32_e32 v145, v145
	v_rcp_f32_e32 v146, v146
	v_rcp_f32_e32 v147, v147
	v_rcp_f32_e32 v148, v148
	v_rcp_f32_e32 v149, v149
	v_rcp_f32_e32 v150, v150
	v_rcp_f32_e32 v151, v151
	v_rcp_f32_e32 v152, v152
	v_rcp_f32_e32 v153, v153
	v_rcp_f32_e32 v154, v154
	v_rcp_f32_e32 v155, v155
	v_pk_mul_f32 v[16:17], v[16:17], v[140:141]
	v_pk_mul_f32 v[18:19], v[18:19], v[142:143]
	v_pk_mul_f32 v[12:13], v[12:13], v[144:145]
	v_pk_mul_f32 v[14:15], v[14:15], v[146:147]
	v_pk_mul_f32 v[8:9], v[8:9], v[148:149]
	v_pk_mul_f32 v[10:11], v[10:11], v[150:151]
	v_pk_mul_f32 v[4:5], v[4:5], v[152:153]
	v_pk_mul_f32 v[6:7], v[6:7], v[154:155]
	v_add_u32_e32 v134, 0x4000, v134
	v_add_u32_e32 v135, 0x400, v135
	v_pk_add_f32 v[216:217], v[16:17], v[18:19]
	v_pk_mul_f32 v[218:219], v[16:17], v[16:17]
	v_pk_fma_f32 v[218:219], v[18:19], v[18:19], v[218:219]
	v_pk_add_f32 v[216:217], v[216:217], v[12:13]
	v_pk_fma_f32 v[218:219], v[12:13], v[12:13], v[218:219]
	v_pk_add_f32 v[216:217], v[216:217], v[14:15]
	v_pk_fma_f32 v[218:219], v[14:15], v[14:15], v[218:219]
	v_pk_add_f32 v[216:217], v[216:217], v[8:9]
	v_pk_fma_f32 v[218:219], v[8:9], v[8:9], v[218:219]
	v_pk_add_f32 v[216:217], v[216:217], v[10:11]
	v_pk_fma_f32 v[218:219], v[10:11], v[10:11], v[218:219]
	v_pk_add_f32 v[216:217], v[216:217], v[4:5]
	v_pk_fma_f32 v[218:219], v[4:5], v[4:5], v[218:219]
	v_pk_add_f32 v[216:217], v[216:217], v[6:7]
	v_pk_fma_f32 v[218:219], v[6:7], v[6:7], v[218:219]
	v_add_f32_e32 v162, v216, v217
	v_add_f32_e32 v163, v218, v219
	ds_swizzle_b32 v161, v162 offset:swizzle(SWAP,16)
	ds_swizzle_b32 v198, v163 offset:swizzle(SWAP,16)
	v_cvt_pk_bf16_f32 v16, v16, v17
	v_cvt_pk_bf16_f32 v17, v18, v19
	v_cvt_pk_bf16_f32 v18, v12, v13
	v_cvt_pk_bf16_f32 v19, v14, v15
	global_store_dwordx4 v134, v[16:19], s[0:1]
	v_cvt_pk_bf16_f32 v8, v8, v9
	v_cvt_pk_bf16_f32 v9, v10, v11
	v_cvt_pk_bf16_f32 v10, v4, v5
	v_cvt_pk_bf16_f32 v11, v6, v7
	global_store_dwordx4 v134, v[8:11], s[0:1] offset:256
	s_waitcnt lgkmcnt(0)
	v_add_f32_e32 v162, v162, v161
	v_add_f32_e32 v163, v163, v198
	v_mov_b32_e32 v199, v162
	v_mov_b32_e32 v200, v163
	s_nop 1
	v_permlane32_swap_b32_e32 v162, v199
	v_permlane32_swap_b32_e32 v163, v200
	s_and_b64 exec, exec, s[4:5]
	v_add_f32_e32 v162, v162, v199
	v_add_f32_e32 v163, v163, v200
	global_store_dwordx2 v135, v[162:163], s[38:39]
	s_mov_b64 exec, -1
	s_branch .Lt8_end

; #define PG8_LAS __attribute__((address_space(3)))
; __device__ __forceinline__ unsigned cvt_pk_bf16(float lo, float hi) { unsigned r; asm volatile("v_cvt_pk_bf16_f32 %0, %1, %2" : "=v"(r) : "v"(lo), "v"(hi)); return r; }
; __device__ __forceinline__ float sigm(float x) { return __builtin_amdgcn_rcpf(1.0f + __builtin_amdgcn_exp2f(-1.4426950408889634f * x)); }
; __device__ __forceinline__ float gelu_t(float x) { const float z = x * (-2.302208198f - 0.10294324f * x * x); return x * __builtin_amdgcn_rcpf(1.0f + __builtin_amdgcn_exp2f(z)); }
; __device__ __forceinline__ u32x4 pack8(const f32x4 a, const f32x4 b) { u32x4 w; w.x = cvt_pk_bf16(a[0], a[1]); w.y = cvt_pk_bf16(a[2], a[3]); w.z = cvt_pk_bf16(b[0], b[1]); w.w = cvt_pk_bf16(b[2], b[3]); return w; }
;     __device__ __forceinline__ void operator()(const f32x4 (&acc)[2][2][4][2], const Unit& u, int wr, int wc, int fr, int fq) const {
;         const int rl0 = wr * 64 + fr + (u.half == 2 ? HALF : 0), row0 = u.pm * BM + rl0, col0 = u.pn * HALF + wc * 32 + 8 * fq; const PG8_LAS float* rsr = rsl + rl0;
; #pragma unroll
;         for (int ai = 0; ai < 2; ++ai) { if (ai == 1 && u.half != 0) break;
; #pragma unroll
;             for (int m = 0; m < 4; ++m) { const float rf = rsr[ai * HALF + m * 16]; f32x4 v0 = acc[ai][0][m][0] * rf, v1 = acc[ai][0][m][1] * rf; const f32x4 u0 = acc[ai][1][m][0] * rf, u1 = acc[ai][1][m][1] * rf;
; #pragma unroll
;                 for (int e = 0; e < 4; ++e) { v0[e] = v0[e] * sigm(v0[e]) * u0[e]; v1[e] = v1[e] * sigm(v1[e]) * u1[e]; }
;                 *(u32x4*)(H + (size_t)(row0 + ai * HALF + m * 16) * DFF + col0) = pack8(v0, v1); } }
.LBB0_1480:
	ds_read_b32 v236, v148
	ds_read_b32 v237, v148 offset:64
	ds_read_b32 v238, v148 offset:128
	ds_read_b32 v239, v148 offset:192
	ds_read_b32 v240, v148 offset:512
	ds_read_b32 v241, v148 offset:576
	ds_read_b32 v242, v148 offset:640
	ds_read_b32 v243, v148 offset:704
	v_lshl_or_b32 v252, s20, 7, v149
	v_lshl_add_u32 v253, s14, 8, v146
	v_lshlrev_b32_e32 v252, 1, v252
	v_mad_u32_u24 v252, v253, s2, v252
	s_mov_b32 s0, 0xbfb8aa3b
	s_waitcnt lgkmcnt(0)
	v_pk_mul_f32 v[244:245], v[236:237], s[0:1] op_sel_hi:[1,0]
	v_pk_mul_f32 v[246:247], v[238:239], s[0:1] op_sel_hi:[1,0]
	v_pk_mul_f32 v[248:249], v[240:241], s[0:1] op_sel_hi:[1,0]
	v_pk_mul_f32 v[250:251], v[242:243], s[0:1] op_sel_hi:[1,0]
	v_pk_mul_f32 v[236:237], v[236:237], v[236:237]
	v_pk_mul_f32 v[238:239], v[238:239], v[238:239]
	v_pk_mul_f32 v[240:241], v[240:241], v[240:241]
	v_pk_mul_f32 v[242:243], v[242:243], v[242:243]
	v_rcp_f32_e32 v236, v236
	v_rcp_f32_e32 v237, v237
	v_rcp_f32_e32 v238, v238
	v_rcp_f32_e32 v239, v239
	v_rcp_f32_e32 v240, v240
	v_rcp_f32_e32 v241, v241
	v_rcp_f32_e32 v242, v242
	v_rcp_f32_e32 v243, v243
	v_pk_mul_f32 v[228:229], v[128:129], v[244:245] op_sel:[0,0] op_sel_hi:[1,0]
	v_pk_mul_f32 v[230:231], v[130:131], v[244:245] op_sel:[0,0] op_sel_hi:[1,0]
	v_pk_mul_f32 v[232:233], v[124:125], v[244:245] op_sel:[0,0] op_sel_hi:[1,0]
	v_pk_mul_f32 v[234:235], v[126:127], v[244:245] op_sel:[0,0] op_sel_hi:[1,0]
	v_exp_f32_e32 v228, v228
	v_exp_f32_e32 v229, v229
	v_exp_f32_e32 v230, v230
	v_exp_f32_e32 v231, v231
	v_exp_f32_e32 v232, v232
	v_exp_f32_e32 v233, v233
	v_exp_f32_e32 v234, v234
	v_exp_f32_e32 v235, v235
	v_pk_fma_f32 v[228:229], v[228:229], v[236:237], v[236:237] op_sel:[0,0,0] op_sel_hi:[1,0,0]
	v_pk_fma_f32 v[230:231], v[230:231], v[236:237], v[236:237] op_sel:[0,0,0] op_sel_hi:[1,0,0]
	v_pk_fma_f32 v[232:233], v[232:233], v[236:237], v[236:237] op_sel:[0,0,0] op_sel_hi:[1,0,0]
	v_pk_fma_f32 v[234:235], v[234:235], v[236:237], v[236:237] op_sel:[0,0,0] op_sel_hi:[1,0,0]
	v_rcp_f32_e32 v228, v228
	v_rcp_f32_e32 v229, v229
	v_rcp_f32_e32 v230, v230
	v_rcp_f32_e32 v231, v231
	v_rcp_f32_e32 v232, v232
	v_rcp_f32_e32 v233, v233
	v_rcp_f32_e32 v234, v234
	v_rcp_f32_e32 v235, v235
	v_pk_mul_f32 v[120:121], v[128:129], v[120:121]
	v_pk_mul_f32 v[122:123], v[130:131], v[122:123]
	v_pk_mul_f32 v[116:117], v[124:125], v[116:117]
	v_pk_mul_f32 v[118:119], v[126:127], v[118:119]
	v_pk_mul_f32 v[128:129], v[120:121], v[228:229]
	v_pk_mul_f32 v[130:131], v[122:123], v[230:231]
	v_pk_mul_f32 v[124:125], v[116:117], v[232:233]
	v_pk_mul_f32 v[126:127], v[118:119], v[234:235]
	v_cvt_pk_bf16_f32 v128, v128, v129
	v_cvt_pk_bf16_f32 v129, v130, v131
	v_cvt_pk_bf16_f32 v130, v124, v125
	v_cvt_pk_bf16_f32 v131, v126, v127
	global_store_dwordx4 v252, v[128:131], s[4:5]
	v_pk_mul_f32 v[228:229], v[112:113], v[244:245] op_sel:[0,1] op_sel_hi:[1,1]
	v_pk_mul_f32 v[230:231], v[114:115], v[244:245] op_sel:[0,1] op_sel_hi:[1,1]
	v_pk_mul_f32 v[232:233], v[108:109], v[244:245] op_sel:[0,1] op_sel_hi:[1,1]
	v_pk_mul_f32 v[234:235], v[110:111], v[244:245] op_sel:[0,1] op_sel_hi:[1,1]
	v_exp_f32_e32 v228, v228
	v_exp_f32_e32 v229, v229
	v_exp_f32_e32 v230, v230
	v_exp_f32_e32 v231, v231
	v_exp_f32_e32 v232, v232
	v_exp_f32_e32 v233, v233
	v_exp_f32_e32 v234, v234
	v_exp_f32_e32 v235, v235
	v_pk_fma_f32 v[228:229], v[228:229], v[236:237], v[236:237] op_sel:[0,1,1] op_sel_hi:[1,1,1]
	v_pk_fma_f32 v[230:231], v[230:231], v[236:237], v[236:237] op_sel:[0,1,1] op_sel_hi:[1,1,1]
	v_pk_fma_f32 v[232:233], v[232:233], v[236:237], v[236:237] op_sel:[0,1,1] op_sel_hi:[1,1,1]
	v_pk_fma_f32 v[234:235], v[234:235], v[236:237], v[236:237] op_sel:[0,1,1] op_sel_hi:[1,1,1]
	v_rcp_f32_e32 v228, v228
	v_rcp_f32_e32 v229, v229
	v_rcp_f32_e32 v230, v230
	v_rcp_f32_e32 v231, v231
	v_rcp_f32_e32 v232, v232
	v_rcp_f32_e32 v233, v233
	v_rcp_f32_e32 v234, v234
	v_rcp_f32_e32 v235, v235
	v_pk_mul_f32 v[104:105], v[112:113], v[104:105]
	v_pk_mul_f32 v[106:107], v[114:115], v[106:107]
	v_pk_mul_f32 v[100:101], v[108:109], v[100:101]
	v_pk_mul_f32 v[102:103], v[110:111], v[102:103]
	v_add_u32_e32 v252, 0x16000, v252
	v_pk_mul_f32 v[112:113], v[104:105], v[228:229]
	v_pk_mul_f32 v[114:115], v[106:107], v[230:231]
	v_pk_mul_f32 v[108:109], v[100:101], v[232:233]
	v_pk_mul_f32 v[110:111], v[102:103], v[234:235]
	v_cvt_pk_bf16_f32 v104, v112, v113
	v_cvt_pk_bf16_f32 v105, v114, v115
	v_cvt_pk_bf16_f32 v106, v108, v109
	v_cvt_pk_bf16_f32 v107, v110, v111
	global_store_dwordx4 v252, v[104:107], s[4:5]
	v_pk_mul_f32 v[228:229], v[96:97], v[246:247] op_sel:[0,0] op_sel_hi:[1,0]
	v_pk_mul_f32 v[230:231], v[98:99], v[246:247] op_sel:[0,0] op_sel_hi:[1,0]
	v_pk_mul_f32 v[232:233], v[92:93], v[246:247] op_sel:[0,0] op_sel_hi:[1,0]
	v_pk_mul_f32 v[234:235], v[94:95], v[246:247] op_sel:[0,0] op_sel_hi:[1,0]
	v_exp_f32_e32 v228, v228
	v_exp_f32_e32 v229, v229
	v_exp_f32_e32 v230, v230
	v_exp_f32_e32 v231, v231
	v_exp_f32_e32 v232, v232
	v_exp_f32_e32 v233, v233
	v_exp_f32_e32 v234, v234
	v_exp_f32_e32 v235, v235
	v_pk_fma_f32 v[228:229], v[228:229], v[238:239], v[238:239] op_sel:[0,0,0] op_sel_hi:[1,0,0]
	v_pk_fma_f32 v[230:231], v[230:231], v[238:239], v[238:239] op_sel:[0,0,0] op_sel_hi:[1,0,0]
	v_pk_fma_f32 v[232:233], v[232:233], v[238:239], v[238:239] op_sel:[0,0,0] op_sel_hi:[1,0,0]
	v_pk_fma_f32 v[234:235], v[234:235], v[238:239], v[238:239] op_sel:[0,0,0] op_sel_hi:[1,0,0]
	v_rcp_f32_e32 v228, v228
	v_rcp_f32_e32 v229, v229
	v_rcp_f32_e32 v230, v230
	v_rcp_f32_e32 v231, v231
	v_rcp_f32_e32 v232, v232
	v_rcp_f32_e32 v233, v233
	v_rcp_f32_e32 v234, v234
	v_rcp_f32_e32 v235, v235
; #define PG8_LAS __attribute__((address_space(3)))
; __device__ __forceinline__ unsigned cvt_pk_bf16(float lo, float hi) { unsigned r; asm volatile("v_cvt_pk_bf16_f32 %0, %1, %2" : "=v"(r) : "v"(lo), "v"(hi)); return r; }
; __device__ __forceinline__ float sigm(float x) { return __builtin_amdgcn_rcpf(1.0f + __builtin_amdgcn_exp2f(-1.4426950408889634f * x)); }
; __device__ __forceinline__ float gelu_t(float x) { const float z = x * (-2.302208198f - 0.10294324f * x * x); return x * __builtin_amdgcn_rcpf(1.0f + __builtin_amdgcn_exp2f(z)); }
; __device__ __forceinline__ u32x4 pack8(const f32x4 a, const f32x4 b) { u32x4 w; w.x = cvt_pk_bf16(a[0], a[1]); w.y = cvt_pk_bf16(a[2], a[3]); w.z = cvt_pk_bf16(b[0], b[1]); w.w = cvt_pk_bf16(b[2], b[3]); return w; }
;     __device__ __forceinline__ void operator()(const f32x4 (&acc)[2][2][4][2], const Unit& u, int wr, int wc, int fr, int fq) const {
;         const int rl0 = wr * 64 + fr + (u.half == 2 ? HALF : 0), row0 = u.pm * BM + rl0, col0 = u.pn * HALF + wc * 32 + 8 * fq; const PG8_LAS float* rsr = rsl + rl0;
; #pragma unroll
;         for (int ai = 0; ai < 2; ++ai) { if (ai == 1 && u.half != 0) break;
; #pragma unroll
;             for (int m = 0; m < 4; ++m) { const float rf = rsr[ai * HALF + m * 16]; f32x4 v0 = acc[ai][0][m][0] * rf, v1 = acc[ai][0][m][1] * rf; const f32x4 u0 = acc[ai][1][m][0] * rf, u1 = acc[ai][1][m][1] * rf;
; #pragma unroll
;                 for (int e = 0; e < 4; ++e) { v0[e] = v0[e] * sigm(v0[e]) * u0[e]; v1[e] = v1[e] * sigm(v1[e]) * u1[e]; }
;                 *(u32x4*)(H + (size_t)(row0 + ai * HALF + m * 16) * DFF + col0) = pack8(v0, v1); } }
	v_pk_mul_f32 v[88:89], v[96:97], v[88:89]
	v_pk_mul_f32 v[90:91], v[98:99], v[90:91]
	v_pk_mul_f32 v[84:85], v[92:93], v[84:85]
	v_pk_mul_f32 v[86:87], v[94:95], v[86:87]
	v_add_u32_e32 v252, 0x16000, v252
	v_pk_mul_f32 v[96:97], v[88:89], v[228:229]
	v_pk_mul_f32 v[98:99], v[90:91], v[230:231]
	v_pk_mul_f32 v[92:93], v[84:85], v[232:233]
	v_pk_mul_f32 v[94:95], v[86:87], v[234:235]
	v_cvt_pk_bf16_f32 v96, v96, v97
	v_cvt_pk_bf16_f32 v97, v98, v99
	v_cvt_pk_bf16_f32 v98, v92, v93
	v_cvt_pk_bf16_f32 v99, v94, v95
	global_store_dwordx4 v252, v[96:99], s[4:5]
	v_pk_mul_f32 v[228:229], v[80:81], v[246:247] op_sel:[0,1] op_sel_hi:[1,1]
	v_pk_mul_f32 v[230:231], v[82:83], v[246:247] op_sel:[0,1] op_sel_hi:[1,1]
	v_pk_mul_f32 v[232:233], v[76:77], v[246:247] op_sel:[0,1] op_sel_hi:[1,1]
	v_pk_mul_f32 v[234:235], v[78:79], v[246:247] op_sel:[0,1] op_sel_hi:[1,1]
	v_exp_f32_e32 v228, v228
	v_exp_f32_e32 v229, v229
	v_exp_f32_e32 v230, v230
	v_exp_f32_e32 v231, v231
	v_exp_f32_e32 v232, v232
	v_exp_f32_e32 v233, v233
	v_exp_f32_e32 v234, v234
	v_exp_f32_e32 v235, v235
	v_pk_fma_f32 v[228:229], v[228:229], v[238:239], v[238:239] op_sel:[0,1,1] op_sel_hi:[1,1,1]
	v_pk_fma_f32 v[230:231], v[230:231], v[238:239], v[238:239] op_sel:[0,1,1] op_sel_hi:[1,1,1]
	v_pk_fma_f32 v[232:233], v[232:233], v[238:239], v[238:239] op_sel:[0,1,1] op_sel_hi:[1,1,1]
	v_pk_fma_f32 v[234:235], v[234:235], v[238:239], v[238:239] op_sel:[0,1,1] op_sel_hi:[1,1,1]
	v_rcp_f32_e32 v228, v228
	v_rcp_f32_e32 v229, v229
	v_rcp_f32_e32 v230, v230
	v_rcp_f32_e32 v231, v231
	v_rcp_f32_e32 v232, v232
	v_rcp_f32_e32 v233, v233
	v_rcp_f32_e32 v234, v234
	v_rcp_f32_e32 v235, v235
	v_pk_mul_f32 v[72:73], v[80:81], v[72:73]
	v_pk_mul_f32 v[74:75], v[82:83], v[74:75]
	v_pk_mul_f32 v[68:69], v[76:77], v[68:69]
	v_pk_mul_f32 v[70:71], v[78:79], v[70:71]
	v_add_u32_e32 v252, 0x16000, v252
	v_pk_mul_f32 v[80:81], v[72:73], v[228:229]
	v_pk_mul_f32 v[82:83], v[74:75], v[230:231]
	v_pk_mul_f32 v[76:77], v[68:69], v[232:233]
	v_pk_mul_f32 v[78:79], v[70:71], v[234:235]
	v_cvt_pk_bf16_f32 v72, v80, v81
	v_cvt_pk_bf16_f32 v73, v82, v83
	v_cvt_pk_bf16_f32 v74, v76, v77
	v_cvt_pk_bf16_f32 v75, v78, v79
	global_store_dwordx4 v252, v[72:75], s[4:5]
	v_pk_mul_f32 v[228:229], v[64:65], v[248:249] op_sel:[0,0] op_sel_hi:[1,0]
	v_pk_mul_f32 v[230:231], v[66:67], v[248:249] op_sel:[0,0] op_sel_hi:[1,0]
	v_pk_mul_f32 v[232:233], v[60:61], v[248:249] op_sel:[0,0] op_sel_hi:[1,0]
	v_pk_mul_f32 v[234:235], v[62:63], v[248:249] op_sel:[0,0] op_sel_hi:[1,0]
	v_exp_f32_e32 v228, v228
	v_exp_f32_e32 v229, v229
	v_exp_f32_e32 v230, v230
	v_exp_f32_e32 v231, v231
	v_exp_f32_e32 v232, v232
	v_exp_f32_e32 v233, v233
	v_exp_f32_e32 v234, v234
	v_exp_f32_e32 v235, v235
	v_pk_fma_f32 v[228:229], v[228:229], v[240:241], v[240:241] op_sel:[0,0,0] op_sel_hi:[1,0,0]
	v_pk_fma_f32 v[230:231], v[230:231], v[240:241], v[240:241] op_sel:[0,0,0] op_sel_hi:[1,0,0]
	v_pk_fma_f32 v[232:233], v[232:233], v[240:241], v[240:241] op_sel:[0,0,0] op_sel_hi:[1,0,0]
	v_pk_fma_f32 v[234:235], v[234:235], v[240:241], v[240:241] op_sel:[0,0,0] op_sel_hi:[1,0,0]
	v_rcp_f32_e32 v228, v228
	v_rcp_f32_e32 v229, v229
	v_rcp_f32_e32 v230, v230
	v_rcp_f32_e32 v231, v231
	v_rcp_f32_e32 v232, v232
	v_rcp_f32_e32 v233, v233
	v_rcp_f32_e32 v234, v234
	v_rcp_f32_e32 v235, v235
	v_pk_mul_f32 v[56:57], v[64:65], v[56:57]
	v_pk_mul_f32 v[58:59], v[66:67], v[58:59]
	v_pk_mul_f32 v[52:53], v[60:61], v[52:53]
	v_pk_mul_f32 v[54:55], v[62:63], v[54:55]
	v_add_u32_e32 v252, 0x6e000, v252
	v_pk_mul_f32 v[64:65], v[56:57], v[228:229]
	v_pk_mul_f32 v[66:67], v[58:59], v[230:231]
	v_pk_mul_f32 v[60:61], v[52:53], v[232:233]
	v_pk_mul_f32 v[62:63], v[54:55], v[234:235]
	v_cvt_pk_bf16_f32 v64, v64, v65
	v_cvt_pk_bf16_f32 v65, v66, v67
	v_cvt_pk_bf16_f32 v66, v60, v61
	v_cvt_pk_bf16_f32 v67, v62, v63
	global_store_dwordx4 v252, v[64:67], s[4:5]
	v_pk_mul_f32 v[228:229], v[48:49], v[248:249] op_sel:[0,1] op_sel_hi:[1,1]
	v_pk_mul_f32 v[230:231], v[50:51], v[248:249] op_sel:[0,1] op_sel_hi:[1,1]
	v_pk_mul_f32 v[232:233], v[44:45], v[248:249] op_sel:[0,1] op_sel_hi:[1,1]
	v_pk_mul_f32 v[234:235], v[46:47], v[248:249] op_sel:[0,1] op_sel_hi:[1,1]
	v_exp_f32_e32 v228, v228
	v_exp_f32_e32 v229, v229
	v_exp_f32_e32 v230, v230
	v_exp_f32_e32 v231, v231
	v_exp_f32_e32 v232, v232
	v_exp_f32_e32 v233, v233
	v_exp_f32_e32 v234, v234
	v_exp_f32_e32 v235, v235
	v_pk_fma_f32 v[228:229], v[228:229], v[240:241], v[240:241] op_sel:[0,1,1] op_sel_hi:[1,1,1]
; #define PG8_LAS __attribute__((address_space(3)))
; __device__ __forceinline__ unsigned cvt_pk_bf16(float lo, float hi) { unsigned r; asm volatile("v_cvt_pk_bf16_f32 %0, %1, %2" : "=v"(r) : "v"(lo), "v"(hi)); return r; }
; __device__ __forceinline__ float sigm(float x) { return __builtin_amdgcn_rcpf(1.0f + __builtin_amdgcn_exp2f(-1.4426950408889634f * x)); }
; __device__ __forceinline__ float gelu_t(float x) { const float z = x * (-2.302208198f - 0.10294324f * x * x); return x * __builtin_amdgcn_rcpf(1.0f + __builtin_amdgcn_exp2f(z)); }
; __device__ __forceinline__ u32x4 pack8(const f32x4 a, const f32x4 b) { u32x4 w; w.x = cvt_pk_bf16(a[0], a[1]); w.y = cvt_pk_bf16(a[2], a[3]); w.z = cvt_pk_bf16(b[0], b[1]); w.w = cvt_pk_bf16(b[2], b[3]); return w; }
;     __device__ __forceinline__ void operator()(const f32x4 (&acc)[2][2][4][2], const Unit& u, int wr, int wc, int fr, int fq) const {
;         const int rl0 = wr * 64 + fr + (u.half == 2 ? HALF : 0), row0 = u.pm * BM + rl0, col0 = u.pn * HALF + wc * 32 + 8 * fq; const PG8_LAS float* rsr = rsl + rl0;
; #pragma unroll
;         for (int ai = 0; ai < 2; ++ai) { if (ai == 1 && u.half != 0) break;
; #pragma unroll
;             for (int m = 0; m < 4; ++m) { const float rf = rsr[ai * HALF + m * 16]; f32x4 v0 = acc[ai][0][m][0] * rf, v1 = acc[ai][0][m][1] * rf; const f32x4 u0 = acc[ai][1][m][0] * rf, u1 = acc[ai][1][m][1] * rf;
; #pragma unroll
;                 for (int e = 0; e < 4; ++e) { v0[e] = v0[e] * sigm(v0[e]) * u0[e]; v1[e] = v1[e] * sigm(v1[e]) * u1[e]; }
;                 *(u32x4*)(H + (size_t)(row0 + ai * HALF + m * 16) * DFF + col0) = pack8(v0, v1); } }
	v_pk_fma_f32 v[230:231], v[230:231], v[240:241], v[240:241] op_sel:[0,1,1] op_sel_hi:[1,1,1]
	v_pk_fma_f32 v[232:233], v[232:233], v[240:241], v[240:241] op_sel:[0,1,1] op_sel_hi:[1,1,1]
	v_pk_fma_f32 v[234:235], v[234:235], v[240:241], v[240:241] op_sel:[0,1,1] op_sel_hi:[1,1,1]
	v_rcp_f32_e32 v228, v228
	v_rcp_f32_e32 v229, v229
	v_rcp_f32_e32 v230, v230
	v_rcp_f32_e32 v231, v231
	v_rcp_f32_e32 v232, v232
	v_rcp_f32_e32 v233, v233
	v_rcp_f32_e32 v234, v234
	v_rcp_f32_e32 v235, v235
	v_pk_mul_f32 v[40:41], v[48:49], v[40:41]
	v_pk_mul_f32 v[42:43], v[50:51], v[42:43]
	v_pk_mul_f32 v[36:37], v[44:45], v[36:37]
	v_pk_mul_f32 v[38:39], v[46:47], v[38:39]
	v_add_u32_e32 v252, 0x16000, v252
	v_pk_mul_f32 v[48:49], v[40:41], v[228:229]
	v_pk_mul_f32 v[50:51], v[42:43], v[230:231]
	v_pk_mul_f32 v[44:45], v[36:37], v[232:233]
	v_pk_mul_f32 v[46:47], v[38:39], v[234:235]
	v_cvt_pk_bf16_f32 v40, v48, v49
	v_cvt_pk_bf16_f32 v41, v50, v51
	v_cvt_pk_bf16_f32 v42, v44, v45
	v_cvt_pk_bf16_f32 v43, v46, v47
	global_store_dwordx4 v252, v[40:43], s[4:5]
	v_pk_mul_f32 v[228:229], v[32:33], v[250:251] op_sel:[0,0] op_sel_hi:[1,0]
	v_pk_mul_f32 v[230:231], v[34:35], v[250:251] op_sel:[0,0] op_sel_hi:[1,0]
	v_pk_mul_f32 v[232:233], v[28:29], v[250:251] op_sel:[0,0] op_sel_hi:[1,0]
	v_pk_mul_f32 v[234:235], v[30:31], v[250:251] op_sel:[0,0] op_sel_hi:[1,0]
	v_exp_f32_e32 v228, v228
	v_exp_f32_e32 v229, v229
	v_exp_f32_e32 v230, v230
	v_exp_f32_e32 v231, v231
	v_exp_f32_e32 v232, v232
	v_exp_f32_e32 v233, v233
	v_exp_f32_e32 v234, v234
	v_exp_f32_e32 v235, v235
	v_pk_fma_f32 v[228:229], v[228:229], v[242:243], v[242:243] op_sel:[0,0,0] op_sel_hi:[1,0,0]
	v_pk_fma_f32 v[230:231], v[230:231], v[242:243], v[242:243] op_sel:[0,0,0] op_sel_hi:[1,0,0]
	v_pk_fma_f32 v[232:233], v[232:233], v[242:243], v[242:243] op_sel:[0,0,0] op_sel_hi:[1,0,0]
	v_pk_fma_f32 v[234:235], v[234:235], v[242:243], v[242:243] op_sel:[0,0,0] op_sel_hi:[1,0,0]
	v_rcp_f32_e32 v228, v228
	v_rcp_f32_e32 v229, v229
	v_rcp_f32_e32 v230, v230
	v_rcp_f32_e32 v231, v231
	v_rcp_f32_e32 v232, v232
	v_rcp_f32_e32 v233, v233
	v_rcp_f32_e32 v234, v234
	v_rcp_f32_e32 v235, v235
	v_pk_mul_f32 v[24:25], v[32:33], v[24:25]
	v_pk_mul_f32 v[26:27], v[34:35], v[26:27]
	v_pk_mul_f32 v[20:21], v[28:29], v[20:21]
	v_pk_mul_f32 v[22:23], v[30:31], v[22:23]
	v_add_u32_e32 v252, 0x16000, v252
	v_pk_mul_f32 v[32:33], v[24:25], v[228:229]
	v_pk_mul_f32 v[34:35], v[26:27], v[230:231]
	v_pk_mul_f32 v[28:29], v[20:21], v[232:233]
	v_pk_mul_f32 v[30:31], v[22:23], v[234:235]
	v_cvt_pk_bf16_f32 v32, v32, v33
	v_cvt_pk_bf16_f32 v33, v34, v35
	v_cvt_pk_bf16_f32 v34, v28, v29
	v_cvt_pk_bf16_f32 v35, v30, v31
	global_store_dwordx4 v252, v[32:35], s[4:5]
	v_pk_mul_f32 v[228:229], v[16:17], v[250:251] op_sel:[0,1] op_sel_hi:[1,1]
	v_pk_mul_f32 v[230:231], v[18:19], v[250:251] op_sel:[0,1] op_sel_hi:[1,1]
	v_pk_mul_f32 v[232:233], v[12:13], v[250:251] op_sel:[0,1] op_sel_hi:[1,1]
	v_pk_mul_f32 v[234:235], v[14:15], v[250:251] op_sel:[0,1] op_sel_hi:[1,1]
	v_exp_f32_e32 v228, v228
	v_exp_f32_e32 v229, v229
	v_exp_f32_e32 v230, v230
	v_exp_f32_e32 v231, v231
	v_exp_f32_e32 v232, v232
	v_exp_f32_e32 v233, v233
	v_exp_f32_e32 v234, v234
	v_exp_f32_e32 v235, v235
	v_pk_fma_f32 v[228:229], v[228:229], v[242:243], v[242:243] op_sel:[0,1,1] op_sel_hi:[1,1,1]
	v_pk_fma_f32 v[230:231], v[230:231], v[242:243], v[242:243] op_sel:[0,1,1] op_sel_hi:[1,1,1]
	v_pk_fma_f32 v[232:233], v[232:233], v[242:243], v[242:243] op_sel:[0,1,1] op_sel_hi:[1,1,1]
	v_pk_fma_f32 v[234:235], v[234:235], v[242:243], v[242:243] op_sel:[0,1,1] op_sel_hi:[1,1,1]
	v_rcp_f32_e32 v228, v228
	v_rcp_f32_e32 v229, v229
	v_rcp_f32_e32 v230, v230
	v_rcp_f32_e32 v231, v231
	v_rcp_f32_e32 v232, v232
	v_rcp_f32_e32 v233, v233
	v_rcp_f32_e32 v234, v234
	v_rcp_f32_e32 v235, v235
	v_pk_mul_f32 v[8:9], v[16:17], v[8:9]
	v_pk_mul_f32 v[10:11], v[18:19], v[10:11]
	v_pk_mul_f32 v[4:5], v[12:13], v[4:5]
	v_pk_mul_f32 v[6:7], v[14:15], v[6:7]
	v_add_u32_e32 v252, 0x16000, v252
	v_pk_mul_f32 v[16:17], v[8:9], v[228:229]
	v_pk_mul_f32 v[18:19], v[10:11], v[230:231]
	v_pk_mul_f32 v[12:13], v[4:5], v[232:233]
	v_pk_mul_f32 v[14:15], v[6:7], v[234:235]
	v_cvt_pk_bf16_f32 v8, v16, v17
	v_cvt_pk_bf16_f32 v9, v18, v19
	v_cvt_pk_bf16_f32 v10, v12, v13
	v_cvt_pk_bf16_f32 v11, v14, v15
	global_store_dwordx4 v252, v[8:11], s[4:5]
	s_andn2_b64 vcc, exec, s[38:39]
	s_mov_b64 s[0:1], -1
	s_cbranch_vccnz .LBB0_1473
	s_andn2_b64 vcc, exec, s[8:9]
	s_cbranch_vccnz .LBB0_1472
	s_barrier
	s_branch .LBB0_1472
